# v_Y with the 68 adjacent vmcnt / lgkmcnt(0) wait pairs of the K-loops merged into single s_waitcnt instructions
# speedup vs baseline: 1.0049x; 1.0049x over previous
.LBB0_216:
	v_add_u32_e32 v130, s88, v196
	v_add_u32_e32 v134, s89, v196
	ds_read_b128 v[158:161], v130
	ds_read_b128 v[150:153], v130 offset:1024
	ds_read_b128 v[154:157], v130 offset:2048
	ds_read_b128 v[146:149], v130 offset:3072
	ds_read_b128 v[142:145], v134
	ds_read_b128 v[130:133], v134 offset:1024
	ds_read_b128 v[138:141], v134 offset:2048
	ds_read_b128 v[134:137], v134 offset:3072
	s_add_u32 s25, s50, 0xfff80080
	s_addc_u32 s56, s51, -1
	s_and_b64 s[18:19], s[18:19], exec
	s_cselect_b32 s59, s31, s56
	s_cselect_b32 s58, s4, s25
	s_cselect_b32 s57, s5, s64
	s_cselect_b32 s56, s29, s92
	s_add_i32 m0, s39, 0xc000
	ds_read_b128 v[186:189], v198
	ds_read_b128 v[190:193], v198 offset:1024
	ds_read_b128 v[200:203], v198 offset:2048
	ds_read_b128 v[204:207], v198 offset:3072
	ds_read_b128 v[208:211], v198 offset:4096
	ds_read_b128 v[212:215], v198 offset:5120
	ds_read_b128 v[216:219], v198 offset:6144
	ds_read_b128 v[220:223], v198 offset:7168
	global_load_lds_dwordx4 v170, s[50:51]
	s_add_i32 m0, s39, 0xe000
	s_nop 0
	global_load_lds_dwordx4 v172, s[50:51]
	s_waitcnt vmcnt(8) lgkmcnt(0)
	s_barrier
	s_setprio 1
	v_mfma_i32_16x16x64_i8 v[126:129], v[158:161], v[186:189], v[126:129]
	v_mfma_i32_16x16x64_i8 v[122:125], v[154:157], v[186:189], v[122:125]
	v_mfma_i32_16x16x64_i8 v[106:109], v[154:157], v[200:203], v[106:109]
	v_mfma_i32_16x16x64_i8 v[110:113], v[158:161], v[200:203], v[110:113]
	v_mfma_i32_16x16x64_i8 v[94:97], v[158:161], v[208:211], v[94:97]
	v_mfma_i32_16x16x64_i8 v[90:93], v[154:157], v[208:211], v[90:93]
	v_mfma_i32_16x16x64_i8 v[74:77], v[154:157], v[216:219], v[74:77]
	v_mfma_i32_16x16x64_i8 v[78:81], v[158:161], v[216:219], v[78:81]
	s_nop 0
	v_mfma_i32_16x16x64_i8 v[126:129], v[150:153], v[190:193], v[126:129]
	v_mfma_i32_16x16x64_i8 v[122:125], v[146:149], v[190:193], v[122:125]
	v_mfma_i32_16x16x64_i8 v[106:109], v[146:149], v[204:207], v[106:109]
	v_mfma_i32_16x16x64_i8 v[110:113], v[150:153], v[204:207], v[110:113]
	v_mfma_i32_16x16x64_i8 v[94:97], v[150:153], v[212:215], v[94:97]
	v_mfma_i32_16x16x64_i8 v[90:93], v[146:149], v[212:215], v[90:93]
	v_mfma_i32_16x16x64_i8 v[74:77], v[146:149], v[220:223], v[74:77]
	v_mfma_i32_16x16x64_i8 v[78:81], v[150:153], v[220:223], v[78:81]
	v_mfma_i32_16x16x64_i8 v[118:121], v[142:145], v[186:189], v[118:121]
	v_mfma_i32_16x16x64_i8 v[114:117], v[138:141], v[186:189], v[114:117]
	v_mfma_i32_16x16x64_i8 v[98:101], v[138:141], v[200:203], v[98:101]
	v_mfma_i32_16x16x64_i8 v[102:105], v[142:145], v[200:203], v[102:105]
	v_mfma_i32_16x16x64_i8 v[86:89], v[142:145], v[208:211], v[86:89]
	v_mfma_i32_16x16x64_i8 v[82:85], v[138:141], v[208:211], v[82:85]
	v_mfma_i32_16x16x64_i8 v[66:69], v[138:141], v[216:219], v[66:69]
	v_mfma_i32_16x16x64_i8 v[70:73], v[142:145], v[216:219], v[70:73]
	s_nop 0
	v_mfma_i32_16x16x64_i8 v[118:121], v[130:133], v[190:193], v[118:121]
	v_mfma_i32_16x16x64_i8 v[114:117], v[134:137], v[190:193], v[114:117]
	v_mfma_i32_16x16x64_i8 v[98:101], v[134:137], v[204:207], v[98:101]
	v_mfma_i32_16x16x64_i8 v[102:105], v[130:133], v[204:207], v[102:105]
	v_mfma_i32_16x16x64_i8 v[86:89], v[130:133], v[212:215], v[86:89]
	v_mfma_i32_16x16x64_i8 v[82:85], v[134:137], v[212:215], v[82:85]
	v_mfma_i32_16x16x64_i8 v[66:69], v[134:137], v[220:223], v[66:69]
	v_mfma_i32_16x16x64_i8 v[70:73], v[130:133], v[220:223], v[70:73]
	s_setprio 0
	s_barrier
	s_add_i32 s18, s88, s7
	s_mov_b32 m0, s18
	ds_read_b128 v[200:203], v198 offset:16384
	ds_read_b128 v[204:207], v198 offset:17408
	ds_read_b128 v[208:211], v198 offset:18432
	ds_read_b128 v[212:215], v198 offset:19456
	ds_read_b128 v[216:219], v198 offset:20480
	ds_read_b128 v[220:223], v198 offset:21504
	ds_read_b128 v[224:227], v198 offset:22528
	ds_read_b128 v[228:231], v198 offset:23552
	global_load_lds_dwordx4 v164, s[56:57]
	s_add_i32 m0, s18, 0x2000
	s_add_u32 s18, s56, 0x80000
	s_addc_u32 s19, s57, 0
	s_add_i32 s25, s89, s7
	global_load_lds_dwordx4 v168, s[56:57]
	s_mov_b32 m0, s25
	s_nop 0
	global_load_lds_dwordx4 v164, s[18:19]
	s_add_i32 m0, s25, 0x2000
	s_nop 0
	global_load_lds_dwordx4 v168, s[18:19]
	s_mov_b32 m0, s39
	s_nop 0
	global_load_lds_dwordx4 v162, s[58:59]
	s_mov_b32 m0, s43
	s_nop 0
	global_load_lds_dwordx4 v166, s[58:59]
	s_waitcnt vmcnt(8) lgkmcnt(0)
	s_barrier
	s_setprio 1
	v_mfma_i32_16x16x64_i8 v[62:65], v[158:161], v[200:203], v[62:65]
	v_mfma_i32_16x16x64_i8 v[58:61], v[154:157], v[200:203], v[58:61]
	v_mfma_i32_16x16x64_i8 v[42:45], v[154:157], v[208:211], v[42:45]
	v_mfma_i32_16x16x64_i8 v[46:49], v[158:161], v[208:211], v[46:49]
	v_mfma_i32_16x16x64_i8 v[30:33], v[158:161], v[216:219], v[30:33]
	v_mfma_i32_16x16x64_i8 v[26:29], v[154:157], v[216:219], v[26:29]
	v_mfma_i32_16x16x64_i8 v[10:13], v[154:157], v[224:227], v[10:13]
	v_mfma_i32_16x16x64_i8 v[14:17], v[158:161], v[224:227], v[14:17]
	s_nop 0
	v_mfma_i32_16x16x64_i8 v[62:65], v[150:153], v[204:207], v[62:65]
	v_mfma_i32_16x16x64_i8 v[58:61], v[146:149], v[204:207], v[58:61]
	v_mfma_i32_16x16x64_i8 v[42:45], v[146:149], v[212:215], v[42:45]
	v_mfma_i32_16x16x64_i8 v[46:49], v[150:153], v[212:215], v[46:49]
	v_mfma_i32_16x16x64_i8 v[30:33], v[150:153], v[220:223], v[30:33]
	v_mfma_i32_16x16x64_i8 v[26:29], v[146:149], v[220:223], v[26:29]
	v_mfma_i32_16x16x64_i8 v[10:13], v[146:149], v[228:231], v[10:13]
	v_mfma_i32_16x16x64_i8 v[14:17], v[150:153], v[228:231], v[14:17]
	v_mfma_i32_16x16x64_i8 v[54:57], v[142:145], v[200:203], v[54:57]
	v_mfma_i32_16x16x64_i8 v[50:53], v[138:141], v[200:203], v[50:53]
	v_mfma_i32_16x16x64_i8 v[34:37], v[138:141], v[208:211], v[34:37]
	v_mfma_i32_16x16x64_i8 v[38:41], v[142:145], v[208:211], v[38:41]
	v_mfma_i32_16x16x64_i8 v[22:25], v[142:145], v[216:219], v[22:25]
	v_mfma_i32_16x16x64_i8 v[18:21], v[138:141], v[216:219], v[18:21]
	v_mfma_i32_16x16x64_i8 v[2:5], v[138:141], v[224:227], v[2:5]
	v_mfma_i32_16x16x64_i8 v[6:9], v[142:145], v[224:227], v[6:9]
	s_nop 0
	v_mfma_i32_16x16x64_i8 v[54:57], v[130:133], v[204:207], v[54:57]
	v_mfma_i32_16x16x64_i8 v[50:53], v[134:137], v[204:207], v[50:53]
	v_mfma_i32_16x16x64_i8 v[34:37], v[134:137], v[212:215], v[34:37]
	v_mfma_i32_16x16x64_i8 v[38:41], v[130:133], v[212:215], v[38:41]
	v_mfma_i32_16x16x64_i8 v[22:25], v[130:133], v[220:223], v[22:25]
	v_mfma_i32_16x16x64_i8 v[18:21], v[134:137], v[220:223], v[18:21]
	v_mfma_i32_16x16x64_i8 v[2:5], v[134:137], v[228:231], v[2:5]
	v_mfma_i32_16x16x64_i8 v[6:9], v[130:133], v[228:231], v[6:9]
	s_setprio 0
	s_barrier
	s_add_i32 s25, 0, 0x18000
	s_add_i32 vcc_lo, 0, 0x1c000
	v_add_u32_e32 v142, s25, v196
	v_add_u32_e32 v158, vcc_lo, v196
	ds_read_b128 v[130:133], v142
	ds_read_b128 v[134:137], v142 offset:1024
	ds_read_b128 v[138:141], v142 offset:2048
	ds_read_b128 v[142:145], v142 offset:3072
	ds_read_b128 v[146:149], v158
	ds_read_b128 v[150:153], v158 offset:1024
	ds_read_b128 v[154:157], v158 offset:2048
	ds_read_b128 v[158:161], v158 offset:3072
	s_add_u32 s18, s58, 0x80000
	s_addc_u32 s19, s59, 0
	s_mov_b32 m0, s61
	ds_read_b128 v[200:203], v198 offset:32768
	ds_read_b128 v[204:207], v198 offset:33792
	ds_read_b128 v[208:211], v198 offset:34816
	ds_read_b128 v[212:215], v198 offset:35840
	ds_read_b128 v[216:219], v198 offset:36864
	ds_read_b128 v[220:223], v198 offset:37888
	ds_read_b128 v[224:227], v198 offset:38912
	ds_read_b128 v[228:231], v198 offset:39936
	global_load_lds_dwordx4 v162, s[18:19]
	s_mov_b32 m0, s62
	s_nop 0
	global_load_lds_dwordx4 v166, s[18:19]
	s_waitcnt vmcnt(8) lgkmcnt(0)
	s_barrier
	s_setprio 1
	v_mfma_i32_16x16x64_i8 v[126:129], v[130:133], v[200:203], v[126:129]
	v_mfma_i32_16x16x64_i8 v[122:125], v[138:141], v[200:203], v[122:125]
	v_mfma_i32_16x16x64_i8 v[106:109], v[138:141], v[208:211], v[106:109]
	v_mfma_i32_16x16x64_i8 v[110:113], v[130:133], v[208:211], v[110:113]
	v_mfma_i32_16x16x64_i8 v[94:97], v[130:133], v[216:219], v[94:97]
	v_mfma_i32_16x16x64_i8 v[90:93], v[138:141], v[216:219], v[90:93]
	v_mfma_i32_16x16x64_i8 v[74:77], v[138:141], v[224:227], v[74:77]
	v_mfma_i32_16x16x64_i8 v[78:81], v[130:133], v[224:227], v[78:81]
	s_nop 0
	v_mfma_i32_16x16x64_i8 v[126:129], v[134:137], v[204:207], v[126:129]
	v_mfma_i32_16x16x64_i8 v[122:125], v[142:145], v[204:207], v[122:125]
	v_mfma_i32_16x16x64_i8 v[106:109], v[142:145], v[212:215], v[106:109]
	v_mfma_i32_16x16x64_i8 v[110:113], v[134:137], v[212:215], v[110:113]
	v_mfma_i32_16x16x64_i8 v[94:97], v[134:137], v[220:223], v[94:97]
	v_mfma_i32_16x16x64_i8 v[90:93], v[142:145], v[220:223], v[90:93]
	v_mfma_i32_16x16x64_i8 v[74:77], v[142:145], v[228:231], v[74:77]
	v_mfma_i32_16x16x64_i8 v[78:81], v[134:137], v[228:231], v[78:81]
	v_mfma_i32_16x16x64_i8 v[118:121], v[146:149], v[200:203], v[118:121]
	v_mfma_i32_16x16x64_i8 v[114:117], v[154:157], v[200:203], v[114:117]
	v_mfma_i32_16x16x64_i8 v[98:101], v[154:157], v[208:211], v[98:101]
	v_mfma_i32_16x16x64_i8 v[102:105], v[146:149], v[208:211], v[102:105]
	v_mfma_i32_16x16x64_i8 v[86:89], v[146:149], v[216:219], v[86:89]
	v_mfma_i32_16x16x64_i8 v[82:85], v[154:157], v[216:219], v[82:85]
	v_mfma_i32_16x16x64_i8 v[66:69], v[154:157], v[224:227], v[66:69]
	v_mfma_i32_16x16x64_i8 v[70:73], v[146:149], v[224:227], v[70:73]
	s_nop 0
	v_mfma_i32_16x16x64_i8 v[118:121], v[150:153], v[204:207], v[118:121]
	v_mfma_i32_16x16x64_i8 v[114:117], v[158:161], v[204:207], v[114:117]
	v_mfma_i32_16x16x64_i8 v[98:101], v[158:161], v[212:215], v[98:101]
	v_mfma_i32_16x16x64_i8 v[102:105], v[150:153], v[212:215], v[102:105]
	v_mfma_i32_16x16x64_i8 v[86:89], v[150:153], v[220:223], v[86:89]
	v_mfma_i32_16x16x64_i8 v[82:85], v[158:161], v[220:223], v[82:85]
	v_mfma_i32_16x16x64_i8 v[66:69], v[158:161], v[228:231], v[66:69]
	v_mfma_i32_16x16x64_i8 v[70:73], v[150:153], v[228:231], v[70:73]
	s_setprio 0
	s_barrier
	s_add_i32 s18, s25, s7
	s_mov_b32 m0, s18
	s_add_u32 s98, s56, 0x80
	s_addc_u32 s99, s57, 0
	s_add_u32 s100, s58, 0x80
	s_addc_u32 s101, s59, 0
	ds_read_b128 v[200:203], v198 offset:49152
	ds_read_b128 v[204:207], v198 offset:50176
	ds_read_b128 v[208:211], v198 offset:51200
	ds_read_b128 v[212:215], v198 offset:52224
	ds_read_b128 v[216:219], v198 offset:53248
	ds_read_b128 v[220:223], v198 offset:54272
	ds_read_b128 v[224:227], v198 offset:55296
	ds_read_b128 v[228:231], v198 offset:56320
	global_load_lds_dwordx4 v164, s[98:99]
	s_add_i32 m0, s18, 0x2000
	s_add_u32 s18, s56, 0x80080
	s_addc_u32 s19, s57, 0
	s_add_i32 s25, vcc_lo, s7
	global_load_lds_dwordx4 v168, s[98:99]
	s_mov_b32 m0, s25
	s_nop 0
	global_load_lds_dwordx4 v164, s[18:19]
	s_add_i32 m0, s25, 0x2000
	s_nop 0
	global_load_lds_dwordx4 v168, s[18:19]
	s_mov_b32 m0, s67
	s_nop 0
	global_load_lds_dwordx4 v162, s[100:101]
	s_mov_b32 m0, s68
	s_nop 0
	global_load_lds_dwordx4 v166, s[100:101]
	s_waitcnt vmcnt(8) lgkmcnt(0)
	s_barrier
	s_setprio 1
	v_mfma_i32_16x16x64_i8 v[62:65], v[130:133], v[200:203], v[62:65]
	v_mfma_i32_16x16x64_i8 v[58:61], v[138:141], v[200:203], v[58:61]
	v_mfma_i32_16x16x64_i8 v[42:45], v[138:141], v[208:211], v[42:45]
	v_mfma_i32_16x16x64_i8 v[46:49], v[130:133], v[208:211], v[46:49]
	v_mfma_i32_16x16x64_i8 v[30:33], v[130:133], v[216:219], v[30:33]
	v_mfma_i32_16x16x64_i8 v[26:29], v[138:141], v[216:219], v[26:29]
	v_mfma_i32_16x16x64_i8 v[10:13], v[138:141], v[224:227], v[10:13]
	v_mfma_i32_16x16x64_i8 v[14:17], v[130:133], v[224:227], v[14:17]
	s_nop 0
	v_mfma_i32_16x16x64_i8 v[62:65], v[134:137], v[204:207], v[62:65]
	v_mfma_i32_16x16x64_i8 v[58:61], v[142:145], v[204:207], v[58:61]
	v_mfma_i32_16x16x64_i8 v[42:45], v[142:145], v[212:215], v[42:45]
	v_mfma_i32_16x16x64_i8 v[46:49], v[134:137], v[212:215], v[46:49]
	v_mfma_i32_16x16x64_i8 v[30:33], v[134:137], v[220:223], v[30:33]
	v_mfma_i32_16x16x64_i8 v[26:29], v[142:145], v[220:223], v[26:29]
	v_mfma_i32_16x16x64_i8 v[10:13], v[142:145], v[228:231], v[10:13]
	v_mfma_i32_16x16x64_i8 v[14:17], v[134:137], v[228:231], v[14:17]
	v_mfma_i32_16x16x64_i8 v[54:57], v[146:149], v[200:203], v[54:57]
	v_mfma_i32_16x16x64_i8 v[50:53], v[154:157], v[200:203], v[50:53]
	v_mfma_i32_16x16x64_i8 v[34:37], v[154:157], v[208:211], v[34:37]
	v_mfma_i32_16x16x64_i8 v[38:41], v[146:149], v[208:211], v[38:41]
	v_mfma_i32_16x16x64_i8 v[22:25], v[146:149], v[216:219], v[22:25]
	v_mfma_i32_16x16x64_i8 v[18:21], v[154:157], v[216:219], v[18:21]
	v_mfma_i32_16x16x64_i8 v[2:5], v[154:157], v[224:227], v[2:5]
	v_mfma_i32_16x16x64_i8 v[6:9], v[146:149], v[224:227], v[6:9]
	s_nop 0
	v_mfma_i32_16x16x64_i8 v[54:57], v[150:153], v[204:207], v[54:57]
	v_mfma_i32_16x16x64_i8 v[50:53], v[158:161], v[204:207], v[50:53]
	v_mfma_i32_16x16x64_i8 v[34:37], v[158:161], v[212:215], v[34:37]
	v_mfma_i32_16x16x64_i8 v[38:41], v[150:153], v[212:215], v[38:41]
	v_mfma_i32_16x16x64_i8 v[22:25], v[150:153], v[220:223], v[22:25]
	v_mfma_i32_16x16x64_i8 v[18:21], v[158:161], v[220:223], v[18:21]
	v_mfma_i32_16x16x64_i8 v[2:5], v[158:161], v[228:231], v[2:5]
	v_mfma_i32_16x16x64_i8 v[6:9], v[150:153], v[228:231], v[6:9]
	s_setprio 0
	s_barrier
	s_add_i32 s65, s65, 2
	s_add_u32 s50, s50, 0x100
	s_addc_u32 s51, s51, 0
	s_add_u32 s92, s92, 0x100
	s_addc_u32 s64, s64, 0
	s_cmp_gt_u32 s65, 29
	s_cbranch_scc1 .LBB0_219

.LBB0_242:
	ds_read_b128 v[150:153], v146
	ds_read_b128 v[154:157], v146 offset:1024
	ds_read_b128 v[158:161], v146 offset:2048
	ds_read_b128 v[162:165], v146 offset:3072
	ds_read_b128 v[166:169], v147
	ds_read_b128 v[170:173], v147 offset:1024
	ds_read_b128 v[174:177], v147 offset:2048
	ds_read_b128 v[178:181], v147 offset:3072
	s_add_u32 s36, s34, 0xfff00080
	s_addc_u32 s37, s35, -1
	s_cmp_eq_u32 s25, 60
	s_cselect_b32 s39, s5, s37
	s_cselect_b32 s38, s18, s36
	s_cselect_b32 s37, s17, s24
	s_cselect_b32 s36, s19, s21
	v_lshl_add_u64 v[142:143], s[34:35], 0, v[138:139]
	s_add_i32 m0, s31, 0xc000
	ds_read_b128 v[182:185], v148
	ds_read_b128 v[186:189], v148 offset:1024
	ds_read_b128 v[190:193], v148 offset:2048
	ds_read_b128 v[194:197], v148 offset:3072
	ds_read_b128 v[198:201], v148 offset:4096
	ds_read_b128 v[202:205], v148 offset:5120
	ds_read_b128 v[206:209], v148 offset:6144
	ds_read_b128 v[210:213], v148 offset:7168
	global_load_lds_dwordx4 v[142:143], off
	v_lshl_add_u64 v[142:143], s[34:35], 0, v[140:141]
	s_add_i32 m0, s31, 0xe000
	s_nop 0
	global_load_lds_dwordx4 v[142:143], off
	s_waitcnt vmcnt(8) lgkmcnt(0)
	s_barrier
	s_setprio 1
	v_mfma_f32_16x16x32_bf16 v[126:129], v[150:153], v[182:185], v[126:129]
	v_mfma_f32_16x16x32_bf16 v[122:125], v[158:161], v[182:185], v[122:125]
	v_mfma_f32_16x16x32_bf16 v[114:117], v[150:153], v[190:193], v[114:117]
	v_mfma_f32_16x16x32_bf16 v[106:109], v[158:161], v[190:193], v[106:109]
	v_mfma_f32_16x16x32_bf16 v[98:101], v[150:153], v[198:201], v[98:101]
	v_mfma_f32_16x16x32_bf16 v[90:93], v[158:161], v[198:201], v[90:93]
	v_mfma_f32_16x16x32_bf16 v[78:81], v[150:153], v[206:209], v[78:81]
	v_mfma_f32_16x16x32_bf16 v[74:77], v[158:161], v[206:209], v[74:77]
	v_mfma_f32_16x16x32_bf16 v[126:129], v[154:157], v[186:189], v[126:129]
	v_mfma_f32_16x16x32_bf16 v[122:125], v[162:165], v[186:189], v[122:125]
	v_mfma_f32_16x16x32_bf16 v[114:117], v[154:157], v[194:197], v[114:117]
	v_mfma_f32_16x16x32_bf16 v[106:109], v[162:165], v[194:197], v[106:109]
	v_mfma_f32_16x16x32_bf16 v[98:101], v[154:157], v[202:205], v[98:101]
	v_mfma_f32_16x16x32_bf16 v[90:93], v[162:165], v[202:205], v[90:93]
	v_mfma_f32_16x16x32_bf16 v[78:81], v[154:157], v[210:213], v[78:81]
	v_mfma_f32_16x16x32_bf16 v[74:77], v[162:165], v[210:213], v[74:77]
	v_mfma_f32_16x16x32_bf16 v[118:121], v[166:169], v[182:185], v[118:121]
	v_mfma_f32_16x16x32_bf16 v[110:113], v[174:177], v[182:185], v[110:113]
	v_mfma_f32_16x16x32_bf16 v[102:105], v[166:169], v[190:193], v[102:105]
	v_mfma_f32_16x16x32_bf16 v[94:97], v[174:177], v[190:193], v[94:97]
	v_mfma_f32_16x16x32_bf16 v[86:89], v[166:169], v[198:201], v[86:89]
	v_mfma_f32_16x16x32_bf16 v[82:85], v[174:177], v[198:201], v[82:85]
	v_mfma_f32_16x16x32_bf16 v[70:73], v[166:169], v[206:209], v[70:73]
	v_mfma_f32_16x16x32_bf16 v[66:69], v[174:177], v[206:209], v[66:69]
	v_mfma_f32_16x16x32_bf16 v[118:121], v[170:173], v[186:189], v[118:121]
	v_mfma_f32_16x16x32_bf16 v[110:113], v[178:181], v[186:189], v[110:113]
	v_mfma_f32_16x16x32_bf16 v[102:105], v[170:173], v[194:197], v[102:105]
	v_mfma_f32_16x16x32_bf16 v[94:97], v[178:181], v[194:197], v[94:97]
	v_mfma_f32_16x16x32_bf16 v[86:89], v[170:173], v[202:205], v[86:89]
	v_mfma_f32_16x16x32_bf16 v[82:85], v[178:181], v[202:205], v[82:85]
	v_mfma_f32_16x16x32_bf16 v[70:73], v[170:173], v[210:213], v[70:73]
	v_mfma_f32_16x16x32_bf16 v[66:69], v[178:181], v[210:213], v[66:69]
	s_setprio 0
	s_barrier
	s_add_i32 s61, s59, s42
	v_lshl_add_u64 v[142:143], s[36:37], 0, v[132:133]
	s_mov_b32 m0, s61
	ds_read_b128 v[182:185], v148 offset:16384
	ds_read_b128 v[186:189], v148 offset:17408
	ds_read_b128 v[190:193], v148 offset:18432
	ds_read_b128 v[194:197], v148 offset:19456
	ds_read_b128 v[198:201], v148 offset:20480
	ds_read_b128 v[202:205], v148 offset:21504
	ds_read_b128 v[206:209], v148 offset:22528
	ds_read_b128 v[210:213], v148 offset:23552
	global_load_lds_dwordx4 v[142:143], off
	s_add_i32 m0, s61, 0x2000
	s_add_u32 s62, s36, 0x100000
	v_lshl_add_u64 v[214:215], s[36:37], 0, v[136:137]
	s_addc_u32 s63, s37, 0
	s_add_i32 s61, s60, s42
	global_load_lds_dwordx4 v[214:215], off
	v_lshl_add_u64 v[216:217], s[62:63], 0, v[132:133]
	s_mov_b32 m0, s61
	v_lshl_add_u64 v[218:219], s[38:39], 0, v[134:135]
	global_load_lds_dwordx4 v[216:217], off
	v_lshl_add_u64 v[216:217], s[62:63], 0, v[136:137]
	s_add_i32 m0, s61, 0x2000
	s_nop 0
	global_load_lds_dwordx4 v[216:217], off
	v_lshl_add_u64 v[216:217], s[38:39], 0, v[130:131]
	s_mov_b32 m0, s31
	s_nop 0
	global_load_lds_dwordx4 v[216:217], off
	s_mov_b32 m0, s49
	s_nop 0
	global_load_lds_dwordx4 v[218:219], off
	s_waitcnt vmcnt(8) lgkmcnt(0)
	s_barrier
	s_setprio 1
	v_mfma_f32_16x16x32_bf16 v[62:65], v[150:153], v[182:185], v[62:65]
	v_mfma_f32_16x16x32_bf16 v[58:61], v[158:161], v[182:185], v[58:61]
	v_mfma_f32_16x16x32_bf16 v[50:53], v[150:153], v[190:193], v[50:53]
	v_mfma_f32_16x16x32_bf16 v[42:45], v[158:161], v[190:193], v[42:45]
	v_mfma_f32_16x16x32_bf16 v[34:37], v[150:153], v[198:201], v[34:37]
	v_mfma_f32_16x16x32_bf16 v[26:29], v[158:161], v[198:201], v[26:29]
	v_mfma_f32_16x16x32_bf16 v[18:21], v[150:153], v[206:209], v[18:21]
	v_mfma_f32_16x16x32_bf16 v[10:13], v[158:161], v[206:209], v[10:13]
	v_mfma_f32_16x16x32_bf16 v[62:65], v[154:157], v[186:189], v[62:65]
	v_mfma_f32_16x16x32_bf16 v[58:61], v[162:165], v[186:189], v[58:61]
	v_mfma_f32_16x16x32_bf16 v[50:53], v[154:157], v[194:197], v[50:53]
	v_mfma_f32_16x16x32_bf16 v[42:45], v[162:165], v[194:197], v[42:45]
	v_mfma_f32_16x16x32_bf16 v[34:37], v[154:157], v[202:205], v[34:37]
	v_mfma_f32_16x16x32_bf16 v[26:29], v[162:165], v[202:205], v[26:29]
	v_mfma_f32_16x16x32_bf16 v[18:21], v[154:157], v[210:213], v[18:21]
	v_mfma_f32_16x16x32_bf16 v[10:13], v[162:165], v[210:213], v[10:13]
	v_mfma_f32_16x16x32_bf16 v[54:57], v[166:169], v[182:185], v[54:57]
	v_mfma_f32_16x16x32_bf16 v[46:49], v[174:177], v[182:185], v[46:49]
	v_mfma_f32_16x16x32_bf16 v[38:41], v[166:169], v[190:193], v[38:41]
	v_mfma_f32_16x16x32_bf16 v[30:33], v[174:177], v[190:193], v[30:33]
	v_mfma_f32_16x16x32_bf16 v[22:25], v[166:169], v[198:201], v[22:25]
	v_mfma_f32_16x16x32_bf16 v[14:17], v[174:177], v[198:201], v[14:17]
	v_mfma_f32_16x16x32_bf16 v[6:9], v[166:169], v[206:209], v[6:9]
	v_mfma_f32_16x16x32_bf16 v[2:5], v[174:177], v[206:209], v[2:5]
	v_mfma_f32_16x16x32_bf16 v[54:57], v[170:173], v[186:189], v[54:57]
	v_mfma_f32_16x16x32_bf16 v[46:49], v[178:181], v[186:189], v[46:49]
	v_mfma_f32_16x16x32_bf16 v[38:41], v[170:173], v[194:197], v[38:41]
	v_mfma_f32_16x16x32_bf16 v[30:33], v[178:181], v[194:197], v[30:33]
	v_mfma_f32_16x16x32_bf16 v[22:25], v[170:173], v[202:205], v[22:25]
	v_mfma_f32_16x16x32_bf16 v[14:17], v[178:181], v[202:205], v[14:17]
	v_mfma_f32_16x16x32_bf16 v[6:9], v[170:173], v[210:213], v[6:9]
	v_mfma_f32_16x16x32_bf16 v[2:5], v[178:181], v[210:213], v[2:5]
	s_setprio 0
	s_barrier
	s_add_i32 s61, 0, 0x18000
	v_add_u32_e32 v149, s61, v144
	s_add_i32 s62, 0, 0x1c000
	ds_read_b128 v[150:153], v149
	ds_read_b128 v[154:157], v149 offset:1024
	ds_read_b128 v[158:161], v149 offset:2048
	ds_read_b128 v[162:165], v149 offset:3072
	v_add_u32_e32 v149, s62, v144
	ds_read_b128 v[166:169], v149
	ds_read_b128 v[170:173], v149 offset:1024
	ds_read_b128 v[174:177], v149 offset:2048
	ds_read_b128 v[178:181], v149 offset:3072
	s_add_u32 s38, s38, 0x100000
	s_addc_u32 s39, s39, 0
	s_mov_b32 m0, s50
	v_lshl_add_u64 v[220:221], s[38:39], 0, v[130:131]
	ds_read_b128 v[182:185], v148 offset:32768
	ds_read_b128 v[186:189], v148 offset:33792
	ds_read_b128 v[190:193], v148 offset:34816
	ds_read_b128 v[194:197], v148 offset:35840
	ds_read_b128 v[198:201], v148 offset:36864
	ds_read_b128 v[202:205], v148 offset:37888
	ds_read_b128 v[206:209], v148 offset:38912
	ds_read_b128 v[210:213], v148 offset:39936
	global_load_lds_dwordx4 v[220:221], off
	v_lshl_add_u64 v[220:221], s[38:39], 0, v[134:135]
	s_mov_b32 m0, s51
	s_nop 0
	global_load_lds_dwordx4 v[220:221], off
	s_waitcnt vmcnt(8) lgkmcnt(0)
	s_barrier
	s_setprio 1
	v_mfma_f32_16x16x32_bf16 v[126:129], v[150:153], v[182:185], v[126:129]
	v_mfma_f32_16x16x32_bf16 v[122:125], v[158:161], v[182:185], v[122:125]
	v_mfma_f32_16x16x32_bf16 v[114:117], v[150:153], v[190:193], v[114:117]
	v_mfma_f32_16x16x32_bf16 v[106:109], v[158:161], v[190:193], v[106:109]
	v_mfma_f32_16x16x32_bf16 v[98:101], v[150:153], v[198:201], v[98:101]
	v_mfma_f32_16x16x32_bf16 v[90:93], v[158:161], v[198:201], v[90:93]
	v_mfma_f32_16x16x32_bf16 v[78:81], v[150:153], v[206:209], v[78:81]
	v_mfma_f32_16x16x32_bf16 v[74:77], v[158:161], v[206:209], v[74:77]
	v_mfma_f32_16x16x32_bf16 v[126:129], v[154:157], v[186:189], v[126:129]
	v_mfma_f32_16x16x32_bf16 v[122:125], v[162:165], v[186:189], v[122:125]
	v_mfma_f32_16x16x32_bf16 v[114:117], v[154:157], v[194:197], v[114:117]
	v_mfma_f32_16x16x32_bf16 v[106:109], v[162:165], v[194:197], v[106:109]
	v_mfma_f32_16x16x32_bf16 v[98:101], v[154:157], v[202:205], v[98:101]
	v_mfma_f32_16x16x32_bf16 v[90:93], v[162:165], v[202:205], v[90:93]
	v_mfma_f32_16x16x32_bf16 v[78:81], v[154:157], v[210:213], v[78:81]
	v_mfma_f32_16x16x32_bf16 v[74:77], v[162:165], v[210:213], v[74:77]
	v_mfma_f32_16x16x32_bf16 v[118:121], v[166:169], v[182:185], v[118:121]
	v_mfma_f32_16x16x32_bf16 v[110:113], v[174:177], v[182:185], v[110:113]
	v_mfma_f32_16x16x32_bf16 v[102:105], v[166:169], v[190:193], v[102:105]
	v_mfma_f32_16x16x32_bf16 v[94:97], v[174:177], v[190:193], v[94:97]
	v_mfma_f32_16x16x32_bf16 v[86:89], v[166:169], v[198:201], v[86:89]
	v_mfma_f32_16x16x32_bf16 v[82:85], v[174:177], v[198:201], v[82:85]
	v_mfma_f32_16x16x32_bf16 v[70:73], v[166:169], v[206:209], v[70:73]
	v_mfma_f32_16x16x32_bf16 v[66:69], v[174:177], v[206:209], v[66:69]
	v_mfma_f32_16x16x32_bf16 v[118:121], v[170:173], v[186:189], v[118:121]
	v_mfma_f32_16x16x32_bf16 v[110:113], v[178:181], v[186:189], v[110:113]
	v_mfma_f32_16x16x32_bf16 v[102:105], v[170:173], v[194:197], v[102:105]
	v_mfma_f32_16x16x32_bf16 v[94:97], v[178:181], v[194:197], v[94:97]
	v_mfma_f32_16x16x32_bf16 v[86:89], v[170:173], v[202:205], v[86:89]
	v_mfma_f32_16x16x32_bf16 v[82:85], v[178:181], v[202:205], v[82:85]
	v_mfma_f32_16x16x32_bf16 v[70:73], v[170:173], v[210:213], v[70:73]
	v_mfma_f32_16x16x32_bf16 v[66:69], v[178:181], v[210:213], v[66:69]
	s_setprio 0
	s_barrier
	s_add_i32 s38, s61, s42
	v_lshl_add_u64 v[142:143], v[142:143], 0, s[10:11]
	s_mov_b32 m0, s38
	ds_read_b128 v[182:185], v148 offset:49152
	ds_read_b128 v[186:189], v148 offset:50176
	ds_read_b128 v[190:193], v148 offset:51200
	ds_read_b128 v[194:197], v148 offset:52224
	ds_read_b128 v[198:201], v148 offset:53248
	ds_read_b128 v[202:205], v148 offset:54272
	ds_read_b128 v[206:209], v148 offset:55296
	ds_read_b128 v[210:213], v148 offset:56320
	global_load_lds_dwordx4 v[142:143], off
	s_add_i32 m0, s38, 0x2000
	s_add_u32 s36, s36, 0x100080
	v_lshl_add_u64 v[142:143], v[214:215], 0, s[10:11]
	s_addc_u32 s37, s37, 0
	s_add_i32 s38, s62, s42
	global_load_lds_dwordx4 v[142:143], off
	v_lshl_add_u64 v[142:143], s[36:37], 0, v[132:133]
	s_mov_b32 m0, s38
	s_nop 0
	global_load_lds_dwordx4 v[142:143], off
	v_lshl_add_u64 v[142:143], s[36:37], 0, v[136:137]
	s_add_i32 m0, s38, 0x2000
	s_nop 0
	global_load_lds_dwordx4 v[142:143], off
	v_lshl_add_u64 v[142:143], v[216:217], 0, s[10:11]
	s_mov_b32 m0, s57
	s_nop 0
	global_load_lds_dwordx4 v[142:143], off
	v_lshl_add_u64 v[142:143], v[218:219], 0, s[10:11]
	s_mov_b32 m0, s58
	s_nop 0
	global_load_lds_dwordx4 v[142:143], off
	s_waitcnt vmcnt(8) lgkmcnt(0)
	s_barrier
	s_setprio 1
	v_mfma_f32_16x16x32_bf16 v[62:65], v[150:153], v[182:185], v[62:65]
	v_mfma_f32_16x16x32_bf16 v[58:61], v[158:161], v[182:185], v[58:61]
	v_mfma_f32_16x16x32_bf16 v[50:53], v[150:153], v[190:193], v[50:53]
	v_mfma_f32_16x16x32_bf16 v[42:45], v[158:161], v[190:193], v[42:45]
	v_mfma_f32_16x16x32_bf16 v[34:37], v[150:153], v[198:201], v[34:37]
	v_mfma_f32_16x16x32_bf16 v[26:29], v[158:161], v[198:201], v[26:29]
	v_mfma_f32_16x16x32_bf16 v[18:21], v[150:153], v[206:209], v[18:21]
	v_mfma_f32_16x16x32_bf16 v[10:13], v[158:161], v[206:209], v[10:13]
	v_mfma_f32_16x16x32_bf16 v[62:65], v[154:157], v[186:189], v[62:65]
	v_mfma_f32_16x16x32_bf16 v[58:61], v[162:165], v[186:189], v[58:61]
	v_mfma_f32_16x16x32_bf16 v[50:53], v[154:157], v[194:197], v[50:53]
	v_mfma_f32_16x16x32_bf16 v[42:45], v[162:165], v[194:197], v[42:45]
	v_mfma_f32_16x16x32_bf16 v[34:37], v[154:157], v[202:205], v[34:37]
	v_mfma_f32_16x16x32_bf16 v[26:29], v[162:165], v[202:205], v[26:29]
	v_mfma_f32_16x16x32_bf16 v[18:21], v[154:157], v[210:213], v[18:21]
	v_mfma_f32_16x16x32_bf16 v[10:13], v[162:165], v[210:213], v[10:13]
	v_mfma_f32_16x16x32_bf16 v[54:57], v[166:169], v[182:185], v[54:57]
	v_mfma_f32_16x16x32_bf16 v[46:49], v[174:177], v[182:185], v[46:49]
	v_mfma_f32_16x16x32_bf16 v[38:41], v[166:169], v[190:193], v[38:41]
	v_mfma_f32_16x16x32_bf16 v[30:33], v[174:177], v[190:193], v[30:33]
	v_mfma_f32_16x16x32_bf16 v[22:25], v[166:169], v[198:201], v[22:25]
	v_mfma_f32_16x16x32_bf16 v[14:17], v[174:177], v[198:201], v[14:17]
	v_mfma_f32_16x16x32_bf16 v[6:9], v[166:169], v[206:209], v[6:9]
	v_mfma_f32_16x16x32_bf16 v[2:5], v[174:177], v[206:209], v[2:5]
	v_mfma_f32_16x16x32_bf16 v[54:57], v[170:173], v[186:189], v[54:57]
	v_mfma_f32_16x16x32_bf16 v[46:49], v[178:181], v[186:189], v[46:49]
	v_mfma_f32_16x16x32_bf16 v[38:41], v[170:173], v[194:197], v[38:41]
	v_mfma_f32_16x16x32_bf16 v[30:33], v[178:181], v[194:197], v[30:33]
	v_mfma_f32_16x16x32_bf16 v[22:25], v[170:173], v[202:205], v[22:25]
	v_mfma_f32_16x16x32_bf16 v[14:17], v[178:181], v[202:205], v[14:17]
	v_mfma_f32_16x16x32_bf16 v[6:9], v[170:173], v[210:213], v[6:9]
	v_mfma_f32_16x16x32_bf16 v[2:5], v[178:181], v[210:213], v[2:5]
	s_setprio 0
	s_barrier
	s_add_i32 s25, s25, 2
	s_add_u32 s34, s34, 0x100
	s_addc_u32 s35, s35, 0
	s_add_u32 s21, s21, 0x100
	s_addc_u32 s24, s24, 0
	s_cmp_gt_u32 s25, 61
	s_cbranch_scc0 .LBB0_242
	s_and_b64 vcc, exec, s[12:13]
	s_cbranch_vccz .LBB0_245
	s_barrier

.LBB0_318:
	ds_read_b128 v[26:29], v185
	ds_read_b128 v[30:33], v185 offset:1024
	ds_read_b128 v[18:21], v185 offset:2048
	ds_read_b128 v[22:25], v185 offset:3072
	ds_read_b128 v[10:13], v186
	ds_read_b128 v[14:17], v186 offset:1024
	ds_read_b128 v[2:5], v186 offset:2048
	ds_read_b128 v[6:9], v186 offset:3072
	s_add_u32 s24, s26, 0xffea8080
	s_addc_u32 s25, s27, -1
	s_cmpk_eq_i32 s58, 0x52
	s_cselect_b32 s31, s5, s25
	s_cselect_b32 s30, s4, s24
	s_cselect_b32 s29, s21, s51
	s_cselect_b32 s28, s20, s50
	v_lshl_add_u64 v[212:213], s[26:27], 0, v[166:167]
	s_add_i32 m0, s7, 0xc000
	ds_read_b128 v[174:177], v187
	ds_read_b128 v[178:181], v187 offset:1024
	ds_read_b128 v[188:191], v187 offset:2048
	ds_read_b128 v[192:195], v187 offset:3072
	ds_read_b128 v[196:199], v187 offset:4096
	ds_read_b128 v[200:203], v187 offset:5120
	ds_read_b128 v[204:207], v187 offset:6144
	ds_read_b128 v[208:211], v187 offset:7168
	global_load_lds_dwordx4 v[212:213], off
	v_lshl_add_u64 v[212:213], s[26:27], 0, v[168:169]
	s_add_i32 m0, s7, 0xe000
	s_nop 0
	global_load_lds_dwordx4 v[212:213], off
	s_waitcnt vmcnt(8) lgkmcnt(0)
	s_barrier
	s_setprio 1
	v_mfma_f32_16x16x128_f8f6f4 v[158:161], v[26:33], v[174:181], v[158:161]
	v_mfma_f32_16x16x128_f8f6f4 v[154:157], v[18:25], v[174:181], v[154:157]
	v_mfma_f32_16x16x128_f8f6f4 v[138:141], v[18:25], v[188:195], v[138:141]
	v_mfma_f32_16x16x128_f8f6f4 v[142:145], v[26:33], v[188:195], v[142:145]
	v_mfma_f32_16x16x128_f8f6f4 v[126:129], v[26:33], v[196:203], v[126:129]
	v_mfma_f32_16x16x128_f8f6f4 v[122:125], v[18:25], v[196:203], v[122:125]
	v_mfma_f32_16x16x128_f8f6f4 v[106:109], v[18:25], v[204:211], v[106:109]
	v_mfma_f32_16x16x128_f8f6f4 v[110:113], v[26:33], v[204:211], v[110:113]
	v_mfma_f32_16x16x128_f8f6f4 v[102:105], v[10:17], v[204:211], v[102:105]
	v_mfma_f32_16x16x128_f8f6f4 v[98:101], v[2:9], v[204:211], v[98:101]
	v_mfma_f32_16x16x128_f8f6f4 v[146:149], v[2:9], v[174:181], v[146:149]
	v_mfma_f32_16x16x128_f8f6f4 v[150:153], v[10:17], v[174:181], v[150:153]
	v_mfma_f32_16x16x128_f8f6f4 v[134:137], v[10:17], v[188:195], v[134:137]
	v_mfma_f32_16x16x128_f8f6f4 v[130:133], v[2:9], v[188:195], v[130:133]
	v_mfma_f32_16x16x128_f8f6f4 v[114:117], v[2:9], v[196:203], v[114:117]
	v_mfma_f32_16x16x128_f8f6f4 v[118:121], v[10:17], v[196:203], v[118:121]
	s_setprio 0
	s_barrier
	s_add_i32 s24, s42, s3
	v_lshl_add_u64 v[174:175], s[28:29], 0, v[164:165]
	s_mov_b32 m0, s24
	ds_read_b128 v[188:191], v187 offset:16384
	ds_read_b128 v[192:195], v187 offset:17408
	ds_read_b128 v[196:199], v187 offset:18432
	ds_read_b128 v[200:203], v187 offset:19456
	ds_read_b128 v[204:207], v187 offset:20480
	ds_read_b128 v[208:211], v187 offset:21504
	ds_read_b128 v[212:215], v187 offset:22528
	ds_read_b128 v[216:219], v187 offset:23552
	global_load_lds_dwordx4 v[174:175], off
	s_add_i32 m0, s24, 0x2000
	s_add_u32 s24, s28, 0x158000
	v_lshl_add_u64 v[176:177], s[28:29], 0, v[162:163]
	s_addc_u32 s25, s29, 0
	s_add_i32 s59, s43, s3
	global_load_lds_dwordx4 v[176:177], off
	v_lshl_add_u64 v[178:179], s[24:25], 0, v[164:165]
	s_mov_b32 m0, s59
	v_lshl_add_u64 v[180:181], s[30:31], 0, v[162:163]
	global_load_lds_dwordx4 v[178:179], off
	v_lshl_add_u64 v[178:179], s[24:25], 0, v[162:163]
	s_add_i32 m0, s59, 0x2000
	s_nop 0
	global_load_lds_dwordx4 v[178:179], off
	v_lshl_add_u64 v[178:179], s[30:31], 0, v[164:165]
	s_mov_b32 m0, s7
	s_nop 0
	global_load_lds_dwordx4 v[178:179], off
	s_mov_b32 m0, s17
	s_nop 0
	global_load_lds_dwordx4 v[180:181], off
	s_waitcnt vmcnt(8) lgkmcnt(0)
	s_barrier
	s_setprio 1
	v_mfma_f32_16x16x128_f8f6f4 v[78:81], v[26:33], v[196:203], v[78:81]
	v_mfma_f32_16x16x128_f8f6f4 v[74:77], v[18:25], v[196:203], v[74:77]
	v_mfma_f32_16x16x128_f8f6f4 v[90:93], v[18:25], v[188:195], v[90:93]
	v_mfma_f32_16x16x128_f8f6f4 v[94:97], v[26:33], v[188:195], v[94:97]
	v_mfma_f32_16x16x128_f8f6f4 v[62:65], v[26:33], v[204:211], v[62:65]
	v_mfma_f32_16x16x128_f8f6f4 v[58:61], v[18:25], v[204:211], v[58:61]
	v_mfma_f32_16x16x128_f8f6f4 v[42:45], v[18:25], v[212:219], v[42:45]
	v_mfma_f32_16x16x128_f8f6f4 v[46:49], v[26:33], v[212:219], v[46:49]
	v_mfma_f32_16x16x128_f8f6f4 v[38:41], v[10:17], v[212:219], v[38:41]
	v_mfma_f32_16x16x128_f8f6f4 v[34:37], v[2:9], v[212:219], v[34:37]
	v_mfma_f32_16x16x128_f8f6f4 v[82:85], v[2:9], v[188:195], v[82:85]
	v_mfma_f32_16x16x128_f8f6f4 v[86:89], v[10:17], v[188:195], v[86:89]
	v_mfma_f32_16x16x128_f8f6f4 v[70:73], v[10:17], v[196:203], v[70:73]
	v_mfma_f32_16x16x128_f8f6f4 v[66:69], v[2:9], v[196:203], v[66:69]
	v_mfma_f32_16x16x128_f8f6f4 v[50:53], v[2:9], v[204:211], v[50:53]
	v_mfma_f32_16x16x128_f8f6f4 v[54:57], v[10:17], v[204:211], v[54:57]
	s_setprio 0
	s_barrier
	s_add_i32 s59, 0, 0x18000
	s_add_i32 s60, 0, 0x1c000
	v_add_u32_e32 v14, s59, v183
	v_add_u32_e32 v30, s60, v183
	ds_read_b128 v[2:5], v14
	ds_read_b128 v[6:9], v14 offset:1024
	ds_read_b128 v[10:13], v14 offset:2048
	ds_read_b128 v[14:17], v14 offset:3072
	ds_read_b128 v[18:21], v30
	ds_read_b128 v[22:25], v30 offset:1024
	ds_read_b128 v[26:29], v30 offset:2048
	ds_read_b128 v[30:33], v30 offset:3072
	s_add_u32 s24, s30, 0x158000
	s_addc_u32 s25, s31, 0
	s_mov_b32 m0, s34
	v_lshl_add_u64 v[220:221], s[24:25], 0, v[164:165]
	ds_read_b128 v[188:191], v187 offset:32768
	ds_read_b128 v[192:195], v187 offset:33792
	ds_read_b128 v[196:199], v187 offset:34816
	ds_read_b128 v[200:203], v187 offset:35840
	ds_read_b128 v[204:207], v187 offset:36864
	ds_read_b128 v[208:211], v187 offset:37888
	ds_read_b128 v[212:215], v187 offset:38912
	ds_read_b128 v[216:219], v187 offset:39936
	global_load_lds_dwordx4 v[220:221], off
	v_lshl_add_u64 v[220:221], s[24:25], 0, v[162:163]
	s_mov_b32 m0, s35
	s_nop 0
	global_load_lds_dwordx4 v[220:221], off
	s_waitcnt vmcnt(8) lgkmcnt(0)
	s_barrier
	s_setprio 1
	v_mfma_f32_16x16x128_f8f6f4 v[122:125], v[10:17], v[204:211], v[122:125]
	v_mfma_f32_16x16x128_f8f6f4 v[126:129], v[2:9], v[204:211], v[126:129]
	v_mfma_f32_16x16x128_f8f6f4 v[158:161], v[2:9], v[188:195], v[158:161]
	v_mfma_f32_16x16x128_f8f6f4 v[154:157], v[10:17], v[188:195], v[154:157]
	v_mfma_f32_16x16x128_f8f6f4 v[138:141], v[10:17], v[196:203], v[138:141]
	v_mfma_f32_16x16x128_f8f6f4 v[142:145], v[2:9], v[196:203], v[142:145]
	v_mfma_f32_16x16x128_f8f6f4 v[110:113], v[2:9], v[212:219], v[110:113]
	v_mfma_f32_16x16x128_f8f6f4 v[106:109], v[10:17], v[212:219], v[106:109]
	v_mfma_f32_16x16x128_f8f6f4 v[102:105], v[18:25], v[212:219], v[102:105]
	v_mfma_f32_16x16x128_f8f6f4 v[98:101], v[26:33], v[212:219], v[98:101]
	v_mfma_f32_16x16x128_f8f6f4 v[146:149], v[26:33], v[188:195], v[146:149]
	v_mfma_f32_16x16x128_f8f6f4 v[150:153], v[18:25], v[188:195], v[150:153]
	v_mfma_f32_16x16x128_f8f6f4 v[134:137], v[18:25], v[196:203], v[134:137]
	v_mfma_f32_16x16x128_f8f6f4 v[130:133], v[26:33], v[196:203], v[130:133]
	v_mfma_f32_16x16x128_f8f6f4 v[114:117], v[26:33], v[204:211], v[114:117]
	v_mfma_f32_16x16x128_f8f6f4 v[118:121], v[18:25], v[204:211], v[118:121]
	s_setprio 0
	s_barrier
	s_add_i32 s24, s59, s3
	v_lshl_add_u64 v[174:175], v[174:175], 0, s[12:13]
	s_mov_b32 m0, s24
	ds_read_b128 v[188:191], v187 offset:49152
	ds_read_b128 v[192:195], v187 offset:50176
	ds_read_b128 v[196:199], v187 offset:51200
	ds_read_b128 v[200:203], v187 offset:52224
	ds_read_b128 v[204:207], v187 offset:53248
	ds_read_b128 v[208:211], v187 offset:54272
	ds_read_b128 v[212:215], v187 offset:55296
	ds_read_b128 v[216:219], v187 offset:56320
	global_load_lds_dwordx4 v[174:175], off
	s_add_i32 m0, s24, 0x2000
	s_add_u32 s24, s28, 0x158080
	v_lshl_add_u64 v[174:175], v[176:177], 0, s[12:13]
	s_addc_u32 s25, s29, 0
	s_add_i32 s28, s60, s3
	global_load_lds_dwordx4 v[174:175], off
	v_lshl_add_u64 v[174:175], s[24:25], 0, v[164:165]
	s_mov_b32 m0, s28
	s_nop 0
	global_load_lds_dwordx4 v[174:175], off
	v_lshl_add_u64 v[174:175], s[24:25], 0, v[162:163]
	s_add_i32 m0, s28, 0x2000
	s_nop 0
	global_load_lds_dwordx4 v[174:175], off
	v_lshl_add_u64 v[174:175], v[178:179], 0, s[12:13]
	s_mov_b32 m0, s38
	s_nop 0
	global_load_lds_dwordx4 v[174:175], off
	v_lshl_add_u64 v[174:175], v[180:181], 0, s[12:13]
	s_mov_b32 m0, s39
	s_nop 0
	global_load_lds_dwordx4 v[174:175], off
	s_waitcnt vmcnt(8) lgkmcnt(0)
	s_barrier
	s_setprio 1
	v_mfma_f32_16x16x128_f8f6f4 v[62:65], v[2:9], v[204:211], v[62:65]
	v_mfma_f32_16x16x128_f8f6f4 v[58:61], v[10:17], v[204:211], v[58:61]
	v_mfma_f32_16x16x128_f8f6f4 v[90:93], v[10:17], v[188:195], v[90:93]
	v_mfma_f32_16x16x128_f8f6f4 v[94:97], v[2:9], v[188:195], v[94:97]
	v_mfma_f32_16x16x128_f8f6f4 v[78:81], v[2:9], v[196:203], v[78:81]
	v_mfma_f32_16x16x128_f8f6f4 v[74:77], v[10:17], v[196:203], v[74:77]
	v_mfma_f32_16x16x128_f8f6f4 v[42:45], v[10:17], v[212:219], v[42:45]
	v_mfma_f32_16x16x128_f8f6f4 v[46:49], v[2:9], v[212:219], v[46:49]
	v_mfma_f32_16x16x128_f8f6f4 v[38:41], v[18:25], v[212:219], v[38:41]
	v_mfma_f32_16x16x128_f8f6f4 v[34:37], v[26:33], v[212:219], v[34:37]
	v_mfma_f32_16x16x128_f8f6f4 v[82:85], v[26:33], v[188:195], v[82:85]
	v_mfma_f32_16x16x128_f8f6f4 v[86:89], v[18:25], v[188:195], v[86:89]
	v_mfma_f32_16x16x128_f8f6f4 v[70:73], v[18:25], v[196:203], v[70:73]
	v_mfma_f32_16x16x128_f8f6f4 v[66:69], v[26:33], v[196:203], v[66:69]
	v_mfma_f32_16x16x128_f8f6f4 v[50:53], v[26:33], v[204:211], v[50:53]
	v_mfma_f32_16x16x128_f8f6f4 v[54:57], v[18:25], v[204:211], v[54:57]
	s_setprio 0
	s_barrier
	s_add_i32 s58, s58, 2
	s_add_u32 s26, s26, 0x100
	s_addc_u32 s27, s27, 0
	s_add_u32 s50, s50, 0x100
	s_addc_u32 s51, s51, 0
	s_cmpk_gt_u32 s58, 0x53
	s_cbranch_scc0 .LBB0_318
	s_and_b64 vcc, exec, s[14:15]
	s_cbranch_vccz .LBB0_321
	s_barrier

.LBB0_332:
	s_add_u32 s6, s61, s4
	s_addc_u32 s7, s62, s5
	s_add_u32 s6, s6, 0x32800100
	s_addc_u32 s7, s7, 0
	s_add_u32 s24, s63, s4
	s_addc_u32 s25, s68, s5
	s_add_i32 s64, 0, 0x10000
	s_cmpk_eq_i32 s4, 0x2a00
	s_cselect_b32 s13, s1, s7
	s_cselect_b32 s12, s0, s6
	s_cselect_b32 s7, s29, s25
	s_cselect_b32 s6, s28, s24
	s_add_i32 s65, 0, 0x14000
	v_add_u32_e32 v2, s64, v188
	v_add_u32_e32 v6, s65, v188
	ds_read_b128 v[26:29], v2
	ds_read_b128 v[30:33], v2 offset:1024
	ds_read_b128 v[18:21], v2 offset:2048
	ds_read_b128 v[22:25], v2 offset:3072
	ds_read_b128 v[10:13], v6
	ds_read_b128 v[14:17], v6 offset:1024
	ds_read_b128 v[2:5], v6 offset:2048
	ds_read_b128 v[6:9], v6 offset:3072
	v_lshl_add_u64 v[214:215], v[168:169], 0, s[4:5]
	s_add_i32 m0, s18, 0xc000
	ds_read_b128 v[172:175], v189
	ds_read_b128 v[176:179], v189 offset:1024
	ds_read_b128 v[190:193], v189 offset:2048
	ds_read_b128 v[194:197], v189 offset:3072
	ds_read_b128 v[198:201], v189 offset:4096
	ds_read_b128 v[202:205], v189 offset:5120
	ds_read_b128 v[206:209], v189 offset:6144
	ds_read_b128 v[210:213], v189 offset:7168
	global_load_lds_dwordx4 v[214:215], off
	v_lshl_add_u64 v[214:215], v[170:171], 0, s[4:5]
	s_add_i32 m0, s18, 0xe000
	s_nop 0
	global_load_lds_dwordx4 v[214:215], off
	s_waitcnt vmcnt(8) lgkmcnt(0)
	s_barrier
	s_setprio 1
	v_mfma_f32_16x16x128_f8f6f4 v[70:73], v[26:33], v[172:179], v[70:73]
	v_mfma_f32_16x16x128_f8f6f4 v[66:69], v[18:25], v[172:179], v[66:69]
	v_mfma_f32_16x16x128_f8f6f4 v[74:77], v[18:25], v[190:197], v[74:77]
	v_mfma_f32_16x16x128_f8f6f4 v[78:81], v[26:33], v[190:197], v[78:81]
	v_mfma_f32_16x16x128_f8f6f4 v[86:89], v[26:33], v[198:205], v[86:89]
	v_mfma_f32_16x16x128_f8f6f4 v[82:85], v[18:25], v[198:205], v[82:85]
	v_mfma_f32_16x16x128_f8f6f4 v[90:93], v[18:25], v[206:213], v[90:93]
	v_mfma_f32_16x16x128_f8f6f4 v[94:97], v[26:33], v[206:213], v[94:97]
	v_mfma_f32_16x16x128_f8f6f4 v[134:137], v[10:17], v[206:213], v[134:137]
	v_mfma_f32_16x16x128_f8f6f4 v[130:133], v[2:9], v[206:213], v[130:133]
	v_mfma_f32_16x16x128_f8f6f4 v[154:157], v[2:9], v[172:179], v[154:157]
	v_mfma_f32_16x16x128_f8f6f4 v[158:161], v[10:17], v[172:179], v[158:161]
	v_mfma_f32_16x16x128_f8f6f4 v[150:153], v[10:17], v[190:197], v[150:153]
	v_mfma_f32_16x16x128_f8f6f4 v[146:149], v[2:9], v[190:197], v[146:149]
	v_mfma_f32_16x16x128_f8f6f4 v[138:141], v[2:9], v[198:205], v[138:141]
	v_mfma_f32_16x16x128_f8f6f4 v[142:145], v[10:17], v[198:205], v[142:145]
	s_setprio 0
	s_barrier
	s_add_i32 s24, s64, s17
	v_lshl_add_u64 v[172:173], s[6:7], 0, v[162:163]
	s_mov_b32 m0, s24
	ds_read_b128 v[190:193], v189 offset:16384
	ds_read_b128 v[194:197], v189 offset:17408
	ds_read_b128 v[198:201], v189 offset:18432
	ds_read_b128 v[202:205], v189 offset:19456
	ds_read_b128 v[206:209], v189 offset:20480
	ds_read_b128 v[210:213], v189 offset:21504
	ds_read_b128 v[214:217], v189 offset:22528
	ds_read_b128 v[218:221], v189 offset:23552
	global_load_lds_dwordx4 v[172:173], off
	s_add_i32 m0, s24, 0x2000
	s_add_u32 s24, s6, 0x158000
	v_lshl_add_u64 v[174:175], s[6:7], 0, v[166:167]
	s_addc_u32 s25, s7, 0
	s_add_i32 s64, s65, s17
	global_load_lds_dwordx4 v[174:175], off
	v_lshl_add_u64 v[176:177], s[24:25], 0, v[162:163]
	s_mov_b32 m0, s64
	v_lshl_add_u64 v[178:179], s[12:13], 0, v[166:167]
	global_load_lds_dwordx4 v[176:177], off
	v_lshl_add_u64 v[176:177], s[24:25], 0, v[166:167]
	s_add_i32 m0, s64, 0x2000
	s_nop 0
	global_load_lds_dwordx4 v[176:177], off
	v_lshl_add_u64 v[176:177], s[12:13], 0, v[162:163]
	s_mov_b32 m0, s18
	s_nop 0
	global_load_lds_dwordx4 v[176:177], off
	s_mov_b32 m0, s19
	s_nop 0
	global_load_lds_dwordx4 v[178:179], off
	s_waitcnt vmcnt(8) lgkmcnt(0)
	s_barrier
	s_setprio 1
	v_mfma_f32_16x16x128_f8f6f4 v[110:113], v[26:33], v[198:205], v[110:113]
	v_mfma_f32_16x16x128_f8f6f4 v[106:109], v[18:25], v[198:205], v[106:109]
	v_mfma_f32_16x16x128_f8f6f4 v[98:101], v[18:25], v[190:197], v[98:101]
	v_mfma_f32_16x16x128_f8f6f4 v[102:105], v[26:33], v[190:197], v[102:105]
	v_mfma_f32_16x16x128_f8f6f4 v[118:121], v[26:33], v[206:213], v[118:121]
	v_mfma_f32_16x16x128_f8f6f4 v[114:117], v[18:25], v[206:213], v[114:117]
	v_mfma_f32_16x16x128_f8f6f4 v[122:125], v[18:25], v[214:221], v[122:125]
	v_mfma_f32_16x16x128_f8f6f4 v[126:129], v[26:33], v[214:221], v[126:129]
	v_mfma_f32_16x16x128_f8f6f4 v[62:65], v[10:17], v[214:221], v[62:65]
	v_mfma_f32_16x16x128_f8f6f4 v[58:61], v[2:9], v[214:221], v[58:61]
	v_mfma_f32_16x16x128_f8f6f4 v[34:37], v[2:9], v[190:197], v[34:37]
	v_mfma_f32_16x16x128_f8f6f4 v[38:41], v[10:17], v[190:197], v[38:41]
	v_mfma_f32_16x16x128_f8f6f4 v[46:49], v[10:17], v[198:205], v[46:49]
	v_mfma_f32_16x16x128_f8f6f4 v[42:45], v[2:9], v[198:205], v[42:45]
	v_mfma_f32_16x16x128_f8f6f4 v[50:53], v[2:9], v[206:213], v[50:53]
	v_mfma_f32_16x16x128_f8f6f4 v[54:57], v[10:17], v[206:213], v[54:57]
	s_setprio 0
	s_barrier
	s_add_i32 s24, 0, 0x18000
	s_add_i32 s25, 0, 0x1c000
	v_add_u32_e32 v14, s24, v188
	v_add_u32_e32 v30, s25, v188
	ds_read_b128 v[2:5], v14
	ds_read_b128 v[6:9], v14 offset:1024
	ds_read_b128 v[10:13], v14 offset:2048
	ds_read_b128 v[14:17], v14 offset:3072
	ds_read_b128 v[18:21], v30
	ds_read_b128 v[22:25], v30 offset:1024
	ds_read_b128 v[26:29], v30 offset:2048
	ds_read_b128 v[30:33], v30 offset:3072
	s_add_u32 s12, s12, 0x158000
	s_addc_u32 s13, s13, 0
	s_mov_b32 m0, s93
	v_lshl_add_u64 v[222:223], s[12:13], 0, v[162:163]
	ds_read_b128 v[190:193], v189 offset:32768
	ds_read_b128 v[194:197], v189 offset:33792
	ds_read_b128 v[198:201], v189 offset:34816
	ds_read_b128 v[202:205], v189 offset:35840
	ds_read_b128 v[206:209], v189 offset:36864
	ds_read_b128 v[210:213], v189 offset:37888
	ds_read_b128 v[214:217], v189 offset:38912
	ds_read_b128 v[218:221], v189 offset:39936
	global_load_lds_dwordx4 v[222:223], off
	v_lshl_add_u64 v[222:223], s[12:13], 0, v[166:167]
	s_mov_b32 m0, s94
	s_nop 0
	global_load_lds_dwordx4 v[222:223], off
	s_waitcnt vmcnt(8) lgkmcnt(0)
	s_barrier
	s_setprio 1
	v_mfma_f32_16x16x128_f8f6f4 v[82:85], v[10:17], v[206:213], v[82:85]
	v_mfma_f32_16x16x128_f8f6f4 v[86:89], v[2:9], v[206:213], v[86:89]
	v_mfma_f32_16x16x128_f8f6f4 v[70:73], v[2:9], v[190:197], v[70:73]
	v_mfma_f32_16x16x128_f8f6f4 v[66:69], v[10:17], v[190:197], v[66:69]
	v_mfma_f32_16x16x128_f8f6f4 v[74:77], v[10:17], v[198:205], v[74:77]
	v_mfma_f32_16x16x128_f8f6f4 v[78:81], v[2:9], v[198:205], v[78:81]
	v_mfma_f32_16x16x128_f8f6f4 v[94:97], v[2:9], v[214:221], v[94:97]
	v_mfma_f32_16x16x128_f8f6f4 v[90:93], v[10:17], v[214:221], v[90:93]
	v_mfma_f32_16x16x128_f8f6f4 v[134:137], v[18:25], v[214:221], v[134:137]
	v_mfma_f32_16x16x128_f8f6f4 v[130:133], v[26:33], v[214:221], v[130:133]
	v_mfma_f32_16x16x128_f8f6f4 v[154:157], v[26:33], v[190:197], v[154:157]
	v_mfma_f32_16x16x128_f8f6f4 v[158:161], v[18:25], v[190:197], v[158:161]
	v_mfma_f32_16x16x128_f8f6f4 v[150:153], v[18:25], v[198:205], v[150:153]
	v_mfma_f32_16x16x128_f8f6f4 v[146:149], v[26:33], v[198:205], v[146:149]
	v_mfma_f32_16x16x128_f8f6f4 v[138:141], v[26:33], v[206:213], v[138:141]
	v_mfma_f32_16x16x128_f8f6f4 v[142:145], v[18:25], v[206:213], v[142:145]
	s_setprio 0
	s_barrier
	s_add_i32 s12, s24, s17
	v_lshl_add_u64 v[172:173], v[172:173], 0, s[76:77]
	s_mov_b32 m0, s12
	ds_read_b128 v[190:193], v189 offset:49152
	ds_read_b128 v[194:197], v189 offset:50176
	ds_read_b128 v[198:201], v189 offset:51200
	ds_read_b128 v[202:205], v189 offset:52224
	ds_read_b128 v[206:209], v189 offset:53248
	ds_read_b128 v[210:213], v189 offset:54272
	ds_read_b128 v[214:217], v189 offset:55296
	ds_read_b128 v[218:221], v189 offset:56320
	global_load_lds_dwordx4 v[172:173], off
	s_add_i32 m0, s12, 0x2000
	s_add_u32 s6, s6, 0x158080
	v_lshl_add_u64 v[172:173], v[174:175], 0, s[76:77]
	s_addc_u32 s7, s7, 0
	s_add_i32 s12, s25, s17
	global_load_lds_dwordx4 v[172:173], off
	v_lshl_add_u64 v[172:173], s[6:7], 0, v[162:163]
	s_mov_b32 m0, s12
	s_nop 0
	global_load_lds_dwordx4 v[172:173], off
	v_lshl_add_u64 v[172:173], s[6:7], 0, v[166:167]
	s_add_i32 m0, s12, 0x2000
	s_nop 0
	global_load_lds_dwordx4 v[172:173], off
	v_lshl_add_u64 v[172:173], v[176:177], 0, s[76:77]
	s_mov_b32 m0, s95
	s_nop 0
	global_load_lds_dwordx4 v[172:173], off
	v_lshl_add_u64 v[172:173], v[178:179], 0, s[76:77]
	s_mov_b32 m0, vcc_lo
	s_nop 0
	global_load_lds_dwordx4 v[172:173], off
	s_waitcnt vmcnt(8) lgkmcnt(0)
	s_barrier
	s_setprio 1
	v_mfma_f32_16x16x128_f8f6f4 v[118:121], v[2:9], v[206:213], v[118:121]
	v_mfma_f32_16x16x128_f8f6f4 v[114:117], v[10:17], v[206:213], v[114:117]
	v_mfma_f32_16x16x128_f8f6f4 v[98:101], v[10:17], v[190:197], v[98:101]
	v_mfma_f32_16x16x128_f8f6f4 v[102:105], v[2:9], v[190:197], v[102:105]
	v_mfma_f32_16x16x128_f8f6f4 v[110:113], v[2:9], v[198:205], v[110:113]
	v_mfma_f32_16x16x128_f8f6f4 v[106:109], v[10:17], v[198:205], v[106:109]
	v_mfma_f32_16x16x128_f8f6f4 v[122:125], v[10:17], v[214:221], v[122:125]
	v_mfma_f32_16x16x128_f8f6f4 v[126:129], v[2:9], v[214:221], v[126:129]
	v_mfma_f32_16x16x128_f8f6f4 v[62:65], v[18:25], v[214:221], v[62:65]
	v_mfma_f32_16x16x128_f8f6f4 v[58:61], v[26:33], v[214:221], v[58:61]
	v_mfma_f32_16x16x128_f8f6f4 v[34:37], v[26:33], v[190:197], v[34:37]
	v_mfma_f32_16x16x128_f8f6f4 v[38:41], v[18:25], v[190:197], v[38:41]
	v_mfma_f32_16x16x128_f8f6f4 v[46:49], v[18:25], v[198:205], v[46:49]
	v_mfma_f32_16x16x128_f8f6f4 v[42:45], v[26:33], v[198:205], v[42:45]
	v_mfma_f32_16x16x128_f8f6f4 v[50:53], v[26:33], v[206:213], v[50:53]
	v_mfma_f32_16x16x128_f8f6f4 v[54:57], v[18:25], v[206:213], v[54:57]
	s_setprio 0
	s_barrier
	s_add_i32 vcc_hi, vcc_hi, 2
	s_add_u32 s4, s4, 0x100
	s_addc_u32 s5, s5, 0
	s_cmpk_lt_u32 vcc_hi, 0x54
	s_cbranch_scc1 .LBB0_332
	s_waitcnt vmcnt(0)
	s_mov_b64 s[12:13], s[54:55]
	s_cmpk_gt_u32 s89, 0xff
	s_cbranch_scc1 .LBB0_335
	s_barrier

.LBB0_758:
	ds_read_b128 v[148:151], v146
	ds_read_b128 v[152:155], v146 offset:1024
	ds_read_b128 v[156:159], v146 offset:2048
	ds_read_b128 v[160:163], v146 offset:3072
	ds_read_b128 v[164:167], v147
	ds_read_b128 v[168:171], v147 offset:1024
	ds_read_b128 v[172:175], v147 offset:2048
	ds_read_b128 v[176:179], v147 offset:3072
	s_add_u32 s16, s42, s14
	s_addc_u32 s17, s43, s15
	s_add_u32 s16, s16, 0x2a800100
	s_addc_u32 s17, s17, 0
	s_add_u32 s60, s48, s14
	s_addc_u32 s61, s49, s15
	s_cmpk_eq_i32 s14, 0x700
	s_cselect_b32 s21, s13, s17
	s_cselect_b32 s20, s12, s16
	s_cselect_b32 s17, s11, s61
	s_cselect_b32 s16, s10, s60
	s_mov_b32 m0, s51
	v_lshl_add_u64 v[212:213], v[138:139], 0, s[14:15]
	ds_read_b128 v[180:183], v145
	ds_read_b128 v[184:187], v145 offset:1024
	ds_read_b128 v[188:191], v145 offset:2048
	ds_read_b128 v[192:195], v145 offset:3072
	ds_read_b128 v[196:199], v145 offset:4096
	ds_read_b128 v[200:203], v145 offset:5120
	ds_read_b128 v[204:207], v145 offset:6144
	ds_read_b128 v[208:211], v145 offset:7168
	global_load_lds_dwordx4 v[212:213], off
	v_lshl_add_u64 v[212:213], v[140:141], 0, s[14:15]
	s_mov_b32 m0, s58
	s_nop 0
	global_load_lds_dwordx4 v[212:213], off
	s_waitcnt vmcnt(8) lgkmcnt(0)
	s_barrier
	s_setprio 1
	v_mfma_f32_16x16x32_bf16 v[126:129], v[148:151], v[180:183], v[126:129]
	v_mfma_f32_16x16x32_bf16 v[122:125], v[156:159], v[180:183], v[122:125]
	v_mfma_f32_16x16x32_bf16 v[118:121], v[148:151], v[188:191], v[118:121]
	v_mfma_f32_16x16x32_bf16 v[114:117], v[156:159], v[188:191], v[114:117]
	v_mfma_f32_16x16x32_bf16 v[106:109], v[148:151], v[196:199], v[106:109]
	v_mfma_f32_16x16x32_bf16 v[98:101], v[156:159], v[196:199], v[98:101]
	v_mfma_f32_16x16x32_bf16 v[90:93], v[148:151], v[204:207], v[90:93]
	v_mfma_f32_16x16x32_bf16 v[82:85], v[156:159], v[204:207], v[82:85]
	v_mfma_f32_16x16x32_bf16 v[126:129], v[152:155], v[184:187], v[126:129]
	v_mfma_f32_16x16x32_bf16 v[122:125], v[160:163], v[184:187], v[122:125]
	v_mfma_f32_16x16x32_bf16 v[118:121], v[152:155], v[192:195], v[118:121]
	v_mfma_f32_16x16x32_bf16 v[114:117], v[160:163], v[192:195], v[114:117]
	v_mfma_f32_16x16x32_bf16 v[106:109], v[152:155], v[200:203], v[106:109]
	v_mfma_f32_16x16x32_bf16 v[98:101], v[160:163], v[200:203], v[98:101]
	v_mfma_f32_16x16x32_bf16 v[90:93], v[152:155], v[208:211], v[90:93]
	v_mfma_f32_16x16x32_bf16 v[82:85], v[160:163], v[208:211], v[82:85]
	v_mfma_f32_16x16x32_bf16 v[110:113], v[164:167], v[180:183], v[110:113]
	v_mfma_f32_16x16x32_bf16 v[102:105], v[172:175], v[180:183], v[102:105]
	v_mfma_f32_16x16x32_bf16 v[94:97], v[164:167], v[188:191], v[94:97]
	v_mfma_f32_16x16x32_bf16 v[86:89], v[172:175], v[188:191], v[86:89]
	v_mfma_f32_16x16x32_bf16 v[78:81], v[164:167], v[196:199], v[78:81]
	v_mfma_f32_16x16x32_bf16 v[74:77], v[172:175], v[196:199], v[74:77]
	v_mfma_f32_16x16x32_bf16 v[70:73], v[164:167], v[204:207], v[70:73]
	v_mfma_f32_16x16x32_bf16 v[66:69], v[172:175], v[204:207], v[66:69]
	v_mfma_f32_16x16x32_bf16 v[110:113], v[168:171], v[184:187], v[110:113]
	v_mfma_f32_16x16x32_bf16 v[102:105], v[176:179], v[184:187], v[102:105]
	v_mfma_f32_16x16x32_bf16 v[94:97], v[168:171], v[192:195], v[94:97]
	v_mfma_f32_16x16x32_bf16 v[86:89], v[176:179], v[192:195], v[86:89]
	v_mfma_f32_16x16x32_bf16 v[78:81], v[168:171], v[200:203], v[78:81]
	v_mfma_f32_16x16x32_bf16 v[74:77], v[176:179], v[200:203], v[74:77]
	v_mfma_f32_16x16x32_bf16 v[70:73], v[168:171], v[208:211], v[70:73]
	v_mfma_f32_16x16x32_bf16 v[66:69], v[176:179], v[208:211], v[66:69]
	s_setprio 0
	s_barrier
	s_mov_b32 m0, s59
	v_lshl_add_u64 v[212:213], s[16:17], 0, v[130:131]
	ds_read_b128 v[180:183], v145 offset:16384
	ds_read_b128 v[184:187], v145 offset:17408
	ds_read_b128 v[188:191], v145 offset:18432
	ds_read_b128 v[192:195], v145 offset:19456
	ds_read_b128 v[196:199], v145 offset:20480
	ds_read_b128 v[200:203], v145 offset:21504
	ds_read_b128 v[204:207], v145 offset:22528
	ds_read_b128 v[208:211], v145 offset:23552
	global_load_lds_dwordx4 v[212:213], off
	s_add_i32 m0, s59, 0x2000
	s_add_u32 s60, s16, 0x100000
	v_lshl_add_u64 v[214:215], s[16:17], 0, v[136:137]
	s_addc_u32 s61, s17, 0
	s_add_i32 s62, s26, s31
	global_load_lds_dwordx4 v[214:215], off
	v_lshl_add_u64 v[216:217], s[60:61], 0, v[130:131]
	s_mov_b32 m0, s62
	v_lshl_add_u64 v[218:219], s[20:21], 0, v[134:135]
	global_load_lds_dwordx4 v[216:217], off
	v_lshl_add_u64 v[216:217], s[60:61], 0, v[136:137]
	s_add_i32 m0, s62, 0x2000
	s_nop 0
	global_load_lds_dwordx4 v[216:217], off
	v_lshl_add_u64 v[216:217], s[20:21], 0, v[132:133]
	s_mov_b32 m0, s7
	s_nop 0
	global_load_lds_dwordx4 v[216:217], off
	s_mov_b32 m0, s34
	s_nop 0
	global_load_lds_dwordx4 v[218:219], off
	s_waitcnt vmcnt(8) lgkmcnt(0)
	s_barrier
	s_setprio 1
	v_mfma_f32_16x16x32_bf16 v[62:65], v[148:151], v[180:183], v[62:65]
	v_mfma_f32_16x16x32_bf16 v[58:61], v[156:159], v[180:183], v[58:61]
	v_mfma_f32_16x16x32_bf16 v[54:57], v[148:151], v[188:191], v[54:57]
	v_mfma_f32_16x16x32_bf16 v[50:53], v[156:159], v[188:191], v[50:53]
	v_mfma_f32_16x16x32_bf16 v[42:45], v[148:151], v[196:199], v[42:45]
	v_mfma_f32_16x16x32_bf16 v[34:37], v[156:159], v[196:199], v[34:37]
	v_mfma_f32_16x16x32_bf16 v[26:29], v[148:151], v[204:207], v[26:29]
	v_mfma_f32_16x16x32_bf16 v[18:21], v[156:159], v[204:207], v[18:21]
	v_mfma_f32_16x16x32_bf16 v[62:65], v[152:155], v[184:187], v[62:65]
	v_mfma_f32_16x16x32_bf16 v[58:61], v[160:163], v[184:187], v[58:61]
	v_mfma_f32_16x16x32_bf16 v[54:57], v[152:155], v[192:195], v[54:57]
	v_mfma_f32_16x16x32_bf16 v[50:53], v[160:163], v[192:195], v[50:53]
	v_mfma_f32_16x16x32_bf16 v[42:45], v[152:155], v[200:203], v[42:45]
	v_mfma_f32_16x16x32_bf16 v[34:37], v[160:163], v[200:203], v[34:37]
	v_mfma_f32_16x16x32_bf16 v[26:29], v[152:155], v[208:211], v[26:29]
	v_mfma_f32_16x16x32_bf16 v[18:21], v[160:163], v[208:211], v[18:21]
	v_mfma_f32_16x16x32_bf16 v[46:49], v[164:167], v[180:183], v[46:49]
	v_mfma_f32_16x16x32_bf16 v[38:41], v[172:175], v[180:183], v[38:41]
	v_mfma_f32_16x16x32_bf16 v[30:33], v[164:167], v[188:191], v[30:33]
	v_mfma_f32_16x16x32_bf16 v[22:25], v[172:175], v[188:191], v[22:25]
	v_mfma_f32_16x16x32_bf16 v[14:17], v[164:167], v[196:199], v[14:17]
	v_mfma_f32_16x16x32_bf16 v[10:13], v[172:175], v[196:199], v[10:13]
	v_mfma_f32_16x16x32_bf16 v[6:9], v[164:167], v[204:207], v[6:9]
	v_mfma_f32_16x16x32_bf16 v[2:5], v[172:175], v[204:207], v[2:5]
	v_mfma_f32_16x16x32_bf16 v[46:49], v[168:171], v[184:187], v[46:49]
	v_mfma_f32_16x16x32_bf16 v[38:41], v[176:179], v[184:187], v[38:41]
	v_mfma_f32_16x16x32_bf16 v[30:33], v[168:171], v[192:195], v[30:33]
	v_mfma_f32_16x16x32_bf16 v[22:25], v[176:179], v[192:195], v[22:25]
	v_mfma_f32_16x16x32_bf16 v[14:17], v[168:171], v[200:203], v[14:17]
	v_mfma_f32_16x16x32_bf16 v[10:13], v[176:179], v[200:203], v[10:13]
	v_mfma_f32_16x16x32_bf16 v[6:9], v[168:171], v[208:211], v[6:9]
	v_mfma_f32_16x16x32_bf16 v[2:5], v[176:179], v[208:211], v[2:5]
	s_setprio 0
	s_barrier
	s_add_i32 s60, 0, 0x18000
	s_add_i32 s61, 0, 0x1c000
	v_add_u32_e32 v160, s60, v144
	v_add_u32_e32 v176, s61, v144
	ds_read_b128 v[148:151], v160
	ds_read_b128 v[152:155], v160 offset:1024
	ds_read_b128 v[156:159], v160 offset:2048
	ds_read_b128 v[160:163], v160 offset:3072
	ds_read_b128 v[164:167], v176
	ds_read_b128 v[168:171], v176 offset:1024
	ds_read_b128 v[172:175], v176 offset:2048
	ds_read_b128 v[176:179], v176 offset:3072
	s_add_u32 s20, s20, 0x100000
	s_addc_u32 s21, s21, 0
	s_mov_b32 m0, s35
	v_lshl_add_u64 v[220:221], s[20:21], 0, v[132:133]
	ds_read_b128 v[180:183], v145 offset:32768
	ds_read_b128 v[184:187], v145 offset:33792
	ds_read_b128 v[188:191], v145 offset:34816
	ds_read_b128 v[192:195], v145 offset:35840
	ds_read_b128 v[196:199], v145 offset:36864
	ds_read_b128 v[200:203], v145 offset:37888
	ds_read_b128 v[204:207], v145 offset:38912
	ds_read_b128 v[208:211], v145 offset:39936
	global_load_lds_dwordx4 v[220:221], off
	v_lshl_add_u64 v[220:221], s[20:21], 0, v[134:135]
	s_mov_b32 m0, s38
	s_nop 0
	global_load_lds_dwordx4 v[220:221], off
	s_waitcnt vmcnt(8) lgkmcnt(0)
	s_barrier
	s_setprio 1
	v_mfma_f32_16x16x32_bf16 v[126:129], v[148:151], v[180:183], v[126:129]
	v_mfma_f32_16x16x32_bf16 v[122:125], v[156:159], v[180:183], v[122:125]
	v_mfma_f32_16x16x32_bf16 v[118:121], v[148:151], v[188:191], v[118:121]
	v_mfma_f32_16x16x32_bf16 v[114:117], v[156:159], v[188:191], v[114:117]
	v_mfma_f32_16x16x32_bf16 v[106:109], v[148:151], v[196:199], v[106:109]
	v_mfma_f32_16x16x32_bf16 v[98:101], v[156:159], v[196:199], v[98:101]
	v_mfma_f32_16x16x32_bf16 v[90:93], v[148:151], v[204:207], v[90:93]
	v_mfma_f32_16x16x32_bf16 v[82:85], v[156:159], v[204:207], v[82:85]
	v_mfma_f32_16x16x32_bf16 v[126:129], v[152:155], v[184:187], v[126:129]
	v_mfma_f32_16x16x32_bf16 v[122:125], v[160:163], v[184:187], v[122:125]
	v_mfma_f32_16x16x32_bf16 v[118:121], v[152:155], v[192:195], v[118:121]
	v_mfma_f32_16x16x32_bf16 v[114:117], v[160:163], v[192:195], v[114:117]
	v_mfma_f32_16x16x32_bf16 v[106:109], v[152:155], v[200:203], v[106:109]
	v_mfma_f32_16x16x32_bf16 v[98:101], v[160:163], v[200:203], v[98:101]
	v_mfma_f32_16x16x32_bf16 v[90:93], v[152:155], v[208:211], v[90:93]
	v_mfma_f32_16x16x32_bf16 v[82:85], v[160:163], v[208:211], v[82:85]
	v_mfma_f32_16x16x32_bf16 v[110:113], v[164:167], v[180:183], v[110:113]
	v_mfma_f32_16x16x32_bf16 v[102:105], v[172:175], v[180:183], v[102:105]
	v_mfma_f32_16x16x32_bf16 v[94:97], v[164:167], v[188:191], v[94:97]
	v_mfma_f32_16x16x32_bf16 v[86:89], v[172:175], v[188:191], v[86:89]
	v_mfma_f32_16x16x32_bf16 v[78:81], v[164:167], v[196:199], v[78:81]
	v_mfma_f32_16x16x32_bf16 v[74:77], v[172:175], v[196:199], v[74:77]
	v_mfma_f32_16x16x32_bf16 v[70:73], v[164:167], v[204:207], v[70:73]
	v_mfma_f32_16x16x32_bf16 v[66:69], v[172:175], v[204:207], v[66:69]
	v_mfma_f32_16x16x32_bf16 v[110:113], v[168:171], v[184:187], v[110:113]
	v_mfma_f32_16x16x32_bf16 v[102:105], v[176:179], v[184:187], v[102:105]
	v_mfma_f32_16x16x32_bf16 v[94:97], v[168:171], v[192:195], v[94:97]
	v_mfma_f32_16x16x32_bf16 v[86:89], v[176:179], v[192:195], v[86:89]
	v_mfma_f32_16x16x32_bf16 v[78:81], v[168:171], v[200:203], v[78:81]
	v_mfma_f32_16x16x32_bf16 v[74:77], v[176:179], v[200:203], v[74:77]
	v_mfma_f32_16x16x32_bf16 v[70:73], v[168:171], v[208:211], v[70:73]
	v_mfma_f32_16x16x32_bf16 v[66:69], v[176:179], v[208:211], v[66:69]
	s_setprio 0
	s_barrier
	s_add_i32 s20, s60, s31
	v_lshl_add_u64 v[212:213], v[212:213], 0, s[4:5]
	s_mov_b32 m0, s20
	ds_read_b128 v[180:183], v145 offset:49152
	ds_read_b128 v[184:187], v145 offset:50176
	ds_read_b128 v[188:191], v145 offset:51200
	ds_read_b128 v[192:195], v145 offset:52224
	ds_read_b128 v[196:199], v145 offset:53248
	ds_read_b128 v[200:203], v145 offset:54272
	ds_read_b128 v[204:207], v145 offset:55296
	ds_read_b128 v[208:211], v145 offset:56320
	global_load_lds_dwordx4 v[212:213], off
	s_add_i32 m0, s20, 0x2000
	s_add_u32 s16, s16, 0x100080
	v_lshl_add_u64 v[212:213], v[214:215], 0, s[4:5]
	s_addc_u32 s17, s17, 0
	s_add_i32 s20, s61, s31
	global_load_lds_dwordx4 v[212:213], off
	v_lshl_add_u64 v[212:213], s[16:17], 0, v[130:131]
	s_mov_b32 m0, s20
	s_nop 0
	global_load_lds_dwordx4 v[212:213], off
	v_lshl_add_u64 v[212:213], s[16:17], 0, v[136:137]
	s_add_i32 m0, s20, 0x2000
	s_nop 0
	global_load_lds_dwordx4 v[212:213], off
	v_lshl_add_u64 v[212:213], v[216:217], 0, s[4:5]
	s_mov_b32 m0, s40
	s_nop 0
	global_load_lds_dwordx4 v[212:213], off
	v_lshl_add_u64 v[212:213], v[218:219], 0, s[4:5]
	s_mov_b32 m0, s41
	s_nop 0
	global_load_lds_dwordx4 v[212:213], off
	s_waitcnt vmcnt(8) lgkmcnt(0)
	s_barrier
	s_setprio 1
	v_mfma_f32_16x16x32_bf16 v[62:65], v[148:151], v[180:183], v[62:65]
	v_mfma_f32_16x16x32_bf16 v[58:61], v[156:159], v[180:183], v[58:61]
	v_mfma_f32_16x16x32_bf16 v[54:57], v[148:151], v[188:191], v[54:57]
	v_mfma_f32_16x16x32_bf16 v[50:53], v[156:159], v[188:191], v[50:53]
	v_mfma_f32_16x16x32_bf16 v[42:45], v[148:151], v[196:199], v[42:45]
	v_mfma_f32_16x16x32_bf16 v[34:37], v[156:159], v[196:199], v[34:37]
	v_mfma_f32_16x16x32_bf16 v[26:29], v[148:151], v[204:207], v[26:29]
	v_mfma_f32_16x16x32_bf16 v[18:21], v[156:159], v[204:207], v[18:21]
	v_mfma_f32_16x16x32_bf16 v[62:65], v[152:155], v[184:187], v[62:65]
	v_mfma_f32_16x16x32_bf16 v[58:61], v[160:163], v[184:187], v[58:61]
	v_mfma_f32_16x16x32_bf16 v[54:57], v[152:155], v[192:195], v[54:57]
	v_mfma_f32_16x16x32_bf16 v[50:53], v[160:163], v[192:195], v[50:53]
	v_mfma_f32_16x16x32_bf16 v[42:45], v[152:155], v[200:203], v[42:45]
	v_mfma_f32_16x16x32_bf16 v[34:37], v[160:163], v[200:203], v[34:37]
	v_mfma_f32_16x16x32_bf16 v[26:29], v[152:155], v[208:211], v[26:29]
	v_mfma_f32_16x16x32_bf16 v[18:21], v[160:163], v[208:211], v[18:21]
	v_mfma_f32_16x16x32_bf16 v[46:49], v[164:167], v[180:183], v[46:49]
	v_mfma_f32_16x16x32_bf16 v[38:41], v[172:175], v[180:183], v[38:41]
	v_mfma_f32_16x16x32_bf16 v[30:33], v[164:167], v[188:191], v[30:33]
	v_mfma_f32_16x16x32_bf16 v[22:25], v[172:175], v[188:191], v[22:25]
	v_mfma_f32_16x16x32_bf16 v[14:17], v[164:167], v[196:199], v[14:17]
	v_mfma_f32_16x16x32_bf16 v[10:13], v[172:175], v[196:199], v[10:13]
	v_mfma_f32_16x16x32_bf16 v[6:9], v[164:167], v[204:207], v[6:9]
	v_mfma_f32_16x16x32_bf16 v[2:5], v[172:175], v[204:207], v[2:5]
	v_mfma_f32_16x16x32_bf16 v[46:49], v[168:171], v[184:187], v[46:49]
	v_mfma_f32_16x16x32_bf16 v[38:41], v[176:179], v[184:187], v[38:41]
	v_mfma_f32_16x16x32_bf16 v[30:33], v[168:171], v[192:195], v[30:33]
	v_mfma_f32_16x16x32_bf16 v[22:25], v[176:179], v[192:195], v[22:25]
	v_mfma_f32_16x16x32_bf16 v[14:17], v[168:171], v[200:203], v[14:17]
	v_mfma_f32_16x16x32_bf16 v[10:13], v[176:179], v[200:203], v[10:13]
	v_mfma_f32_16x16x32_bf16 v[6:9], v[168:171], v[208:211], v[6:9]
	v_mfma_f32_16x16x32_bf16 v[2:5], v[176:179], v[208:211], v[2:5]
	s_setprio 0
	s_barrier
	s_add_i32 s50, s50, 2
	s_add_u32 s14, s14, 0x100
	s_addc_u32 s15, s15, 0
	s_cmp_gt_u32 s50, 13
	s_cbranch_scc0 .LBB0_758
	s_cmpk_lt_u32 s30, 0x100
	s_cbranch_scc0 .LBB0_754
	s_barrier
	s_branch .LBB0_754

.LBB0_768:
	ds_read_b128 v[130:133], v1
	ds_read_b128 v[134:137], v1 offset:1024
	ds_read_b128 v[138:141], v1 offset:2048
	ds_read_b128 v[142:145], v1 offset:3072
	ds_read_b128 v[180:183], v176
	ds_read_b128 v[184:187], v176 offset:1024
	ds_read_b128 v[188:191], v176 offset:2048
	ds_read_b128 v[192:195], v176 offset:3072
	s_add_u32 s1, s16, 0xfff00080
	s_addc_u32 s20, s17, -1
	s_add_u32 s49, s16, 0xdb300080
	s_addc_u32 s21, s17, -1
	s_cmp_eq_u32 s0, 60
	s_cselect_b32 s25, s55, s20
	s_cselect_b32 s24, s54, s1
	s_cselect_b32 s21, s9, s21
	s_cselect_b32 s20, s8, s49
	s_mov_b32 m0, s35
	v_lshl_add_u64 v[228:229], s[16:17], 0, v[172:173]
	ds_read_b128 v[196:199], v177
	ds_read_b128 v[200:203], v177 offset:1024
	ds_read_b128 v[204:207], v177 offset:2048
	ds_read_b128 v[208:211], v177 offset:3072
	ds_read_b128 v[212:215], v177 offset:4096
	ds_read_b128 v[216:219], v177 offset:5120
	ds_read_b128 v[220:223], v177 offset:6144
	ds_read_b128 v[224:227], v177 offset:7168
	global_load_lds_dwordx4 v[228:229], off
	v_lshl_add_u64 v[228:229], s[16:17], 0, v[174:175]
	s_mov_b32 m0, s36
	s_nop 0
	global_load_lds_dwordx4 v[228:229], off
	s_waitcnt vmcnt(8) lgkmcnt(0)
	s_barrier
	s_setprio 1
	v_mfma_f32_16x16x32_bf16 v[126:129], v[130:133], v[196:199], v[126:129]
	v_mfma_f32_16x16x32_bf16 v[122:125], v[138:141], v[196:199], v[122:125]
	v_mfma_f32_16x16x32_bf16 v[114:117], v[130:133], v[204:207], v[114:117]
	v_mfma_f32_16x16x32_bf16 v[106:109], v[138:141], v[204:207], v[106:109]
	v_mfma_f32_16x16x32_bf16 v[98:101], v[130:133], v[212:215], v[98:101]
	v_mfma_f32_16x16x32_bf16 v[90:93], v[138:141], v[212:215], v[90:93]
	v_mfma_f32_16x16x32_bf16 v[82:85], v[130:133], v[220:223], v[82:85]
	v_mfma_f32_16x16x32_bf16 v[74:77], v[138:141], v[220:223], v[74:77]
	v_mfma_f32_16x16x32_bf16 v[126:129], v[134:137], v[200:203], v[126:129]
	v_mfma_f32_16x16x32_bf16 v[122:125], v[142:145], v[200:203], v[122:125]
	v_mfma_f32_16x16x32_bf16 v[114:117], v[134:137], v[208:211], v[114:117]
	v_mfma_f32_16x16x32_bf16 v[106:109], v[142:145], v[208:211], v[106:109]
	v_mfma_f32_16x16x32_bf16 v[98:101], v[134:137], v[216:219], v[98:101]
	v_mfma_f32_16x16x32_bf16 v[90:93], v[142:145], v[216:219], v[90:93]
	v_mfma_f32_16x16x32_bf16 v[82:85], v[134:137], v[224:227], v[82:85]
	v_mfma_f32_16x16x32_bf16 v[74:77], v[142:145], v[224:227], v[74:77]
	v_mfma_f32_16x16x32_bf16 v[118:121], v[180:183], v[196:199], v[118:121]
	v_mfma_f32_16x16x32_bf16 v[110:113], v[188:191], v[196:199], v[110:113]
	v_mfma_f32_16x16x32_bf16 v[102:105], v[180:183], v[204:207], v[102:105]
	v_mfma_f32_16x16x32_bf16 v[94:97], v[188:191], v[204:207], v[94:97]
	v_mfma_f32_16x16x32_bf16 v[86:89], v[180:183], v[212:215], v[86:89]
	v_mfma_f32_16x16x32_bf16 v[78:81], v[188:191], v[212:215], v[78:81]
	v_mfma_f32_16x16x32_bf16 v[70:73], v[180:183], v[220:223], v[70:73]
	v_mfma_f32_16x16x32_bf16 v[66:69], v[188:191], v[220:223], v[66:69]
	v_mfma_f32_16x16x32_bf16 v[118:121], v[184:187], v[200:203], v[118:121]
	v_mfma_f32_16x16x32_bf16 v[110:113], v[192:195], v[200:203], v[110:113]
	v_mfma_f32_16x16x32_bf16 v[102:105], v[184:187], v[208:211], v[102:105]
	v_mfma_f32_16x16x32_bf16 v[94:97], v[192:195], v[208:211], v[94:97]
	v_mfma_f32_16x16x32_bf16 v[86:89], v[184:187], v[216:219], v[86:89]
	v_mfma_f32_16x16x32_bf16 v[78:81], v[192:195], v[216:219], v[78:81]
	v_mfma_f32_16x16x32_bf16 v[70:73], v[184:187], v[224:227], v[70:73]
	v_mfma_f32_16x16x32_bf16 v[66:69], v[192:195], v[224:227], v[66:69]
	s_setprio 0
	s_barrier
	s_mov_b32 m0, s37
	v_lshl_add_u64 v[228:229], s[20:21], 0, v[150:151]
	s_add_u32 s50, s20, 0x100000
	ds_read_b128 v[196:199], v177 offset:16384
	ds_read_b128 v[200:203], v177 offset:17408
	ds_read_b128 v[204:207], v177 offset:18432
	ds_read_b128 v[208:211], v177 offset:19456
	ds_read_b128 v[212:215], v177 offset:20480
	ds_read_b128 v[216:219], v177 offset:21504
	ds_read_b128 v[220:223], v177 offset:22528
	ds_read_b128 v[224:227], v177 offset:23552
	global_load_lds_dwordx4 v[228:229], off
	v_lshl_add_u64 v[230:231], s[20:21], 0, v[146:147]
	s_mov_b32 m0, s38
	s_addc_u32 s51, s21, 0
	global_load_lds_dwordx4 v[230:231], off
	v_lshl_add_u64 v[232:233], s[50:51], 0, v[150:151]
	s_mov_b32 m0, s39
	v_lshl_add_u64 v[234:235], s[24:25], 0, v[148:149]
	global_load_lds_dwordx4 v[232:233], off
	v_lshl_add_u64 v[232:233], s[50:51], 0, v[146:147]
	s_mov_b32 m0, s40
	s_nop 0
	global_load_lds_dwordx4 v[232:233], off
	v_lshl_add_u64 v[232:233], s[24:25], 0, v[152:153]
	s_mov_b32 m0, s26
	s_nop 0
	global_load_lds_dwordx4 v[232:233], off
	s_mov_b32 m0, s27
	s_nop 0
	global_load_lds_dwordx4 v[234:235], off
	s_waitcnt vmcnt(8) lgkmcnt(0)
	s_barrier
	s_setprio 1
	v_mfma_f32_16x16x32_bf16 v[62:65], v[130:133], v[196:199], v[62:65]
	v_mfma_f32_16x16x32_bf16 v[58:61], v[138:141], v[196:199], v[58:61]
	v_mfma_f32_16x16x32_bf16 v[50:53], v[130:133], v[204:207], v[50:53]
	v_mfma_f32_16x16x32_bf16 v[42:45], v[138:141], v[204:207], v[42:45]
	v_mfma_f32_16x16x32_bf16 v[34:37], v[130:133], v[212:215], v[34:37]
	v_mfma_f32_16x16x32_bf16 v[26:29], v[138:141], v[212:215], v[26:29]
	v_mfma_f32_16x16x32_bf16 v[18:21], v[130:133], v[220:223], v[18:21]
	v_mfma_f32_16x16x32_bf16 v[10:13], v[138:141], v[220:223], v[10:13]
	v_mfma_f32_16x16x32_bf16 v[62:65], v[134:137], v[200:203], v[62:65]
	v_mfma_f32_16x16x32_bf16 v[58:61], v[142:145], v[200:203], v[58:61]
	v_mfma_f32_16x16x32_bf16 v[50:53], v[134:137], v[208:211], v[50:53]
	v_mfma_f32_16x16x32_bf16 v[42:45], v[142:145], v[208:211], v[42:45]
	v_mfma_f32_16x16x32_bf16 v[34:37], v[134:137], v[216:219], v[34:37]
	v_mfma_f32_16x16x32_bf16 v[26:29], v[142:145], v[216:219], v[26:29]
	v_mfma_f32_16x16x32_bf16 v[18:21], v[134:137], v[224:227], v[18:21]
	v_mfma_f32_16x16x32_bf16 v[10:13], v[142:145], v[224:227], v[10:13]
	v_mfma_f32_16x16x32_bf16 v[54:57], v[180:183], v[196:199], v[54:57]
	v_mfma_f32_16x16x32_bf16 v[46:49], v[188:191], v[196:199], v[46:49]
	v_mfma_f32_16x16x32_bf16 v[38:41], v[180:183], v[204:207], v[38:41]
	v_mfma_f32_16x16x32_bf16 v[30:33], v[188:191], v[204:207], v[30:33]
	v_mfma_f32_16x16x32_bf16 v[22:25], v[180:183], v[212:215], v[22:25]
	v_mfma_f32_16x16x32_bf16 v[14:17], v[188:191], v[212:215], v[14:17]
	v_mfma_f32_16x16x32_bf16 v[6:9], v[180:183], v[220:223], v[6:9]
	v_mfma_f32_16x16x32_bf16 v[2:5], v[188:191], v[220:223], v[2:5]
	v_mfma_f32_16x16x32_bf16 v[54:57], v[184:187], v[200:203], v[54:57]
	v_mfma_f32_16x16x32_bf16 v[46:49], v[192:195], v[200:203], v[46:49]
	v_mfma_f32_16x16x32_bf16 v[38:41], v[184:187], v[208:211], v[38:41]
	v_mfma_f32_16x16x32_bf16 v[30:33], v[192:195], v[208:211], v[30:33]
	v_mfma_f32_16x16x32_bf16 v[22:25], v[184:187], v[216:219], v[22:25]
	v_mfma_f32_16x16x32_bf16 v[14:17], v[192:195], v[216:219], v[14:17]
	v_mfma_f32_16x16x32_bf16 v[6:9], v[184:187], v[224:227], v[6:9]
	v_mfma_f32_16x16x32_bf16 v[2:5], v[192:195], v[224:227], v[2:5]
	s_setprio 0
	s_barrier
	ds_read_b128 v[130:133], v178
	ds_read_b128 v[134:137], v178 offset:1024
	ds_read_b128 v[138:141], v178 offset:2048
	ds_read_b128 v[142:145], v178 offset:3072
	ds_read_b128 v[180:183], v179
	ds_read_b128 v[184:187], v179 offset:1024
	ds_read_b128 v[188:191], v179 offset:2048
	ds_read_b128 v[192:195], v179 offset:3072
	s_add_u32 s24, s24, 0x100000
	s_addc_u32 s25, s25, 0
	s_mov_b32 m0, s28
	v_lshl_add_u64 v[236:237], s[24:25], 0, v[152:153]
	ds_read_b128 v[196:199], v177 offset:32768
	ds_read_b128 v[200:203], v177 offset:33792
	ds_read_b128 v[204:207], v177 offset:34816
	ds_read_b128 v[208:211], v177 offset:35840
	ds_read_b128 v[212:215], v177 offset:36864
	ds_read_b128 v[216:219], v177 offset:37888
	ds_read_b128 v[220:223], v177 offset:38912
	ds_read_b128 v[224:227], v177 offset:39936
	global_load_lds_dwordx4 v[236:237], off
	v_lshl_add_u64 v[236:237], s[24:25], 0, v[148:149]
	s_mov_b32 m0, s29
	s_nop 0
	global_load_lds_dwordx4 v[236:237], off
	s_waitcnt vmcnt(8) lgkmcnt(0)
	s_barrier
	s_setprio 1
	v_mfma_f32_16x16x32_bf16 v[126:129], v[130:133], v[196:199], v[126:129]
	v_mfma_f32_16x16x32_bf16 v[122:125], v[138:141], v[196:199], v[122:125]
	v_mfma_f32_16x16x32_bf16 v[114:117], v[130:133], v[204:207], v[114:117]
	v_mfma_f32_16x16x32_bf16 v[106:109], v[138:141], v[204:207], v[106:109]
	v_mfma_f32_16x16x32_bf16 v[98:101], v[130:133], v[212:215], v[98:101]
	v_mfma_f32_16x16x32_bf16 v[90:93], v[138:141], v[212:215], v[90:93]
	v_mfma_f32_16x16x32_bf16 v[82:85], v[130:133], v[220:223], v[82:85]
	v_mfma_f32_16x16x32_bf16 v[74:77], v[138:141], v[220:223], v[74:77]
	v_mfma_f32_16x16x32_bf16 v[126:129], v[134:137], v[200:203], v[126:129]
	v_mfma_f32_16x16x32_bf16 v[122:125], v[142:145], v[200:203], v[122:125]
	v_mfma_f32_16x16x32_bf16 v[114:117], v[134:137], v[208:211], v[114:117]
	v_mfma_f32_16x16x32_bf16 v[106:109], v[142:145], v[208:211], v[106:109]
	v_mfma_f32_16x16x32_bf16 v[98:101], v[134:137], v[216:219], v[98:101]
	v_mfma_f32_16x16x32_bf16 v[90:93], v[142:145], v[216:219], v[90:93]
	v_mfma_f32_16x16x32_bf16 v[82:85], v[134:137], v[224:227], v[82:85]
	v_mfma_f32_16x16x32_bf16 v[74:77], v[142:145], v[224:227], v[74:77]
	v_mfma_f32_16x16x32_bf16 v[118:121], v[180:183], v[196:199], v[118:121]
	v_mfma_f32_16x16x32_bf16 v[110:113], v[188:191], v[196:199], v[110:113]
	v_mfma_f32_16x16x32_bf16 v[102:105], v[180:183], v[204:207], v[102:105]
	v_mfma_f32_16x16x32_bf16 v[94:97], v[188:191], v[204:207], v[94:97]
	v_mfma_f32_16x16x32_bf16 v[86:89], v[180:183], v[212:215], v[86:89]
	v_mfma_f32_16x16x32_bf16 v[78:81], v[188:191], v[212:215], v[78:81]
	v_mfma_f32_16x16x32_bf16 v[70:73], v[180:183], v[220:223], v[70:73]
	v_mfma_f32_16x16x32_bf16 v[66:69], v[188:191], v[220:223], v[66:69]
	v_mfma_f32_16x16x32_bf16 v[118:121], v[184:187], v[200:203], v[118:121]
	v_mfma_f32_16x16x32_bf16 v[110:113], v[192:195], v[200:203], v[110:113]
	v_mfma_f32_16x16x32_bf16 v[102:105], v[184:187], v[208:211], v[102:105]
	v_mfma_f32_16x16x32_bf16 v[94:97], v[192:195], v[208:211], v[94:97]
	v_mfma_f32_16x16x32_bf16 v[86:89], v[184:187], v[216:219], v[86:89]
	v_mfma_f32_16x16x32_bf16 v[78:81], v[192:195], v[216:219], v[78:81]
	v_mfma_f32_16x16x32_bf16 v[70:73], v[184:187], v[224:227], v[70:73]
	v_mfma_f32_16x16x32_bf16 v[66:69], v[192:195], v[224:227], v[66:69]
	s_setprio 0
	s_barrier
	s_mov_b32 m0, s41
	v_lshl_add_u64 v[228:229], v[228:229], 0, s[14:15]
	s_add_u32 s20, s20, 0x100080
	ds_read_b128 v[196:199], v177 offset:49152
	ds_read_b128 v[200:203], v177 offset:50176
	ds_read_b128 v[204:207], v177 offset:51200
	ds_read_b128 v[208:211], v177 offset:52224
	ds_read_b128 v[212:215], v177 offset:53248
	ds_read_b128 v[216:219], v177 offset:54272
	ds_read_b128 v[220:223], v177 offset:55296
	ds_read_b128 v[224:227], v177 offset:56320
	global_load_lds_dwordx4 v[228:229], off
	v_lshl_add_u64 v[228:229], v[230:231], 0, s[14:15]
	s_mov_b32 m0, s42
	s_addc_u32 s21, s21, 0
	global_load_lds_dwordx4 v[228:229], off
	v_lshl_add_u64 v[228:229], s[20:21], 0, v[150:151]
	s_mov_b32 m0, s43
	s_nop 0
	global_load_lds_dwordx4 v[228:229], off
	v_lshl_add_u64 v[228:229], s[20:21], 0, v[146:147]
	s_mov_b32 m0, s48
	s_nop 0
	global_load_lds_dwordx4 v[228:229], off
	v_lshl_add_u64 v[228:229], v[232:233], 0, s[14:15]
	s_mov_b32 m0, s31
	s_nop 0
	global_load_lds_dwordx4 v[228:229], off
	v_lshl_add_u64 v[228:229], v[234:235], 0, s[14:15]
	s_mov_b32 m0, s34
	s_nop 0
	global_load_lds_dwordx4 v[228:229], off
	s_waitcnt vmcnt(8) lgkmcnt(0)
	s_barrier
	s_setprio 1
	v_mfma_f32_16x16x32_bf16 v[62:65], v[130:133], v[196:199], v[62:65]
	v_mfma_f32_16x16x32_bf16 v[58:61], v[138:141], v[196:199], v[58:61]
	v_mfma_f32_16x16x32_bf16 v[50:53], v[130:133], v[204:207], v[50:53]
	v_mfma_f32_16x16x32_bf16 v[42:45], v[138:141], v[204:207], v[42:45]
	v_mfma_f32_16x16x32_bf16 v[34:37], v[130:133], v[212:215], v[34:37]
	v_mfma_f32_16x16x32_bf16 v[26:29], v[138:141], v[212:215], v[26:29]
	v_mfma_f32_16x16x32_bf16 v[18:21], v[130:133], v[220:223], v[18:21]
	v_mfma_f32_16x16x32_bf16 v[10:13], v[138:141], v[220:223], v[10:13]
	v_mfma_f32_16x16x32_bf16 v[62:65], v[134:137], v[200:203], v[62:65]
	v_mfma_f32_16x16x32_bf16 v[58:61], v[142:145], v[200:203], v[58:61]
	v_mfma_f32_16x16x32_bf16 v[50:53], v[134:137], v[208:211], v[50:53]
	v_mfma_f32_16x16x32_bf16 v[42:45], v[142:145], v[208:211], v[42:45]
	v_mfma_f32_16x16x32_bf16 v[34:37], v[134:137], v[216:219], v[34:37]
	v_mfma_f32_16x16x32_bf16 v[26:29], v[142:145], v[216:219], v[26:29]
	v_mfma_f32_16x16x32_bf16 v[18:21], v[134:137], v[224:227], v[18:21]
	v_mfma_f32_16x16x32_bf16 v[10:13], v[142:145], v[224:227], v[10:13]
	v_mfma_f32_16x16x32_bf16 v[54:57], v[180:183], v[196:199], v[54:57]
	v_mfma_f32_16x16x32_bf16 v[46:49], v[188:191], v[196:199], v[46:49]
	v_mfma_f32_16x16x32_bf16 v[38:41], v[180:183], v[204:207], v[38:41]
	v_mfma_f32_16x16x32_bf16 v[30:33], v[188:191], v[204:207], v[30:33]
	v_mfma_f32_16x16x32_bf16 v[22:25], v[180:183], v[212:215], v[22:25]
	v_mfma_f32_16x16x32_bf16 v[14:17], v[188:191], v[212:215], v[14:17]
	v_mfma_f32_16x16x32_bf16 v[6:9], v[180:183], v[220:223], v[6:9]
	v_mfma_f32_16x16x32_bf16 v[2:5], v[188:191], v[220:223], v[2:5]
	v_mfma_f32_16x16x32_bf16 v[54:57], v[184:187], v[200:203], v[54:57]
	v_mfma_f32_16x16x32_bf16 v[46:49], v[192:195], v[200:203], v[46:49]
	v_mfma_f32_16x16x32_bf16 v[38:41], v[184:187], v[208:211], v[38:41]
	v_mfma_f32_16x16x32_bf16 v[30:33], v[192:195], v[208:211], v[30:33]
	v_mfma_f32_16x16x32_bf16 v[22:25], v[184:187], v[216:219], v[22:25]
	v_mfma_f32_16x16x32_bf16 v[14:17], v[192:195], v[216:219], v[14:17]
	v_mfma_f32_16x16x32_bf16 v[6:9], v[184:187], v[224:227], v[6:9]
	v_mfma_f32_16x16x32_bf16 v[2:5], v[192:195], v[224:227], v[2:5]
	s_setprio 0
	s_barrier
	s_add_i32 s0, s0, 2
	s_add_u32 s16, s16, 0x100
	s_addc_u32 s17, s17, 0
	s_cmp_gt_u32 s0, 61
	s_cbranch_scc0 .LBB0_768
	s_and_b64 vcc, exec, s[10:11]
	s_cbranch_vccz .LBB0_771
	s_barrier

.LBB0_788:
	v_add_u32_e32 v130, s15, v190
	v_add_u32_e32 v134, s50, v190
	ds_read_b128 v[158:161], v130
	ds_read_b128 v[150:153], v130 offset:1024
	ds_read_b128 v[154:157], v130 offset:2048
	ds_read_b128 v[146:149], v130 offset:3072
	ds_read_b128 v[142:145], v134
	ds_read_b128 v[130:133], v134 offset:1024
	ds_read_b128 v[138:141], v134 offset:2048
	ds_read_b128 v[134:137], v134 offset:3072
	s_add_u32 s36, s34, 0xfff80080
	s_addc_u32 s37, s35, -1
	s_and_b64 s[0:1], s[0:1], exec
	s_cselect_b32 s39, s21, s37
	s_cselect_b32 s38, s60, s36
	s_cselect_b32 s37, s17, s63
	s_cselect_b32 s36, s61, s62
	s_add_i32 m0, s29, 0xc000
	ds_read_b128 v[182:185], v193
	ds_read_b128 v[186:189], v193 offset:1024
	ds_read_b128 v[194:197], v193 offset:2048
	ds_read_b128 v[198:201], v193 offset:3072
	ds_read_b128 v[202:205], v193 offset:4096
	ds_read_b128 v[206:209], v193 offset:5120
	ds_read_b128 v[210:213], v193 offset:6144
	ds_read_b128 v[214:217], v193 offset:7168
	global_load_lds_dwordx4 v172, s[34:35]
	s_add_i32 m0, s29, 0xe000
	s_nop 0
	global_load_lds_dwordx4 v174, s[34:35]
	s_waitcnt vmcnt(8) lgkmcnt(0)
	s_barrier
	s_setprio 1
	v_mfma_i32_16x16x64_i8 v[126:129], v[158:161], v[182:185], v[126:129]
	v_mfma_i32_16x16x64_i8 v[122:125], v[154:157], v[182:185], v[122:125]
	v_mfma_i32_16x16x64_i8 v[106:109], v[154:157], v[194:197], v[106:109]
	v_mfma_i32_16x16x64_i8 v[114:117], v[158:161], v[194:197], v[114:117]
	v_mfma_i32_16x16x64_i8 v[98:101], v[158:161], v[202:205], v[98:101]
	v_mfma_i32_16x16x64_i8 v[90:93], v[154:157], v[202:205], v[90:93]
	v_mfma_i32_16x16x64_i8 v[74:77], v[154:157], v[210:213], v[74:77]
	v_mfma_i32_16x16x64_i8 v[82:85], v[158:161], v[210:213], v[82:85]
	s_nop 0
	v_mfma_i32_16x16x64_i8 v[126:129], v[150:153], v[186:189], v[126:129]
	v_mfma_i32_16x16x64_i8 v[122:125], v[146:149], v[186:189], v[122:125]
	v_mfma_i32_16x16x64_i8 v[106:109], v[146:149], v[198:201], v[106:109]
	v_mfma_i32_16x16x64_i8 v[114:117], v[150:153], v[198:201], v[114:117]
	v_mfma_i32_16x16x64_i8 v[98:101], v[150:153], v[206:209], v[98:101]
	v_mfma_i32_16x16x64_i8 v[90:93], v[146:149], v[206:209], v[90:93]
	v_mfma_i32_16x16x64_i8 v[74:77], v[146:149], v[214:217], v[74:77]
	v_mfma_i32_16x16x64_i8 v[82:85], v[150:153], v[214:217], v[82:85]
	v_mfma_i32_16x16x64_i8 v[118:121], v[142:145], v[182:185], v[118:121]
	v_mfma_i32_16x16x64_i8 v[110:113], v[138:141], v[182:185], v[110:113]
	v_mfma_i32_16x16x64_i8 v[94:97], v[138:141], v[194:197], v[94:97]
	v_mfma_i32_16x16x64_i8 v[102:105], v[142:145], v[194:197], v[102:105]
	v_mfma_i32_16x16x64_i8 v[86:89], v[142:145], v[202:205], v[86:89]
	v_mfma_i32_16x16x64_i8 v[78:81], v[138:141], v[202:205], v[78:81]
	v_mfma_i32_16x16x64_i8 v[66:69], v[138:141], v[210:213], v[66:69]
	v_mfma_i32_16x16x64_i8 v[70:73], v[142:145], v[210:213], v[70:73]
	s_nop 0
	v_mfma_i32_16x16x64_i8 v[118:121], v[130:133], v[186:189], v[118:121]
	v_mfma_i32_16x16x64_i8 v[110:113], v[134:137], v[186:189], v[110:113]
	v_mfma_i32_16x16x64_i8 v[94:97], v[134:137], v[198:201], v[94:97]
	v_mfma_i32_16x16x64_i8 v[102:105], v[130:133], v[198:201], v[102:105]
	v_mfma_i32_16x16x64_i8 v[86:89], v[130:133], v[206:209], v[86:89]
	v_mfma_i32_16x16x64_i8 v[78:81], v[134:137], v[206:209], v[78:81]
	v_mfma_i32_16x16x64_i8 v[66:69], v[134:137], v[214:217], v[66:69]
	v_mfma_i32_16x16x64_i8 v[70:73], v[130:133], v[214:217], v[70:73]
	s_setprio 0
	s_barrier
	s_add_i32 s0, s15, s40
	s_mov_b32 m0, s0
	ds_read_b128 v[194:197], v193 offset:16384
	ds_read_b128 v[198:201], v193 offset:17408
	ds_read_b128 v[202:205], v193 offset:18432
	ds_read_b128 v[206:209], v193 offset:19456
	ds_read_b128 v[210:213], v193 offset:20480
	ds_read_b128 v[214:217], v193 offset:21504
	ds_read_b128 v[218:221], v193 offset:22528
	ds_read_b128 v[222:225], v193 offset:23552
	global_load_lds_dwordx4 v164, s[36:37]
	s_add_i32 m0, s0, 0x2000
	s_add_u32 s0, s36, 0x80000
	s_addc_u32 s1, s37, 0
	s_add_i32 s66, s50, s40
	global_load_lds_dwordx4 v168, s[36:37]
	s_mov_b32 m0, s66
	s_nop 0
	global_load_lds_dwordx4 v164, s[0:1]
	s_add_i32 m0, s66, 0x2000
	s_nop 0
	global_load_lds_dwordx4 v168, s[0:1]
	s_mov_b32 m0, s29
	s_nop 0
	global_load_lds_dwordx4 v162, s[38:39]
	s_mov_b32 m0, s31
	s_nop 0
	global_load_lds_dwordx4 v166, s[38:39]
	s_waitcnt vmcnt(8) lgkmcnt(0)
	s_barrier
	s_setprio 1
	v_mfma_i32_16x16x64_i8 v[62:65], v[158:161], v[194:197], v[62:65]
	v_mfma_i32_16x16x64_i8 v[58:61], v[154:157], v[194:197], v[58:61]
	v_mfma_i32_16x16x64_i8 v[42:45], v[154:157], v[202:205], v[42:45]
	v_mfma_i32_16x16x64_i8 v[50:53], v[158:161], v[202:205], v[50:53]
	v_mfma_i32_16x16x64_i8 v[34:37], v[158:161], v[210:213], v[34:37]
	v_mfma_i32_16x16x64_i8 v[26:29], v[154:157], v[210:213], v[26:29]
	v_mfma_i32_16x16x64_i8 v[10:13], v[154:157], v[218:221], v[10:13]
	v_mfma_i32_16x16x64_i8 v[18:21], v[158:161], v[218:221], v[18:21]
	s_nop 0
	v_mfma_i32_16x16x64_i8 v[62:65], v[150:153], v[198:201], v[62:65]
	v_mfma_i32_16x16x64_i8 v[58:61], v[146:149], v[198:201], v[58:61]
	v_mfma_i32_16x16x64_i8 v[42:45], v[146:149], v[206:209], v[42:45]
	v_mfma_i32_16x16x64_i8 v[50:53], v[150:153], v[206:209], v[50:53]
	v_mfma_i32_16x16x64_i8 v[34:37], v[150:153], v[214:217], v[34:37]
	v_mfma_i32_16x16x64_i8 v[26:29], v[146:149], v[214:217], v[26:29]
	v_mfma_i32_16x16x64_i8 v[10:13], v[146:149], v[222:225], v[10:13]
	v_mfma_i32_16x16x64_i8 v[18:21], v[150:153], v[222:225], v[18:21]
	v_mfma_i32_16x16x64_i8 v[54:57], v[142:145], v[194:197], v[54:57]
	v_mfma_i32_16x16x64_i8 v[46:49], v[138:141], v[194:197], v[46:49]
	v_mfma_i32_16x16x64_i8 v[30:33], v[138:141], v[202:205], v[30:33]
	v_mfma_i32_16x16x64_i8 v[38:41], v[142:145], v[202:205], v[38:41]
	v_mfma_i32_16x16x64_i8 v[22:25], v[142:145], v[210:213], v[22:25]
	v_mfma_i32_16x16x64_i8 v[14:17], v[138:141], v[210:213], v[14:17]
	v_mfma_i32_16x16x64_i8 v[2:5], v[138:141], v[218:221], v[2:5]
	v_mfma_i32_16x16x64_i8 v[6:9], v[142:145], v[218:221], v[6:9]
	s_nop 0
	v_mfma_i32_16x16x64_i8 v[54:57], v[130:133], v[198:201], v[54:57]
	v_mfma_i32_16x16x64_i8 v[46:49], v[134:137], v[198:201], v[46:49]
	v_mfma_i32_16x16x64_i8 v[30:33], v[134:137], v[206:209], v[30:33]
	v_mfma_i32_16x16x64_i8 v[38:41], v[130:133], v[206:209], v[38:41]
	v_mfma_i32_16x16x64_i8 v[22:25], v[130:133], v[214:217], v[22:25]
	v_mfma_i32_16x16x64_i8 v[14:17], v[134:137], v[214:217], v[14:17]
	v_mfma_i32_16x16x64_i8 v[2:5], v[134:137], v[222:225], v[2:5]
	v_mfma_i32_16x16x64_i8 v[6:9], v[130:133], v[222:225], v[6:9]
	s_setprio 0
	s_barrier
	s_add_i32 s66, 0, 0x18000
	s_add_i32 s67, 0, 0x1c000
	v_add_u32_e32 v142, s66, v190
	v_add_u32_e32 v158, s67, v190
	ds_read_b128 v[130:133], v142
	ds_read_b128 v[134:137], v142 offset:1024
	ds_read_b128 v[138:141], v142 offset:2048
	ds_read_b128 v[142:145], v142 offset:3072
	ds_read_b128 v[146:149], v158
	ds_read_b128 v[150:153], v158 offset:1024
	ds_read_b128 v[154:157], v158 offset:2048
	ds_read_b128 v[158:161], v158 offset:3072
	s_add_u32 s0, s38, 0x80000
	s_addc_u32 s1, s39, 0
	s_mov_b32 m0, s42
	ds_read_b128 v[194:197], v193 offset:32768
	ds_read_b128 v[198:201], v193 offset:33792
	ds_read_b128 v[202:205], v193 offset:34816
	ds_read_b128 v[206:209], v193 offset:35840
	ds_read_b128 v[210:213], v193 offset:36864
	ds_read_b128 v[214:217], v193 offset:37888
	ds_read_b128 v[218:221], v193 offset:38912
	ds_read_b128 v[222:225], v193 offset:39936
	global_load_lds_dwordx4 v162, s[0:1]
	s_mov_b32 m0, s43
	s_nop 0
	global_load_lds_dwordx4 v166, s[0:1]
	s_waitcnt vmcnt(8) lgkmcnt(0)
	s_barrier
	s_setprio 1
	v_mfma_i32_16x16x64_i8 v[126:129], v[130:133], v[194:197], v[126:129]
	v_mfma_i32_16x16x64_i8 v[122:125], v[138:141], v[194:197], v[122:125]
	v_mfma_i32_16x16x64_i8 v[106:109], v[138:141], v[202:205], v[106:109]
	v_mfma_i32_16x16x64_i8 v[114:117], v[130:133], v[202:205], v[114:117]
	v_mfma_i32_16x16x64_i8 v[98:101], v[130:133], v[210:213], v[98:101]
	v_mfma_i32_16x16x64_i8 v[90:93], v[138:141], v[210:213], v[90:93]
	v_mfma_i32_16x16x64_i8 v[74:77], v[138:141], v[218:221], v[74:77]
	v_mfma_i32_16x16x64_i8 v[82:85], v[130:133], v[218:221], v[82:85]
	s_nop 0
	v_mfma_i32_16x16x64_i8 v[126:129], v[134:137], v[198:201], v[126:129]
	v_mfma_i32_16x16x64_i8 v[122:125], v[142:145], v[198:201], v[122:125]
	v_mfma_i32_16x16x64_i8 v[106:109], v[142:145], v[206:209], v[106:109]
	v_mfma_i32_16x16x64_i8 v[114:117], v[134:137], v[206:209], v[114:117]
	v_mfma_i32_16x16x64_i8 v[98:101], v[134:137], v[214:217], v[98:101]
	v_mfma_i32_16x16x64_i8 v[90:93], v[142:145], v[214:217], v[90:93]
	v_mfma_i32_16x16x64_i8 v[74:77], v[142:145], v[222:225], v[74:77]
	v_mfma_i32_16x16x64_i8 v[82:85], v[134:137], v[222:225], v[82:85]
	v_mfma_i32_16x16x64_i8 v[118:121], v[146:149], v[194:197], v[118:121]
	v_mfma_i32_16x16x64_i8 v[110:113], v[154:157], v[194:197], v[110:113]
	v_mfma_i32_16x16x64_i8 v[94:97], v[154:157], v[202:205], v[94:97]
	v_mfma_i32_16x16x64_i8 v[102:105], v[146:149], v[202:205], v[102:105]
	v_mfma_i32_16x16x64_i8 v[86:89], v[146:149], v[210:213], v[86:89]
	v_mfma_i32_16x16x64_i8 v[78:81], v[154:157], v[210:213], v[78:81]
	v_mfma_i32_16x16x64_i8 v[66:69], v[154:157], v[218:221], v[66:69]
	v_mfma_i32_16x16x64_i8 v[70:73], v[146:149], v[218:221], v[70:73]
	s_nop 0
	v_mfma_i32_16x16x64_i8 v[118:121], v[150:153], v[198:201], v[118:121]
	v_mfma_i32_16x16x64_i8 v[110:113], v[158:161], v[198:201], v[110:113]
	v_mfma_i32_16x16x64_i8 v[94:97], v[158:161], v[206:209], v[94:97]
	v_mfma_i32_16x16x64_i8 v[102:105], v[150:153], v[206:209], v[102:105]
	v_mfma_i32_16x16x64_i8 v[86:89], v[150:153], v[214:217], v[86:89]
	v_mfma_i32_16x16x64_i8 v[78:81], v[158:161], v[214:217], v[78:81]
	v_mfma_i32_16x16x64_i8 v[66:69], v[158:161], v[222:225], v[66:69]
	v_mfma_i32_16x16x64_i8 v[70:73], v[150:153], v[222:225], v[70:73]
	s_setprio 0
	s_barrier
	s_add_i32 s0, s66, s40
	s_mov_b32 m0, s0
	s_add_u32 s98, s36, 0x80
	s_addc_u32 s99, s37, 0
	s_add_u32 s100, s38, 0x80
	s_addc_u32 s101, s39, 0
	ds_read_b128 v[194:197], v193 offset:49152
	ds_read_b128 v[198:201], v193 offset:50176
	ds_read_b128 v[202:205], v193 offset:51200
	ds_read_b128 v[206:209], v193 offset:52224
	ds_read_b128 v[210:213], v193 offset:53248
	ds_read_b128 v[214:217], v193 offset:54272
	ds_read_b128 v[218:221], v193 offset:55296
	ds_read_b128 v[222:225], v193 offset:56320
	global_load_lds_dwordx4 v164, s[98:99]
	s_add_i32 m0, s0, 0x2000
	s_add_u32 s0, s36, 0x80080
	s_addc_u32 s1, s37, 0
	s_add_i32 s36, s67, s40
	global_load_lds_dwordx4 v168, s[98:99]
	s_mov_b32 m0, s36
	s_nop 0
	global_load_lds_dwordx4 v164, s[0:1]
	s_add_i32 m0, s36, 0x2000
	s_nop 0
	global_load_lds_dwordx4 v168, s[0:1]
	s_mov_b32 m0, s48
	s_nop 0
	global_load_lds_dwordx4 v162, s[100:101]
	s_mov_b32 m0, s49
	s_nop 0
	global_load_lds_dwordx4 v166, s[100:101]
	s_waitcnt vmcnt(8) lgkmcnt(0)
	s_barrier
	s_setprio 1
	v_mfma_i32_16x16x64_i8 v[62:65], v[130:133], v[194:197], v[62:65]
	v_mfma_i32_16x16x64_i8 v[58:61], v[138:141], v[194:197], v[58:61]
	v_mfma_i32_16x16x64_i8 v[42:45], v[138:141], v[202:205], v[42:45]
	v_mfma_i32_16x16x64_i8 v[50:53], v[130:133], v[202:205], v[50:53]
	v_mfma_i32_16x16x64_i8 v[34:37], v[130:133], v[210:213], v[34:37]
	v_mfma_i32_16x16x64_i8 v[26:29], v[138:141], v[210:213], v[26:29]
	v_mfma_i32_16x16x64_i8 v[10:13], v[138:141], v[218:221], v[10:13]
	v_mfma_i32_16x16x64_i8 v[18:21], v[130:133], v[218:221], v[18:21]
	s_nop 0
	v_mfma_i32_16x16x64_i8 v[62:65], v[134:137], v[198:201], v[62:65]
	v_mfma_i32_16x16x64_i8 v[58:61], v[142:145], v[198:201], v[58:61]
	v_mfma_i32_16x16x64_i8 v[42:45], v[142:145], v[206:209], v[42:45]
	v_mfma_i32_16x16x64_i8 v[50:53], v[134:137], v[206:209], v[50:53]
	v_mfma_i32_16x16x64_i8 v[34:37], v[134:137], v[214:217], v[34:37]
	v_mfma_i32_16x16x64_i8 v[26:29], v[142:145], v[214:217], v[26:29]
	v_mfma_i32_16x16x64_i8 v[10:13], v[142:145], v[222:225], v[10:13]
	v_mfma_i32_16x16x64_i8 v[18:21], v[134:137], v[222:225], v[18:21]
	v_mfma_i32_16x16x64_i8 v[54:57], v[146:149], v[194:197], v[54:57]
	v_mfma_i32_16x16x64_i8 v[46:49], v[154:157], v[194:197], v[46:49]
	v_mfma_i32_16x16x64_i8 v[30:33], v[154:157], v[202:205], v[30:33]
	v_mfma_i32_16x16x64_i8 v[38:41], v[146:149], v[202:205], v[38:41]
	v_mfma_i32_16x16x64_i8 v[22:25], v[146:149], v[210:213], v[22:25]
	v_mfma_i32_16x16x64_i8 v[14:17], v[154:157], v[210:213], v[14:17]
	v_mfma_i32_16x16x64_i8 v[2:5], v[154:157], v[218:221], v[2:5]
	v_mfma_i32_16x16x64_i8 v[6:9], v[146:149], v[218:221], v[6:9]
	s_nop 0
	v_mfma_i32_16x16x64_i8 v[54:57], v[150:153], v[198:201], v[54:57]
	v_mfma_i32_16x16x64_i8 v[46:49], v[158:161], v[198:201], v[46:49]
	v_mfma_i32_16x16x64_i8 v[30:33], v[158:161], v[206:209], v[30:33]
	v_mfma_i32_16x16x64_i8 v[38:41], v[150:153], v[206:209], v[38:41]
	v_mfma_i32_16x16x64_i8 v[22:25], v[150:153], v[214:217], v[22:25]
	v_mfma_i32_16x16x64_i8 v[14:17], v[158:161], v[214:217], v[14:17]
	v_mfma_i32_16x16x64_i8 v[2:5], v[158:161], v[222:225], v[2:5]
	v_mfma_i32_16x16x64_i8 v[6:9], v[150:153], v[222:225], v[6:9]
	s_setprio 0
	s_barrier
	s_add_i32 s64, s64, 2
	s_add_u32 s34, s34, 0x100
	s_addc_u32 s35, s35, 0
	s_add_u32 s62, s62, 0x100
	s_addc_u32 s63, s63, 0
	s_cmp_gt_u32 s64, 29
	s_cbranch_scc1 .LBB0_791

.LBB0_1051:
	s_add_u32 s8, s17, s6
	s_addc_u32 s9, s48, s7
	s_add_u32 s8, s8, 0x32800100
	s_addc_u32 s9, s9, 0
	s_add_u32 s65, s49, s6
	s_addc_u32 s68, s50, s7
	s_add_i32 s69, 0, 0x10000
	s_cmpk_eq_i32 s6, 0xf00
	s_cselect_b32 s41, s5, s9
	s_cselect_b32 s40, s4, s8
	s_cselect_b32 s9, s21, s68
	s_cselect_b32 s8, s20, s65
	s_add_i32 s65, 0, 0x14000
	v_add_u32_e32 v130, s69, v187
	v_add_u32_e32 v134, s65, v187
	ds_read_b128 v[158:161], v130
	ds_read_b128 v[150:153], v130 offset:1024
	ds_read_b128 v[154:157], v130 offset:2048
	ds_read_b128 v[146:149], v130 offset:3072
	ds_read_b128 v[142:145], v134
	ds_read_b128 v[130:133], v134 offset:1024
	ds_read_b128 v[138:141], v134 offset:2048
	ds_read_b128 v[134:137], v134 offset:3072
	v_lshl_add_u64 v[214:215], v[168:169], 0, s[6:7]
	s_add_i32 m0, s43, 0xc000
	ds_read_b128 v[172:175], v188
	ds_read_b128 v[176:179], v188 offset:1024
	ds_read_b128 v[190:193], v188 offset:2048
	ds_read_b128 v[194:197], v188 offset:3072
	ds_read_b128 v[198:201], v188 offset:4096
	ds_read_b128 v[202:205], v188 offset:5120
	ds_read_b128 v[206:209], v188 offset:6144
	ds_read_b128 v[210:213], v188 offset:7168
	global_load_lds_dwordx4 v[214:215], off
	v_lshl_add_u64 v[214:215], v[170:171], 0, s[6:7]
	s_add_i32 m0, s43, 0xe000
	s_nop 0
	global_load_lds_dwordx4 v[214:215], off
	s_waitcnt vmcnt(8) lgkmcnt(0)
	s_barrier
	s_setprio 1
	v_mfma_i32_16x16x64_i8 v[70:73], v[158:161], v[172:175], v[70:73]
	v_mfma_i32_16x16x64_i8 v[34:37], v[154:157], v[172:175], v[34:37]
	v_mfma_i32_16x16x64_i8 v[54:57], v[154:157], v[190:193], v[54:57]
	v_mfma_i32_16x16x64_i8 v[102:105], v[158:161], v[190:193], v[102:105]
	v_mfma_i32_16x16x64_i8 v[114:117], v[158:161], v[198:201], v[114:117]
	v_mfma_i32_16x16x64_i8 v[86:89], v[154:157], v[198:201], v[86:89]
	v_mfma_i32_16x16x64_i8 v[110:113], v[154:157], v[206:209], v[110:113]
	v_mfma_i32_16x16x64_i8 v[126:129], v[158:161], v[206:209], v[126:129]
	s_nop 0
	v_mfma_i32_16x16x64_i8 v[70:73], v[150:153], v[176:179], v[70:73]
	v_mfma_i32_16x16x64_i8 v[34:37], v[146:149], v[176:179], v[34:37]
	v_mfma_i32_16x16x64_i8 v[54:57], v[146:149], v[194:197], v[54:57]
	v_mfma_i32_16x16x64_i8 v[102:105], v[150:153], v[194:197], v[102:105]
	v_mfma_i32_16x16x64_i8 v[114:117], v[150:153], v[202:205], v[114:117]
	v_mfma_i32_16x16x64_i8 v[86:89], v[146:149], v[202:205], v[86:89]
	v_mfma_i32_16x16x64_i8 v[110:113], v[146:149], v[210:213], v[110:113]
	v_mfma_i32_16x16x64_i8 v[126:129], v[150:153], v[210:213], v[126:129]
	v_mfma_i32_16x16x64_i8 v[18:21], v[142:145], v[172:175], v[18:21]
	v_mfma_i32_16x16x64_i8 v[2:5], v[138:141], v[172:175], v[2:5]
	v_mfma_i32_16x16x64_i8 v[6:9], v[138:141], v[190:193], v[6:9]
	v_mfma_i32_16x16x64_i8 v[38:41], v[142:145], v[190:193], v[38:41]
	v_mfma_i32_16x16x64_i8 v[66:69], v[142:145], v[198:201], v[66:69]
	v_mfma_i32_16x16x64_i8 v[26:29], v[138:141], v[198:201], v[26:29]
	v_mfma_i32_16x16x64_i8 v[50:53], v[138:141], v[206:209], v[50:53]
	v_mfma_i32_16x16x64_i8 v[90:93], v[142:145], v[206:209], v[90:93]
	s_nop 0
	v_mfma_i32_16x16x64_i8 v[18:21], v[130:133], v[176:179], v[18:21]
	v_mfma_i32_16x16x64_i8 v[2:5], v[134:137], v[176:179], v[2:5]
	v_mfma_i32_16x16x64_i8 v[6:9], v[134:137], v[194:197], v[6:9]
	v_mfma_i32_16x16x64_i8 v[38:41], v[130:133], v[194:197], v[38:41]
	v_mfma_i32_16x16x64_i8 v[66:69], v[130:133], v[202:205], v[66:69]
	v_mfma_i32_16x16x64_i8 v[26:29], v[134:137], v[202:205], v[26:29]
	v_mfma_i32_16x16x64_i8 v[50:53], v[134:137], v[210:213], v[50:53]
	v_mfma_i32_16x16x64_i8 v[90:93], v[130:133], v[210:213], v[90:93]
	s_setprio 0
	s_barrier
	s_add_i32 s68, s69, s42
	s_mov_b32 m0, s68
	ds_read_b128 v[190:193], v188 offset:16384
	ds_read_b128 v[194:197], v188 offset:17408
	ds_read_b128 v[198:201], v188 offset:18432
	ds_read_b128 v[202:205], v188 offset:19456
	ds_read_b128 v[206:209], v188 offset:20480
	ds_read_b128 v[210:213], v188 offset:21504
	ds_read_b128 v[214:217], v188 offset:22528
	ds_read_b128 v[218:221], v188 offset:23552
	global_load_lds_dwordx4 v162, s[8:9]
	s_add_i32 m0, s68, 0x2000
	s_add_u32 s68, s8, 0x80000
	s_addc_u32 s69, s9, 0
	s_add_i32 s65, s65, s42
	global_load_lds_dwordx4 v166, s[8:9]
	s_mov_b32 m0, s65
	s_nop 0
	global_load_lds_dwordx4 v162, s[68:69]
	s_add_i32 m0, s65, 0x2000
	s_nop 0
	global_load_lds_dwordx4 v166, s[68:69]
	s_mov_b32 m0, s43
	s_nop 0
	global_load_lds_dwordx4 v162, s[40:41]
	s_mov_b32 m0, s60
	s_nop 0
	global_load_lds_dwordx4 v166, s[40:41]
	s_waitcnt vmcnt(8) lgkmcnt(0)
	s_barrier
	s_setprio 1
	v_mfma_i32_16x16x64_i8 v[122:125], v[158:161], v[190:193], v[122:125]
	v_mfma_i32_16x16x64_i8 v[118:121], v[154:157], v[190:193], v[118:121]
	v_mfma_i32_16x16x64_i8 v[94:97], v[154:157], v[198:201], v[94:97]
	v_mfma_i32_16x16x64_i8 v[98:101], v[158:161], v[198:201], v[98:101]
	v_mfma_i32_16x16x64_i8 v[62:65], v[158:161], v[206:209], v[62:65]
	v_mfma_i32_16x16x64_i8 v[58:61], v[154:157], v[206:209], v[58:61]
	v_mfma_i32_16x16x64_i8 v[22:25], v[154:157], v[214:217], v[22:25]
	v_mfma_i32_16x16x64_i8 v[30:33], v[158:161], v[214:217], v[30:33]
	s_nop 0
	v_mfma_i32_16x16x64_i8 v[122:125], v[150:153], v[194:197], v[122:125]
	v_mfma_i32_16x16x64_i8 v[118:121], v[146:149], v[194:197], v[118:121]
	v_mfma_i32_16x16x64_i8 v[94:97], v[146:149], v[202:205], v[94:97]
	v_mfma_i32_16x16x64_i8 v[98:101], v[150:153], v[202:205], v[98:101]
	v_mfma_i32_16x16x64_i8 v[62:65], v[150:153], v[210:213], v[62:65]
	v_mfma_i32_16x16x64_i8 v[58:61], v[146:149], v[210:213], v[58:61]
	v_mfma_i32_16x16x64_i8 v[22:25], v[146:149], v[218:221], v[22:25]
	v_mfma_i32_16x16x64_i8 v[30:33], v[150:153], v[218:221], v[30:33]
	v_mfma_i32_16x16x64_i8 v[106:109], v[142:145], v[190:193], v[106:109]
	v_mfma_i32_16x16x64_i8 v[82:85], v[138:141], v[190:193], v[82:85]
	v_mfma_i32_16x16x64_i8 v[74:77], v[138:141], v[198:201], v[74:77]
	v_mfma_i32_16x16x64_i8 v[78:81], v[142:145], v[198:201], v[78:81]
	v_mfma_i32_16x16x64_i8 v[46:49], v[142:145], v[206:209], v[46:49]
	v_mfma_i32_16x16x64_i8 v[42:45], v[138:141], v[206:209], v[42:45]
	v_mfma_i32_16x16x64_i8 v[10:13], v[138:141], v[214:217], v[10:13]
	v_mfma_i32_16x16x64_i8 v[14:17], v[142:145], v[214:217], v[14:17]
	s_nop 0
	v_mfma_i32_16x16x64_i8 v[106:109], v[130:133], v[194:197], v[106:109]
	v_mfma_i32_16x16x64_i8 v[82:85], v[134:137], v[194:197], v[82:85]
	v_mfma_i32_16x16x64_i8 v[74:77], v[134:137], v[202:205], v[74:77]
	v_mfma_i32_16x16x64_i8 v[78:81], v[130:133], v[202:205], v[78:81]
	v_mfma_i32_16x16x64_i8 v[46:49], v[130:133], v[210:213], v[46:49]
	v_mfma_i32_16x16x64_i8 v[42:45], v[134:137], v[210:213], v[42:45]
	v_mfma_i32_16x16x64_i8 v[10:13], v[134:137], v[218:221], v[10:13]
	v_mfma_i32_16x16x64_i8 v[14:17], v[130:133], v[218:221], v[14:17]
	s_setprio 0
	s_barrier
	s_add_i32 s65, 0, 0x18000
	s_add_i32 s68, 0, 0x1c000
	v_add_u32_e32 v142, s65, v187
	v_add_u32_e32 v158, s68, v187
	ds_read_b128 v[130:133], v142
	ds_read_b128 v[134:137], v142 offset:1024
	ds_read_b128 v[138:141], v142 offset:2048
	ds_read_b128 v[142:145], v142 offset:3072
	ds_read_b128 v[146:149], v158
	ds_read_b128 v[150:153], v158 offset:1024
	ds_read_b128 v[154:157], v158 offset:2048
	ds_read_b128 v[158:161], v158 offset:3072
	s_add_u32 s40, s40, 0x80000
	s_addc_u32 s41, s41, 0
	s_add_u32 s100, s40, 0xfff80080
	s_addc_u32 s101, s41, -1
	s_mov_b32 m0, s61
	ds_read_b128 v[190:193], v188 offset:32768
	ds_read_b128 v[194:197], v188 offset:33792
	ds_read_b128 v[198:201], v188 offset:34816
	ds_read_b128 v[202:205], v188 offset:35840
	ds_read_b128 v[206:209], v188 offset:36864
	ds_read_b128 v[210:213], v188 offset:37888
	ds_read_b128 v[214:217], v188 offset:38912
	ds_read_b128 v[218:221], v188 offset:39936
	global_load_lds_dwordx4 v162, s[40:41]
	s_mov_b32 m0, s62
	s_nop 0
	global_load_lds_dwordx4 v166, s[40:41]
	s_waitcnt vmcnt(8) lgkmcnt(0)
	s_barrier
	s_setprio 1
	v_mfma_i32_16x16x64_i8 v[70:73], v[130:133], v[190:193], v[70:73]
	v_mfma_i32_16x16x64_i8 v[34:37], v[138:141], v[190:193], v[34:37]
	v_mfma_i32_16x16x64_i8 v[54:57], v[138:141], v[198:201], v[54:57]
	v_mfma_i32_16x16x64_i8 v[102:105], v[130:133], v[198:201], v[102:105]
	v_mfma_i32_16x16x64_i8 v[114:117], v[130:133], v[206:209], v[114:117]
	v_mfma_i32_16x16x64_i8 v[86:89], v[138:141], v[206:209], v[86:89]
	v_mfma_i32_16x16x64_i8 v[110:113], v[138:141], v[214:217], v[110:113]
	v_mfma_i32_16x16x64_i8 v[126:129], v[130:133], v[214:217], v[126:129]
	s_nop 0
	v_mfma_i32_16x16x64_i8 v[70:73], v[134:137], v[194:197], v[70:73]
	v_mfma_i32_16x16x64_i8 v[34:37], v[142:145], v[194:197], v[34:37]
	v_mfma_i32_16x16x64_i8 v[54:57], v[142:145], v[202:205], v[54:57]
	v_mfma_i32_16x16x64_i8 v[102:105], v[134:137], v[202:205], v[102:105]
	v_mfma_i32_16x16x64_i8 v[114:117], v[134:137], v[210:213], v[114:117]
	v_mfma_i32_16x16x64_i8 v[86:89], v[142:145], v[210:213], v[86:89]
	v_mfma_i32_16x16x64_i8 v[110:113], v[142:145], v[218:221], v[110:113]
	v_mfma_i32_16x16x64_i8 v[126:129], v[134:137], v[218:221], v[126:129]
	v_mfma_i32_16x16x64_i8 v[18:21], v[146:149], v[190:193], v[18:21]
	v_mfma_i32_16x16x64_i8 v[2:5], v[154:157], v[190:193], v[2:5]
	v_mfma_i32_16x16x64_i8 v[6:9], v[154:157], v[198:201], v[6:9]
	v_mfma_i32_16x16x64_i8 v[38:41], v[146:149], v[198:201], v[38:41]
	v_mfma_i32_16x16x64_i8 v[66:69], v[146:149], v[206:209], v[66:69]
	v_mfma_i32_16x16x64_i8 v[26:29], v[154:157], v[206:209], v[26:29]
	v_mfma_i32_16x16x64_i8 v[50:53], v[154:157], v[214:217], v[50:53]
	v_mfma_i32_16x16x64_i8 v[90:93], v[146:149], v[214:217], v[90:93]
	s_nop 0
	v_mfma_i32_16x16x64_i8 v[18:21], v[150:153], v[194:197], v[18:21]
	v_mfma_i32_16x16x64_i8 v[2:5], v[158:161], v[194:197], v[2:5]
	v_mfma_i32_16x16x64_i8 v[6:9], v[158:161], v[202:205], v[6:9]
	v_mfma_i32_16x16x64_i8 v[38:41], v[150:153], v[202:205], v[38:41]
	v_mfma_i32_16x16x64_i8 v[66:69], v[150:153], v[210:213], v[66:69]
	v_mfma_i32_16x16x64_i8 v[26:29], v[158:161], v[210:213], v[26:29]
	v_mfma_i32_16x16x64_i8 v[50:53], v[158:161], v[218:221], v[50:53]
	v_mfma_i32_16x16x64_i8 v[90:93], v[150:153], v[218:221], v[90:93]
	s_setprio 0
	s_barrier
	s_add_i32 s40, s65, s42
	s_mov_b32 m0, s40
	s_add_u32 s98, s8, 0x80
	s_addc_u32 s99, s9, 0
	ds_read_b128 v[190:193], v188 offset:49152
	ds_read_b128 v[194:197], v188 offset:50176
	ds_read_b128 v[198:201], v188 offset:51200
	ds_read_b128 v[202:205], v188 offset:52224
	ds_read_b128 v[206:209], v188 offset:53248
	ds_read_b128 v[210:213], v188 offset:54272
	ds_read_b128 v[214:217], v188 offset:55296
	ds_read_b128 v[218:221], v188 offset:56320
	global_load_lds_dwordx4 v162, s[98:99]
	s_add_i32 m0, s40, 0x2000
	s_add_u32 s8, s8, 0x80080
	s_addc_u32 s9, s9, 0
	s_add_i32 s40, s68, s42
	global_load_lds_dwordx4 v166, s[98:99]
	s_mov_b32 m0, s40
	s_nop 0
	global_load_lds_dwordx4 v162, s[8:9]
	s_add_i32 m0, s40, 0x2000
	s_nop 0
	global_load_lds_dwordx4 v166, s[8:9]
	s_mov_b32 m0, s66
	s_nop 0
	global_load_lds_dwordx4 v162, s[100:101]
	s_mov_b32 m0, s67
	s_nop 0
	global_load_lds_dwordx4 v166, s[100:101]
	s_waitcnt vmcnt(8) lgkmcnt(0)
	s_barrier
	s_setprio 1
	v_mfma_i32_16x16x64_i8 v[122:125], v[130:133], v[190:193], v[122:125]
	v_mfma_i32_16x16x64_i8 v[118:121], v[138:141], v[190:193], v[118:121]
	v_mfma_i32_16x16x64_i8 v[94:97], v[138:141], v[198:201], v[94:97]
	v_mfma_i32_16x16x64_i8 v[98:101], v[130:133], v[198:201], v[98:101]
	v_mfma_i32_16x16x64_i8 v[62:65], v[130:133], v[206:209], v[62:65]
	v_mfma_i32_16x16x64_i8 v[58:61], v[138:141], v[206:209], v[58:61]
	v_mfma_i32_16x16x64_i8 v[22:25], v[138:141], v[214:217], v[22:25]
	v_mfma_i32_16x16x64_i8 v[30:33], v[130:133], v[214:217], v[30:33]
	s_nop 0
	v_mfma_i32_16x16x64_i8 v[122:125], v[134:137], v[194:197], v[122:125]
	v_mfma_i32_16x16x64_i8 v[118:121], v[142:145], v[194:197], v[118:121]
	v_mfma_i32_16x16x64_i8 v[94:97], v[142:145], v[202:205], v[94:97]
	v_mfma_i32_16x16x64_i8 v[98:101], v[134:137], v[202:205], v[98:101]
	v_mfma_i32_16x16x64_i8 v[62:65], v[134:137], v[210:213], v[62:65]
	v_mfma_i32_16x16x64_i8 v[58:61], v[142:145], v[210:213], v[58:61]
	v_mfma_i32_16x16x64_i8 v[22:25], v[142:145], v[218:221], v[22:25]
	v_mfma_i32_16x16x64_i8 v[30:33], v[134:137], v[218:221], v[30:33]
	v_mfma_i32_16x16x64_i8 v[106:109], v[146:149], v[190:193], v[106:109]
	v_mfma_i32_16x16x64_i8 v[82:85], v[154:157], v[190:193], v[82:85]
	v_mfma_i32_16x16x64_i8 v[74:77], v[154:157], v[198:201], v[74:77]
	v_mfma_i32_16x16x64_i8 v[78:81], v[146:149], v[198:201], v[78:81]
	v_mfma_i32_16x16x64_i8 v[46:49], v[146:149], v[206:209], v[46:49]
	v_mfma_i32_16x16x64_i8 v[42:45], v[154:157], v[206:209], v[42:45]
	v_mfma_i32_16x16x64_i8 v[10:13], v[154:157], v[214:217], v[10:13]
	v_mfma_i32_16x16x64_i8 v[14:17], v[146:149], v[214:217], v[14:17]
	s_nop 0
	v_mfma_i32_16x16x64_i8 v[106:109], v[150:153], v[194:197], v[106:109]
	v_mfma_i32_16x16x64_i8 v[82:85], v[158:161], v[194:197], v[82:85]
	v_mfma_i32_16x16x64_i8 v[74:77], v[158:161], v[202:205], v[74:77]
	v_mfma_i32_16x16x64_i8 v[78:81], v[150:153], v[202:205], v[78:81]
	v_mfma_i32_16x16x64_i8 v[46:49], v[150:153], v[210:213], v[46:49]
	v_mfma_i32_16x16x64_i8 v[42:45], v[158:161], v[210:213], v[42:45]
	v_mfma_i32_16x16x64_i8 v[10:13], v[158:161], v[218:221], v[10:13]
	v_mfma_i32_16x16x64_i8 v[14:17], v[150:153], v[218:221], v[14:17]
	s_setprio 0
	s_barrier
	s_add_i32 s64, s64, 2
	s_add_u32 s6, s6, 0x100
	s_addc_u32 s7, s7, 0
	s_cmp_gt_u32 s64, 29
	s_cbranch_scc0 .LBB0_1051
	s_waitcnt vmcnt(0)
	s_cmpk_lt_u32 s59, 0x100
	s_cbranch_scc0 .LBB0_1054
	s_barrier

.LBB0_1173:
	ds_read_b128 v[158:161], v184
	ds_read_b128 v[150:153], v184 offset:1024
	ds_read_b128 v[154:157], v184 offset:2048
	ds_read_b128 v[146:149], v184 offset:3072
	ds_read_b128 v[142:145], v185
	ds_read_b128 v[130:133], v185 offset:1024
	ds_read_b128 v[138:141], v185 offset:2048
	ds_read_b128 v[134:137], v185 offset:3072
	s_add_u32 s38, s36, 0xfff80080
	s_addc_u32 s39, s37, -1
	s_cmp_eq_u32 s65, 28
	s_cselect_b32 s41, s18, s39
	s_cselect_b32 s40, s19, s38
	s_cselect_b32 s39, s25, s64
	s_cselect_b32 s38, s27, s63
	v_lshl_add_u64 v[212:213], s[36:37], 0, v[166:167]
	s_add_i32 m0, s35, 0xc000
	ds_read_b128 v[174:177], v186
	ds_read_b128 v[178:181], v186 offset:1024
	ds_read_b128 v[188:191], v186 offset:2048
	ds_read_b128 v[192:195], v186 offset:3072
	ds_read_b128 v[196:199], v186 offset:4096
	ds_read_b128 v[200:203], v186 offset:5120
	ds_read_b128 v[204:207], v186 offset:6144
	ds_read_b128 v[208:211], v186 offset:7168
	global_load_lds_dwordx4 v[212:213], off
	v_lshl_add_u64 v[212:213], s[36:37], 0, v[168:169]
	s_add_i32 m0, s35, 0xe000
	s_nop 0
	global_load_lds_dwordx4 v[212:213], off
	s_waitcnt vmcnt(8) lgkmcnt(0)
	s_barrier
	s_setprio 1
	v_mfma_i32_16x16x64_i8 v[126:129], v[158:161], v[174:177], v[126:129]
	v_mfma_i32_16x16x64_i8 v[122:125], v[154:157], v[174:177], v[122:125]
	v_mfma_i32_16x16x64_i8 v[106:109], v[154:157], v[188:191], v[106:109]
	v_mfma_i32_16x16x64_i8 v[110:113], v[158:161], v[188:191], v[110:113]
	v_mfma_i32_16x16x64_i8 v[94:97], v[158:161], v[196:199], v[94:97]
	v_mfma_i32_16x16x64_i8 v[90:93], v[154:157], v[196:199], v[90:93]
	v_mfma_i32_16x16x64_i8 v[74:77], v[154:157], v[204:207], v[74:77]
	v_mfma_i32_16x16x64_i8 v[78:81], v[158:161], v[204:207], v[78:81]
	s_nop 0
	v_mfma_i32_16x16x64_i8 v[126:129], v[150:153], v[178:181], v[126:129]
	v_mfma_i32_16x16x64_i8 v[122:125], v[146:149], v[178:181], v[122:125]
	v_mfma_i32_16x16x64_i8 v[106:109], v[146:149], v[192:195], v[106:109]
	v_mfma_i32_16x16x64_i8 v[110:113], v[150:153], v[192:195], v[110:113]
	v_mfma_i32_16x16x64_i8 v[94:97], v[150:153], v[200:203], v[94:97]
	v_mfma_i32_16x16x64_i8 v[90:93], v[146:149], v[200:203], v[90:93]
	v_mfma_i32_16x16x64_i8 v[74:77], v[146:149], v[208:211], v[74:77]
	v_mfma_i32_16x16x64_i8 v[78:81], v[150:153], v[208:211], v[78:81]
	v_mfma_i32_16x16x64_i8 v[118:121], v[142:145], v[174:177], v[118:121]
	v_mfma_i32_16x16x64_i8 v[114:117], v[138:141], v[174:177], v[114:117]
	v_mfma_i32_16x16x64_i8 v[98:101], v[138:141], v[188:191], v[98:101]
	v_mfma_i32_16x16x64_i8 v[102:105], v[142:145], v[188:191], v[102:105]
	v_mfma_i32_16x16x64_i8 v[86:89], v[142:145], v[196:199], v[86:89]
	v_mfma_i32_16x16x64_i8 v[82:85], v[138:141], v[196:199], v[82:85]
	v_mfma_i32_16x16x64_i8 v[66:69], v[138:141], v[204:207], v[66:69]
	v_mfma_i32_16x16x64_i8 v[70:73], v[142:145], v[204:207], v[70:73]
	s_nop 0
	v_mfma_i32_16x16x64_i8 v[118:121], v[130:133], v[178:181], v[118:121]
	v_mfma_i32_16x16x64_i8 v[114:117], v[134:137], v[178:181], v[114:117]
	v_mfma_i32_16x16x64_i8 v[98:101], v[134:137], v[192:195], v[98:101]
	v_mfma_i32_16x16x64_i8 v[102:105], v[130:133], v[192:195], v[102:105]
	v_mfma_i32_16x16x64_i8 v[86:89], v[130:133], v[200:203], v[86:89]
	v_mfma_i32_16x16x64_i8 v[82:85], v[134:137], v[200:203], v[82:85]
	v_mfma_i32_16x16x64_i8 v[66:69], v[134:137], v[208:211], v[66:69]
	v_mfma_i32_16x16x64_i8 v[70:73], v[130:133], v[208:211], v[70:73]
	s_setprio 0
	s_barrier
	s_add_i32 s66, s51, s3
	v_lshl_add_u64 v[174:175], s[38:39], 0, v[164:165]
	s_mov_b32 m0, s66
	ds_read_b128 v[188:191], v186 offset:16384
	ds_read_b128 v[192:195], v186 offset:17408
	ds_read_b128 v[196:199], v186 offset:18432
	ds_read_b128 v[200:203], v186 offset:19456
	ds_read_b128 v[204:207], v186 offset:20480
	ds_read_b128 v[208:211], v186 offset:21504
	ds_read_b128 v[212:215], v186 offset:22528
	ds_read_b128 v[216:219], v186 offset:23552
	global_load_lds_dwordx4 v[174:175], off
	s_add_i32 m0, s66, 0x2000
	s_add_u32 s66, s38, 0x80000
	v_lshl_add_u64 v[176:177], s[38:39], 0, v[162:163]
	s_addc_u32 s67, s39, 0
	s_add_i32 s68, s58, s3
	global_load_lds_dwordx4 v[176:177], off
	v_lshl_add_u64 v[178:179], s[66:67], 0, v[164:165]
	s_mov_b32 m0, s68
	v_lshl_add_u64 v[180:181], s[40:41], 0, v[162:163]
	global_load_lds_dwordx4 v[178:179], off
	v_lshl_add_u64 v[178:179], s[66:67], 0, v[162:163]
	s_add_i32 m0, s68, 0x2000
	s_nop 0
	global_load_lds_dwordx4 v[178:179], off
	v_lshl_add_u64 v[178:179], s[40:41], 0, v[164:165]
	s_mov_b32 m0, s35
	s_nop 0
	global_load_lds_dwordx4 v[178:179], off
	s_mov_b32 m0, s42
	s_nop 0
	global_load_lds_dwordx4 v[180:181], off
	s_waitcnt vmcnt(8) lgkmcnt(0)
	s_barrier
	s_setprio 1
	v_mfma_i32_16x16x64_i8 v[62:65], v[158:161], v[188:191], v[62:65]
	v_mfma_i32_16x16x64_i8 v[58:61], v[154:157], v[188:191], v[58:61]
	v_mfma_i32_16x16x64_i8 v[42:45], v[154:157], v[196:199], v[42:45]
	v_mfma_i32_16x16x64_i8 v[46:49], v[158:161], v[196:199], v[46:49]
	v_mfma_i32_16x16x64_i8 v[30:33], v[158:161], v[204:207], v[30:33]
	v_mfma_i32_16x16x64_i8 v[26:29], v[154:157], v[204:207], v[26:29]
	v_mfma_i32_16x16x64_i8 v[10:13], v[154:157], v[212:215], v[10:13]
	v_mfma_i32_16x16x64_i8 v[14:17], v[158:161], v[212:215], v[14:17]
	s_nop 0
	v_mfma_i32_16x16x64_i8 v[62:65], v[150:153], v[192:195], v[62:65]
	v_mfma_i32_16x16x64_i8 v[58:61], v[146:149], v[192:195], v[58:61]
	v_mfma_i32_16x16x64_i8 v[42:45], v[146:149], v[200:203], v[42:45]
	v_mfma_i32_16x16x64_i8 v[46:49], v[150:153], v[200:203], v[46:49]
	v_mfma_i32_16x16x64_i8 v[30:33], v[150:153], v[208:211], v[30:33]
	v_mfma_i32_16x16x64_i8 v[26:29], v[146:149], v[208:211], v[26:29]
	v_mfma_i32_16x16x64_i8 v[10:13], v[146:149], v[216:219], v[10:13]
	v_mfma_i32_16x16x64_i8 v[14:17], v[150:153], v[216:219], v[14:17]
	v_mfma_i32_16x16x64_i8 v[54:57], v[142:145], v[188:191], v[54:57]
	v_mfma_i32_16x16x64_i8 v[50:53], v[138:141], v[188:191], v[50:53]
	v_mfma_i32_16x16x64_i8 v[34:37], v[138:141], v[196:199], v[34:37]
	v_mfma_i32_16x16x64_i8 v[38:41], v[142:145], v[196:199], v[38:41]
	v_mfma_i32_16x16x64_i8 v[22:25], v[142:145], v[204:207], v[22:25]
	v_mfma_i32_16x16x64_i8 v[18:21], v[138:141], v[204:207], v[18:21]
	v_mfma_i32_16x16x64_i8 v[2:5], v[138:141], v[212:215], v[2:5]
	v_mfma_i32_16x16x64_i8 v[6:9], v[142:145], v[212:215], v[6:9]
	s_nop 0
	v_mfma_i32_16x16x64_i8 v[54:57], v[130:133], v[192:195], v[54:57]
	v_mfma_i32_16x16x64_i8 v[50:53], v[134:137], v[192:195], v[50:53]
	v_mfma_i32_16x16x64_i8 v[34:37], v[134:137], v[200:203], v[34:37]
	v_mfma_i32_16x16x64_i8 v[38:41], v[130:133], v[200:203], v[38:41]
	v_mfma_i32_16x16x64_i8 v[22:25], v[130:133], v[208:211], v[22:25]
	v_mfma_i32_16x16x64_i8 v[18:21], v[134:137], v[208:211], v[18:21]
	v_mfma_i32_16x16x64_i8 v[2:5], v[134:137], v[216:219], v[2:5]
	v_mfma_i32_16x16x64_i8 v[6:9], v[130:133], v[216:219], v[6:9]
	s_setprio 0
	s_barrier
	s_add_i32 s66, 0, 0x18000
	s_add_i32 s67, 0, 0x1c000
	v_add_u32_e32 v142, s66, v182
	v_add_u32_e32 v158, s67, v182
	ds_read_b128 v[130:133], v142
	ds_read_b128 v[134:137], v142 offset:1024
	ds_read_b128 v[138:141], v142 offset:2048
	ds_read_b128 v[142:145], v142 offset:3072
	ds_read_b128 v[146:149], v158
	ds_read_b128 v[150:153], v158 offset:1024
	ds_read_b128 v[154:157], v158 offset:2048
	ds_read_b128 v[158:161], v158 offset:3072
	s_add_u32 s40, s40, 0x80000
	s_addc_u32 s41, s41, 0
	s_mov_b32 m0, s43
	v_lshl_add_u64 v[220:221], s[40:41], 0, v[164:165]
	ds_read_b128 v[188:191], v186 offset:32768
	ds_read_b128 v[192:195], v186 offset:33792
	ds_read_b128 v[196:199], v186 offset:34816
	ds_read_b128 v[200:203], v186 offset:35840
	ds_read_b128 v[204:207], v186 offset:36864
	ds_read_b128 v[208:211], v186 offset:37888
	ds_read_b128 v[212:215], v186 offset:38912
	ds_read_b128 v[216:219], v186 offset:39936
	global_load_lds_dwordx4 v[220:221], off
	v_lshl_add_u64 v[220:221], s[40:41], 0, v[162:163]
	s_mov_b32 m0, s44
	s_nop 0
	global_load_lds_dwordx4 v[220:221], off
	s_waitcnt vmcnt(8) lgkmcnt(0)
	s_barrier
	s_setprio 1
	v_mfma_i32_16x16x64_i8 v[126:129], v[130:133], v[188:191], v[126:129]
	v_mfma_i32_16x16x64_i8 v[122:125], v[138:141], v[188:191], v[122:125]
	v_mfma_i32_16x16x64_i8 v[106:109], v[138:141], v[196:199], v[106:109]
	v_mfma_i32_16x16x64_i8 v[110:113], v[130:133], v[196:199], v[110:113]
	v_mfma_i32_16x16x64_i8 v[94:97], v[130:133], v[204:207], v[94:97]
	v_mfma_i32_16x16x64_i8 v[90:93], v[138:141], v[204:207], v[90:93]
	v_mfma_i32_16x16x64_i8 v[74:77], v[138:141], v[212:215], v[74:77]
	v_mfma_i32_16x16x64_i8 v[78:81], v[130:133], v[212:215], v[78:81]
	s_nop 0
	v_mfma_i32_16x16x64_i8 v[126:129], v[134:137], v[192:195], v[126:129]
	v_mfma_i32_16x16x64_i8 v[122:125], v[142:145], v[192:195], v[122:125]
	v_mfma_i32_16x16x64_i8 v[106:109], v[142:145], v[200:203], v[106:109]
	v_mfma_i32_16x16x64_i8 v[110:113], v[134:137], v[200:203], v[110:113]
	v_mfma_i32_16x16x64_i8 v[94:97], v[134:137], v[208:211], v[94:97]
	v_mfma_i32_16x16x64_i8 v[90:93], v[142:145], v[208:211], v[90:93]
	v_mfma_i32_16x16x64_i8 v[74:77], v[142:145], v[216:219], v[74:77]
	v_mfma_i32_16x16x64_i8 v[78:81], v[134:137], v[216:219], v[78:81]
	v_mfma_i32_16x16x64_i8 v[118:121], v[146:149], v[188:191], v[118:121]
	v_mfma_i32_16x16x64_i8 v[114:117], v[154:157], v[188:191], v[114:117]
	v_mfma_i32_16x16x64_i8 v[98:101], v[154:157], v[196:199], v[98:101]
	v_mfma_i32_16x16x64_i8 v[102:105], v[146:149], v[196:199], v[102:105]
	v_mfma_i32_16x16x64_i8 v[86:89], v[146:149], v[204:207], v[86:89]
	v_mfma_i32_16x16x64_i8 v[82:85], v[154:157], v[204:207], v[82:85]
	v_mfma_i32_16x16x64_i8 v[66:69], v[154:157], v[212:215], v[66:69]
	v_mfma_i32_16x16x64_i8 v[70:73], v[146:149], v[212:215], v[70:73]
	s_nop 0
	v_mfma_i32_16x16x64_i8 v[118:121], v[150:153], v[192:195], v[118:121]
	v_mfma_i32_16x16x64_i8 v[114:117], v[158:161], v[192:195], v[114:117]
	v_mfma_i32_16x16x64_i8 v[98:101], v[158:161], v[200:203], v[98:101]
	v_mfma_i32_16x16x64_i8 v[102:105], v[150:153], v[200:203], v[102:105]
	v_mfma_i32_16x16x64_i8 v[86:89], v[150:153], v[208:211], v[86:89]
	v_mfma_i32_16x16x64_i8 v[82:85], v[158:161], v[208:211], v[82:85]
	v_mfma_i32_16x16x64_i8 v[66:69], v[158:161], v[216:219], v[66:69]
	v_mfma_i32_16x16x64_i8 v[70:73], v[150:153], v[216:219], v[70:73]
	s_setprio 0
	s_barrier
	s_add_i32 s40, s66, s3
	v_lshl_add_u64 v[174:175], v[174:175], 0, s[8:9]
	s_mov_b32 m0, s40
	ds_read_b128 v[188:191], v186 offset:49152
	ds_read_b128 v[192:195], v186 offset:50176
	ds_read_b128 v[196:199], v186 offset:51200
	ds_read_b128 v[200:203], v186 offset:52224
	ds_read_b128 v[204:207], v186 offset:53248
	ds_read_b128 v[208:211], v186 offset:54272
	ds_read_b128 v[212:215], v186 offset:55296
	ds_read_b128 v[216:219], v186 offset:56320
	global_load_lds_dwordx4 v[174:175], off
	s_add_i32 m0, s40, 0x2000
	s_add_u32 s38, s38, 0x80080
	v_lshl_add_u64 v[174:175], v[176:177], 0, s[8:9]
	s_addc_u32 s39, s39, 0
	s_add_i32 s40, s67, s3
	global_load_lds_dwordx4 v[174:175], off
	v_lshl_add_u64 v[174:175], s[38:39], 0, v[164:165]
	s_mov_b32 m0, s40
	s_nop 0
	global_load_lds_dwordx4 v[174:175], off
	v_lshl_add_u64 v[174:175], s[38:39], 0, v[162:163]
	s_add_i32 m0, s40, 0x2000
	s_nop 0
	global_load_lds_dwordx4 v[174:175], off
	v_lshl_add_u64 v[174:175], v[178:179], 0, s[8:9]
	s_mov_b32 m0, s49
	s_nop 0
	global_load_lds_dwordx4 v[174:175], off
	v_lshl_add_u64 v[174:175], v[180:181], 0, s[8:9]
	s_mov_b32 m0, s50
	s_nop 0
	global_load_lds_dwordx4 v[174:175], off
	s_waitcnt vmcnt(8) lgkmcnt(0)
	s_barrier
	s_setprio 1
	v_mfma_i32_16x16x64_i8 v[62:65], v[130:133], v[188:191], v[62:65]
	v_mfma_i32_16x16x64_i8 v[58:61], v[138:141], v[188:191], v[58:61]
	v_mfma_i32_16x16x64_i8 v[42:45], v[138:141], v[196:199], v[42:45]
	v_mfma_i32_16x16x64_i8 v[46:49], v[130:133], v[196:199], v[46:49]
	v_mfma_i32_16x16x64_i8 v[30:33], v[130:133], v[204:207], v[30:33]
	v_mfma_i32_16x16x64_i8 v[26:29], v[138:141], v[204:207], v[26:29]
	v_mfma_i32_16x16x64_i8 v[10:13], v[138:141], v[212:215], v[10:13]
	v_mfma_i32_16x16x64_i8 v[14:17], v[130:133], v[212:215], v[14:17]
	s_nop 0
	v_mfma_i32_16x16x64_i8 v[62:65], v[134:137], v[192:195], v[62:65]
	v_mfma_i32_16x16x64_i8 v[58:61], v[142:145], v[192:195], v[58:61]
	v_mfma_i32_16x16x64_i8 v[42:45], v[142:145], v[200:203], v[42:45]
	v_mfma_i32_16x16x64_i8 v[46:49], v[134:137], v[200:203], v[46:49]
	v_mfma_i32_16x16x64_i8 v[30:33], v[134:137], v[208:211], v[30:33]
	v_mfma_i32_16x16x64_i8 v[26:29], v[142:145], v[208:211], v[26:29]
	v_mfma_i32_16x16x64_i8 v[10:13], v[142:145], v[216:219], v[10:13]
	v_mfma_i32_16x16x64_i8 v[14:17], v[134:137], v[216:219], v[14:17]
	v_mfma_i32_16x16x64_i8 v[54:57], v[146:149], v[188:191], v[54:57]
	v_mfma_i32_16x16x64_i8 v[50:53], v[154:157], v[188:191], v[50:53]
	v_mfma_i32_16x16x64_i8 v[34:37], v[154:157], v[196:199], v[34:37]
	v_mfma_i32_16x16x64_i8 v[38:41], v[146:149], v[196:199], v[38:41]
	v_mfma_i32_16x16x64_i8 v[22:25], v[146:149], v[204:207], v[22:25]
	v_mfma_i32_16x16x64_i8 v[18:21], v[154:157], v[204:207], v[18:21]
	v_mfma_i32_16x16x64_i8 v[2:5], v[154:157], v[212:215], v[2:5]
	v_mfma_i32_16x16x64_i8 v[6:9], v[146:149], v[212:215], v[6:9]
	s_nop 0
	v_mfma_i32_16x16x64_i8 v[54:57], v[150:153], v[192:195], v[54:57]
	v_mfma_i32_16x16x64_i8 v[50:53], v[158:161], v[192:195], v[50:53]
	v_mfma_i32_16x16x64_i8 v[34:37], v[158:161], v[200:203], v[34:37]
	v_mfma_i32_16x16x64_i8 v[38:41], v[150:153], v[200:203], v[38:41]
	v_mfma_i32_16x16x64_i8 v[22:25], v[150:153], v[208:211], v[22:25]
	v_mfma_i32_16x16x64_i8 v[18:21], v[158:161], v[208:211], v[18:21]
	v_mfma_i32_16x16x64_i8 v[2:5], v[158:161], v[216:219], v[2:5]
	v_mfma_i32_16x16x64_i8 v[6:9], v[150:153], v[216:219], v[6:9]
	s_setprio 0
	s_barrier
	s_add_i32 s65, s65, 2
	s_add_u32 s36, s36, 0x100
	s_addc_u32 s37, s37, 0
	s_add_u32 s63, s63, 0x100
	s_addc_u32 s64, s64, 0
	s_cmp_gt_u32 s65, 29
	s_cbranch_scc0 .LBB0_1173
	s_and_b64 vcc, exec, s[12:13]
	s_cbranch_vccz .LBB0_1176
	s_barrier

.LBB0_1291:
	ds_read_b128 v[26:29], v184
	ds_read_b128 v[30:33], v184 offset:1024
	ds_read_b128 v[18:21], v184 offset:2048
	ds_read_b128 v[22:25], v184 offset:3072
	ds_read_b128 v[10:13], v185
	ds_read_b128 v[14:17], v185 offset:1024
	ds_read_b128 v[2:5], v185 offset:2048
	ds_read_b128 v[6:9], v185 offset:3072
	s_add_u32 s20, s14, s16
	s_addc_u32 s21, s15, s17
	s_add_u32 s20, s20, 0x2a800100
	s_addc_u32 s21, s21, 0
	s_add_u32 s48, s31, s16
	s_addc_u32 s49, s34, s17
	s_cmpk_eq_i32 s16, 0x700
	s_cselect_b32 s23, s9, s21
	s_cselect_b32 s22, s8, s20
	s_cselect_b32 s21, s5, s49
	s_cselect_b32 s20, s4, s48
	s_mov_b32 m0, s36
	v_lshl_add_u64 v[214:215], v[170:171], 0, s[16:17]
	ds_read_b128 v[174:177], v186
	ds_read_b128 v[178:181], v186 offset:1024
	ds_read_b128 v[190:193], v186 offset:2048
	ds_read_b128 v[194:197], v186 offset:3072
	ds_read_b128 v[198:201], v186 offset:4096
	ds_read_b128 v[202:205], v186 offset:5120
	ds_read_b128 v[206:209], v186 offset:6144
	ds_read_b128 v[210:213], v186 offset:7168
	global_load_lds_dwordx4 v[214:215], off
	v_lshl_add_u64 v[214:215], v[172:173], 0, s[16:17]
	s_mov_b32 m0, s37
	s_nop 0
	global_load_lds_dwordx4 v[214:215], off
	s_waitcnt vmcnt(8) lgkmcnt(0)
	s_barrier
	s_setprio 1
	v_mfma_f32_16x16x128_f8f6f4 v[158:161], v[26:33], v[174:181], v[158:161]
	v_mfma_f32_16x16x128_f8f6f4 v[154:157], v[18:25], v[174:181], v[154:157]
	v_mfma_f32_16x16x128_f8f6f4 v[138:141], v[18:25], v[190:197], v[138:141]
	v_mfma_f32_16x16x128_f8f6f4 v[146:149], v[26:33], v[190:197], v[146:149]
	v_mfma_f32_16x16x128_f8f6f4 v[130:133], v[26:33], v[198:205], v[130:133]
	v_mfma_f32_16x16x128_f8f6f4 v[122:125], v[18:25], v[198:205], v[122:125]
	v_mfma_f32_16x16x128_f8f6f4 v[106:109], v[18:25], v[206:213], v[106:109]
	v_mfma_f32_16x16x128_f8f6f4 v[114:117], v[26:33], v[206:213], v[114:117]
	v_mfma_f32_16x16x128_f8f6f4 v[102:105], v[10:17], v[206:213], v[102:105]
	v_mfma_f32_16x16x128_f8f6f4 v[98:101], v[2:9], v[206:213], v[98:101]
	v_mfma_f32_16x16x128_f8f6f4 v[142:145], v[2:9], v[174:181], v[142:145]
	v_mfma_f32_16x16x128_f8f6f4 v[150:153], v[10:17], v[174:181], v[150:153]
	v_mfma_f32_16x16x128_f8f6f4 v[134:137], v[10:17], v[190:197], v[134:137]
	v_mfma_f32_16x16x128_f8f6f4 v[126:129], v[2:9], v[190:197], v[126:129]
	v_mfma_f32_16x16x128_f8f6f4 v[110:113], v[2:9], v[198:205], v[110:113]
	v_mfma_f32_16x16x128_f8f6f4 v[118:121], v[10:17], v[198:205], v[118:121]
	s_setprio 0
	s_barrier
	s_mov_b32 m0, s38
	v_lshl_add_u64 v[174:175], s[20:21], 0, v[164:165]
	s_add_u32 s48, s20, 0x80000
	ds_read_b128 v[190:193], v186 offset:16384
	ds_read_b128 v[194:197], v186 offset:17408
	ds_read_b128 v[198:201], v186 offset:18432
	ds_read_b128 v[202:205], v186 offset:19456
	ds_read_b128 v[206:209], v186 offset:20480
	ds_read_b128 v[210:213], v186 offset:21504
	ds_read_b128 v[214:217], v186 offset:22528
	ds_read_b128 v[218:221], v186 offset:23552
	global_load_lds_dwordx4 v[174:175], off
	v_lshl_add_u64 v[176:177], s[20:21], 0, v[168:169]
	s_mov_b32 m0, s39
	s_addc_u32 s49, s21, 0
	global_load_lds_dwordx4 v[176:177], off
	v_lshl_add_u64 v[178:179], s[48:49], 0, v[164:165]
	s_mov_b32 m0, s40
	v_lshl_add_u64 v[180:181], s[22:23], 0, v[166:167]
	global_load_lds_dwordx4 v[178:179], off
	v_lshl_add_u64 v[178:179], s[48:49], 0, v[168:169]
	s_mov_b32 m0, s41
	s_nop 0
	global_load_lds_dwordx4 v[178:179], off
	v_lshl_add_u64 v[178:179], s[22:23], 0, v[162:163]
	s_mov_b32 m0, s24
	s_nop 0
	global_load_lds_dwordx4 v[178:179], off
	s_mov_b32 m0, s25
	s_nop 0
	global_load_lds_dwordx4 v[180:181], off
	s_waitcnt vmcnt(8) lgkmcnt(0)
	s_barrier
	s_setprio 1
	v_mfma_f32_16x16x128_f8f6f4 v[82:85], v[26:33], v[198:205], v[82:85]
	v_mfma_f32_16x16x128_f8f6f4 v[74:77], v[18:25], v[198:205], v[74:77]
	v_mfma_f32_16x16x128_f8f6f4 v[90:93], v[18:25], v[190:197], v[90:93]
	v_mfma_f32_16x16x128_f8f6f4 v[94:97], v[26:33], v[190:197], v[94:97]
	v_mfma_f32_16x16x128_f8f6f4 v[66:69], v[26:33], v[206:213], v[66:69]
	v_mfma_f32_16x16x128_f8f6f4 v[58:61], v[18:25], v[206:213], v[58:61]
	v_mfma_f32_16x16x128_f8f6f4 v[42:45], v[18:25], v[214:221], v[42:45]
	v_mfma_f32_16x16x128_f8f6f4 v[50:53], v[26:33], v[214:221], v[50:53]
	v_mfma_f32_16x16x128_f8f6f4 v[38:41], v[10:17], v[214:221], v[38:41]
	v_mfma_f32_16x16x128_f8f6f4 v[34:37], v[2:9], v[214:221], v[34:37]
	v_mfma_f32_16x16x128_f8f6f4 v[78:81], v[2:9], v[190:197], v[78:81]
	v_mfma_f32_16x16x128_f8f6f4 v[86:89], v[10:17], v[190:197], v[86:89]
	v_mfma_f32_16x16x128_f8f6f4 v[70:73], v[10:17], v[198:205], v[70:73]
	v_mfma_f32_16x16x128_f8f6f4 v[62:65], v[2:9], v[198:205], v[62:65]
	v_mfma_f32_16x16x128_f8f6f4 v[46:49], v[2:9], v[206:213], v[46:49]
	v_mfma_f32_16x16x128_f8f6f4 v[54:57], v[10:17], v[206:213], v[54:57]
	s_setprio 0
	s_barrier
	ds_read_b128 v[2:5], v187
	ds_read_b128 v[6:9], v187 offset:1024
	ds_read_b128 v[10:13], v187 offset:2048
	ds_read_b128 v[14:17], v187 offset:3072
	ds_read_b128 v[18:21], v188
	ds_read_b128 v[22:25], v188 offset:1024
	ds_read_b128 v[26:29], v188 offset:2048
	ds_read_b128 v[30:33], v188 offset:3072
	s_add_u32 s22, s22, 0x80000
	s_addc_u32 s23, s23, 0
	s_mov_b32 m0, s26
	v_lshl_add_u64 v[222:223], s[22:23], 0, v[162:163]
	ds_read_b128 v[190:193], v186 offset:32768
	ds_read_b128 v[194:197], v186 offset:33792
	ds_read_b128 v[198:201], v186 offset:34816
	ds_read_b128 v[202:205], v186 offset:35840
	ds_read_b128 v[206:209], v186 offset:36864
	ds_read_b128 v[210:213], v186 offset:37888
	ds_read_b128 v[214:217], v186 offset:38912
	ds_read_b128 v[218:221], v186 offset:39936
	global_load_lds_dwordx4 v[222:223], off
	v_lshl_add_u64 v[222:223], s[22:23], 0, v[166:167]
	s_mov_b32 m0, s27
	s_nop 0
	global_load_lds_dwordx4 v[222:223], off
	s_waitcnt vmcnt(8) lgkmcnt(0)
	s_barrier
	s_setprio 1
	v_mfma_f32_16x16x128_f8f6f4 v[122:125], v[10:17], v[206:213], v[122:125]
	v_mfma_f32_16x16x128_f8f6f4 v[130:133], v[2:9], v[206:213], v[130:133]
	v_mfma_f32_16x16x128_f8f6f4 v[158:161], v[2:9], v[190:197], v[158:161]
	v_mfma_f32_16x16x128_f8f6f4 v[154:157], v[10:17], v[190:197], v[154:157]
	v_mfma_f32_16x16x128_f8f6f4 v[138:141], v[10:17], v[198:205], v[138:141]
	v_mfma_f32_16x16x128_f8f6f4 v[146:149], v[2:9], v[198:205], v[146:149]
	v_mfma_f32_16x16x128_f8f6f4 v[114:117], v[2:9], v[214:221], v[114:117]
	v_mfma_f32_16x16x128_f8f6f4 v[106:109], v[10:17], v[214:221], v[106:109]
	v_mfma_f32_16x16x128_f8f6f4 v[102:105], v[18:25], v[214:221], v[102:105]
	v_mfma_f32_16x16x128_f8f6f4 v[98:101], v[26:33], v[214:221], v[98:101]
	v_mfma_f32_16x16x128_f8f6f4 v[142:145], v[26:33], v[190:197], v[142:145]
	v_mfma_f32_16x16x128_f8f6f4 v[150:153], v[18:25], v[190:197], v[150:153]
	v_mfma_f32_16x16x128_f8f6f4 v[134:137], v[18:25], v[198:205], v[134:137]
	v_mfma_f32_16x16x128_f8f6f4 v[126:129], v[26:33], v[198:205], v[126:129]
	v_mfma_f32_16x16x128_f8f6f4 v[110:113], v[26:33], v[206:213], v[110:113]
	v_mfma_f32_16x16x128_f8f6f4 v[118:121], v[18:25], v[206:213], v[118:121]
	s_setprio 0
	s_barrier
	s_mov_b32 m0, s42
	v_lshl_add_u64 v[174:175], v[174:175], 0, s[12:13]
	s_add_u32 s20, s20, 0x80080
	ds_read_b128 v[190:193], v186 offset:49152
	ds_read_b128 v[194:197], v186 offset:50176
	ds_read_b128 v[198:201], v186 offset:51200
	ds_read_b128 v[202:205], v186 offset:52224
	ds_read_b128 v[206:209], v186 offset:53248
	ds_read_b128 v[210:213], v186 offset:54272
	ds_read_b128 v[214:217], v186 offset:55296
	ds_read_b128 v[218:221], v186 offset:56320
	global_load_lds_dwordx4 v[174:175], off
	v_lshl_add_u64 v[174:175], v[176:177], 0, s[12:13]
	s_mov_b32 m0, s43
	s_addc_u32 s21, s21, 0
	global_load_lds_dwordx4 v[174:175], off
	v_lshl_add_u64 v[174:175], s[20:21], 0, v[164:165]
	s_mov_b32 m0, s44
	s_nop 0
	global_load_lds_dwordx4 v[174:175], off
	v_lshl_add_u64 v[174:175], s[20:21], 0, v[168:169]
	s_mov_b32 m0, s45
	s_nop 0
	global_load_lds_dwordx4 v[174:175], off
	v_lshl_add_u64 v[174:175], v[178:179], 0, s[12:13]
	s_mov_b32 m0, s29
	s_nop 0
	global_load_lds_dwordx4 v[174:175], off
	v_lshl_add_u64 v[174:175], v[180:181], 0, s[12:13]
	s_mov_b32 m0, s30
	s_nop 0
	global_load_lds_dwordx4 v[174:175], off
	s_waitcnt vmcnt(8) lgkmcnt(0)
	s_barrier
	s_setprio 1
	v_mfma_f32_16x16x128_f8f6f4 v[66:69], v[2:9], v[206:213], v[66:69]
	v_mfma_f32_16x16x128_f8f6f4 v[58:61], v[10:17], v[206:213], v[58:61]
	v_mfma_f32_16x16x128_f8f6f4 v[90:93], v[10:17], v[190:197], v[90:93]
	v_mfma_f32_16x16x128_f8f6f4 v[94:97], v[2:9], v[190:197], v[94:97]
	v_mfma_f32_16x16x128_f8f6f4 v[82:85], v[2:9], v[198:205], v[82:85]
	v_mfma_f32_16x16x128_f8f6f4 v[74:77], v[10:17], v[198:205], v[74:77]
	v_mfma_f32_16x16x128_f8f6f4 v[42:45], v[10:17], v[214:221], v[42:45]
	v_mfma_f32_16x16x128_f8f6f4 v[50:53], v[2:9], v[214:221], v[50:53]
	v_mfma_f32_16x16x128_f8f6f4 v[38:41], v[18:25], v[214:221], v[38:41]
	v_mfma_f32_16x16x128_f8f6f4 v[34:37], v[26:33], v[214:221], v[34:37]
	v_mfma_f32_16x16x128_f8f6f4 v[78:81], v[26:33], v[190:197], v[78:81]
	v_mfma_f32_16x16x128_f8f6f4 v[86:89], v[18:25], v[190:197], v[86:89]
	v_mfma_f32_16x16x128_f8f6f4 v[70:73], v[18:25], v[198:205], v[70:73]
	v_mfma_f32_16x16x128_f8f6f4 v[62:65], v[26:33], v[198:205], v[62:65]
	v_mfma_f32_16x16x128_f8f6f4 v[46:49], v[26:33], v[206:213], v[46:49]
	v_mfma_f32_16x16x128_f8f6f4 v[54:57], v[18:25], v[206:213], v[54:57]
	s_setprio 0
	s_barrier
	s_add_i32 s35, s35, 2
	s_add_u32 s16, s16, 0x100
	s_addc_u32 s17, s17, 0
	s_cmp_gt_u32 s35, 13
	s_cbranch_scc0 .LBB0_1291
	s_cmpk_lt_u32 s19, 0x100
	s_cbranch_scc0 .LBB0_1294
	s_barrier

.LBB0_1309:
	ds_read_b128 v[26:29], v189
	ds_read_b128 v[30:33], v189 offset:1024
	ds_read_b128 v[18:21], v189 offset:2048
	ds_read_b128 v[22:25], v189 offset:3072
	ds_read_b128 v[10:13], v190
	ds_read_b128 v[14:17], v190 offset:1024
	ds_read_b128 v[2:5], v190 offset:2048
	ds_read_b128 v[6:9], v190 offset:3072
	s_add_u32 s40, s38, 0xfff80080
	s_addc_u32 s41, s39, -1
	s_cmp_eq_u32 s72, 28
	s_cselect_b32 s43, s18, s41
	s_cselect_b32 s42, s19, s40
	s_cselect_b32 s41, s27, s71
	s_cselect_b32 s40, s29, s70
	v_lshl_add_u64 v[216:217], s[38:39], 0, v[170:171]
	s_add_i32 m0, s37, 0xc000
	ds_read_b128 v[178:181], v191
	ds_read_b128 v[182:185], v191 offset:1024
	ds_read_b128 v[192:195], v191 offset:2048
	ds_read_b128 v[196:199], v191 offset:3072
	ds_read_b128 v[200:203], v191 offset:4096
	ds_read_b128 v[204:207], v191 offset:5120
	ds_read_b128 v[208:211], v191 offset:6144
	ds_read_b128 v[212:215], v191 offset:7168
	global_load_lds_dwordx4 v[216:217], off
	v_lshl_add_u64 v[216:217], s[38:39], 0, v[172:173]
	s_add_i32 m0, s37, 0xe000
	s_nop 0
	global_load_lds_dwordx4 v[216:217], off
	s_waitcnt vmcnt(8) lgkmcnt(0)
	s_barrier
	s_setprio 1
	v_mfma_f32_16x16x128_f8f6f4 v[158:161], v[26:33], v[178:185], v[158:161]
	v_mfma_f32_16x16x128_f8f6f4 v[154:157], v[18:25], v[178:185], v[154:157]
	v_mfma_f32_16x16x128_f8f6f4 v[138:141], v[18:25], v[192:199], v[138:141]
	v_mfma_f32_16x16x128_f8f6f4 v[146:149], v[26:33], v[192:199], v[146:149]
	v_mfma_f32_16x16x128_f8f6f4 v[130:133], v[26:33], v[200:207], v[130:133]
	v_mfma_f32_16x16x128_f8f6f4 v[122:125], v[18:25], v[200:207], v[122:125]
	v_mfma_f32_16x16x128_f8f6f4 v[106:109], v[18:25], v[208:215], v[106:109]
	v_mfma_f32_16x16x128_f8f6f4 v[114:117], v[26:33], v[208:215], v[114:117]
	v_mfma_f32_16x16x128_f8f6f4 v[102:105], v[10:17], v[208:215], v[102:105]
	v_mfma_f32_16x16x128_f8f6f4 v[98:101], v[2:9], v[208:215], v[98:101]
	v_mfma_f32_16x16x128_f8f6f4 v[142:145], v[2:9], v[178:185], v[142:145]
	v_mfma_f32_16x16x128_f8f6f4 v[150:153], v[10:17], v[178:185], v[150:153]
	v_mfma_f32_16x16x128_f8f6f4 v[134:137], v[10:17], v[192:199], v[134:137]
	v_mfma_f32_16x16x128_f8f6f4 v[126:129], v[2:9], v[192:199], v[126:129]
	v_mfma_f32_16x16x128_f8f6f4 v[110:113], v[2:9], v[200:207], v[110:113]
	v_mfma_f32_16x16x128_f8f6f4 v[118:121], v[10:17], v[200:207], v[118:121]
	s_setprio 0
	s_barrier
	s_add_i32 s64, s59, s3
	v_lshl_add_u64 v[178:179], s[40:41], 0, v[166:167]
	s_mov_b32 m0, s64
	ds_read_b128 v[192:195], v191 offset:16384
	ds_read_b128 v[196:199], v191 offset:17408
	ds_read_b128 v[200:203], v191 offset:18432
	ds_read_b128 v[204:207], v191 offset:19456
	ds_read_b128 v[208:211], v191 offset:20480
	ds_read_b128 v[212:215], v191 offset:21504
	ds_read_b128 v[216:219], v191 offset:22528
	ds_read_b128 v[220:223], v191 offset:23552
	global_load_lds_dwordx4 v[178:179], off
	s_add_i32 m0, s64, 0x2000
	s_add_u32 s64, s40, 0x80000
	v_lshl_add_u64 v[180:181], s[40:41], 0, v[162:163]
	s_addc_u32 s65, s41, 0
	s_add_i32 s73, s62, s3
	global_load_lds_dwordx4 v[180:181], off
	v_lshl_add_u64 v[182:183], s[64:65], 0, v[166:167]
	s_mov_b32 m0, s73
	v_lshl_add_u64 v[184:185], s[42:43], 0, v[164:165]
	global_load_lds_dwordx4 v[182:183], off
	v_lshl_add_u64 v[182:183], s[64:65], 0, v[162:163]
	s_add_i32 m0, s73, 0x2000
	s_nop 0
	global_load_lds_dwordx4 v[182:183], off
	v_lshl_add_u64 v[182:183], s[42:43], 0, v[168:169]
	s_mov_b32 m0, s37
	s_nop 0
	global_load_lds_dwordx4 v[182:183], off
	s_mov_b32 m0, s44
	s_nop 0
	global_load_lds_dwordx4 v[184:185], off
	s_waitcnt vmcnt(8) lgkmcnt(0)
	s_barrier
	s_setprio 1
	v_mfma_f32_16x16x128_f8f6f4 v[82:85], v[26:33], v[200:207], v[82:85]
	v_mfma_f32_16x16x128_f8f6f4 v[74:77], v[18:25], v[200:207], v[74:77]
	v_mfma_f32_16x16x128_f8f6f4 v[90:93], v[18:25], v[192:199], v[90:93]
	v_mfma_f32_16x16x128_f8f6f4 v[94:97], v[26:33], v[192:199], v[94:97]
	v_mfma_f32_16x16x128_f8f6f4 v[66:69], v[26:33], v[208:215], v[66:69]
	v_mfma_f32_16x16x128_f8f6f4 v[58:61], v[18:25], v[208:215], v[58:61]
	v_mfma_f32_16x16x128_f8f6f4 v[42:45], v[18:25], v[216:223], v[42:45]
	v_mfma_f32_16x16x128_f8f6f4 v[50:53], v[26:33], v[216:223], v[50:53]
	v_mfma_f32_16x16x128_f8f6f4 v[38:41], v[10:17], v[216:223], v[38:41]
	v_mfma_f32_16x16x128_f8f6f4 v[34:37], v[2:9], v[216:223], v[34:37]
	v_mfma_f32_16x16x128_f8f6f4 v[78:81], v[2:9], v[192:199], v[78:81]
	v_mfma_f32_16x16x128_f8f6f4 v[86:89], v[10:17], v[192:199], v[86:89]
	v_mfma_f32_16x16x128_f8f6f4 v[70:73], v[10:17], v[200:207], v[70:73]
	v_mfma_f32_16x16x128_f8f6f4 v[62:65], v[2:9], v[200:207], v[62:65]
	v_mfma_f32_16x16x128_f8f6f4 v[46:49], v[2:9], v[208:215], v[46:49]
	v_mfma_f32_16x16x128_f8f6f4 v[54:57], v[10:17], v[208:215], v[54:57]
	s_setprio 0
	s_barrier
	s_add_i32 s64, 0, 0x18000
	s_add_i32 s65, 0, 0x1c000
	v_add_u32_e32 v14, s64, v187
	v_add_u32_e32 v30, s65, v187
	ds_read_b128 v[2:5], v14
	ds_read_b128 v[6:9], v14 offset:1024
	ds_read_b128 v[10:13], v14 offset:2048
	ds_read_b128 v[14:17], v14 offset:3072
	ds_read_b128 v[18:21], v30
	ds_read_b128 v[22:25], v30 offset:1024
	ds_read_b128 v[26:29], v30 offset:2048
	ds_read_b128 v[30:33], v30 offset:3072
	s_add_u32 s42, s42, 0x80000
	s_addc_u32 s43, s43, 0
	s_mov_b32 m0, s45
	v_lshl_add_u64 v[224:225], s[42:43], 0, v[168:169]
	ds_read_b128 v[192:195], v191 offset:32768
	ds_read_b128 v[196:199], v191 offset:33792
	ds_read_b128 v[200:203], v191 offset:34816
	ds_read_b128 v[204:207], v191 offset:35840
	ds_read_b128 v[208:211], v191 offset:36864
	ds_read_b128 v[212:215], v191 offset:37888
	ds_read_b128 v[216:219], v191 offset:38912
	ds_read_b128 v[220:223], v191 offset:39936
	global_load_lds_dwordx4 v[224:225], off
	v_lshl_add_u64 v[224:225], s[42:43], 0, v[164:165]
	s_mov_b32 m0, s48
	s_nop 0
	global_load_lds_dwordx4 v[224:225], off
	s_waitcnt vmcnt(8) lgkmcnt(0)
	s_barrier
	s_setprio 1
	v_mfma_f32_16x16x128_f8f6f4 v[122:125], v[10:17], v[208:215], v[122:125]
	v_mfma_f32_16x16x128_f8f6f4 v[130:133], v[2:9], v[208:215], v[130:133]
	v_mfma_f32_16x16x128_f8f6f4 v[158:161], v[2:9], v[192:199], v[158:161]
	v_mfma_f32_16x16x128_f8f6f4 v[154:157], v[10:17], v[192:199], v[154:157]
	v_mfma_f32_16x16x128_f8f6f4 v[138:141], v[10:17], v[200:207], v[138:141]
	v_mfma_f32_16x16x128_f8f6f4 v[146:149], v[2:9], v[200:207], v[146:149]
	v_mfma_f32_16x16x128_f8f6f4 v[114:117], v[2:9], v[216:223], v[114:117]
	v_mfma_f32_16x16x128_f8f6f4 v[106:109], v[10:17], v[216:223], v[106:109]
	v_mfma_f32_16x16x128_f8f6f4 v[102:105], v[18:25], v[216:223], v[102:105]
	v_mfma_f32_16x16x128_f8f6f4 v[98:101], v[26:33], v[216:223], v[98:101]
	v_mfma_f32_16x16x128_f8f6f4 v[142:145], v[26:33], v[192:199], v[142:145]
	v_mfma_f32_16x16x128_f8f6f4 v[150:153], v[18:25], v[192:199], v[150:153]
	v_mfma_f32_16x16x128_f8f6f4 v[134:137], v[18:25], v[200:207], v[134:137]
	v_mfma_f32_16x16x128_f8f6f4 v[126:129], v[26:33], v[200:207], v[126:129]
	v_mfma_f32_16x16x128_f8f6f4 v[110:113], v[26:33], v[208:215], v[110:113]
	v_mfma_f32_16x16x128_f8f6f4 v[118:121], v[18:25], v[208:215], v[118:121]
	s_setprio 0
	s_barrier
	s_add_i32 s42, s64, s3
	v_lshl_add_u64 v[178:179], v[178:179], 0, s[12:13]
	s_mov_b32 m0, s42
	ds_read_b128 v[192:195], v191 offset:49152
	ds_read_b128 v[196:199], v191 offset:50176
	ds_read_b128 v[200:203], v191 offset:51200
	ds_read_b128 v[204:207], v191 offset:52224
	ds_read_b128 v[208:211], v191 offset:53248
	ds_read_b128 v[212:215], v191 offset:54272
	ds_read_b128 v[216:219], v191 offset:55296
	ds_read_b128 v[220:223], v191 offset:56320
	global_load_lds_dwordx4 v[178:179], off
	s_add_i32 m0, s42, 0x2000
	s_add_u32 s40, s40, 0x80080
	v_lshl_add_u64 v[178:179], v[180:181], 0, s[12:13]
	s_addc_u32 s41, s41, 0
	s_add_i32 s42, s65, s3
	global_load_lds_dwordx4 v[178:179], off
	v_lshl_add_u64 v[178:179], s[40:41], 0, v[166:167]
	s_mov_b32 m0, s42
	s_nop 0
	global_load_lds_dwordx4 v[178:179], off
	v_lshl_add_u64 v[178:179], s[40:41], 0, v[162:163]
	s_add_i32 m0, s42, 0x2000
	s_nop 0
	global_load_lds_dwordx4 v[178:179], off
	v_lshl_add_u64 v[178:179], v[182:183], 0, s[12:13]
	s_mov_b32 m0, s51
	s_nop 0
	global_load_lds_dwordx4 v[178:179], off
	v_lshl_add_u64 v[178:179], v[184:185], 0, s[12:13]
	s_mov_b32 m0, s58
	s_nop 0
	global_load_lds_dwordx4 v[178:179], off
	s_waitcnt vmcnt(8) lgkmcnt(0)
	s_barrier
	s_setprio 1
	v_mfma_f32_16x16x128_f8f6f4 v[66:69], v[2:9], v[208:215], v[66:69]
	v_mfma_f32_16x16x128_f8f6f4 v[58:61], v[10:17], v[208:215], v[58:61]
	v_mfma_f32_16x16x128_f8f6f4 v[90:93], v[10:17], v[192:199], v[90:93]
	v_mfma_f32_16x16x128_f8f6f4 v[94:97], v[2:9], v[192:199], v[94:97]
	v_mfma_f32_16x16x128_f8f6f4 v[82:85], v[2:9], v[200:207], v[82:85]
	v_mfma_f32_16x16x128_f8f6f4 v[74:77], v[10:17], v[200:207], v[74:77]
	v_mfma_f32_16x16x128_f8f6f4 v[42:45], v[10:17], v[216:223], v[42:45]
	v_mfma_f32_16x16x128_f8f6f4 v[50:53], v[2:9], v[216:223], v[50:53]
	v_mfma_f32_16x16x128_f8f6f4 v[38:41], v[18:25], v[216:223], v[38:41]
	v_mfma_f32_16x16x128_f8f6f4 v[34:37], v[26:33], v[216:223], v[34:37]
	v_mfma_f32_16x16x128_f8f6f4 v[78:81], v[26:33], v[192:199], v[78:81]
	v_mfma_f32_16x16x128_f8f6f4 v[86:89], v[18:25], v[192:199], v[86:89]
	v_mfma_f32_16x16x128_f8f6f4 v[70:73], v[18:25], v[200:207], v[70:73]
	v_mfma_f32_16x16x128_f8f6f4 v[62:65], v[26:33], v[200:207], v[62:65]
	v_mfma_f32_16x16x128_f8f6f4 v[46:49], v[26:33], v[208:215], v[46:49]
	v_mfma_f32_16x16x128_f8f6f4 v[54:57], v[18:25], v[208:215], v[54:57]
	s_setprio 0
	s_barrier
	s_add_i32 s72, s72, 2
	s_add_u32 s38, s38, 0x100
	s_addc_u32 s39, s39, 0
	s_add_u32 s70, s70, 0x100
	s_addc_u32 s71, s71, 0
	s_cmp_gt_u32 s72, 29
	s_cbranch_scc0 .LBB0_1309
	s_and_b64 vcc, exec, s[14:15]
	s_cbranch_vccz .LBB0_1312
	s_barrier

.LBB0_1437:
	v_and_b32_e32 v188, 15, v189
	v_and_b32_e32 v2, 48, v189
	v_lshlrev_b32_e32 v3, 2, v189
	s_and_b32 s8, s6, 3
	s_lshl_b32 s9, s7, 13
	v_lshl_or_b32 v2, v188, 6, v2
	v_and_b32_e32 v3, 32, v3
	v_bitop3_b32 v4, v2, s9, v3 bitop3:0xde
	s_lshl_b32 s9, s8, 12
	v_lshl_add_u64 v[180:181], s[20:21], 0, v[154:155]
	v_bitop3_b32 v2, v2, s9, v3 bitop3:0xde
	s_add_i32 s9, s60, s72
	v_lshl_add_u64 v[178:179], s[20:21], 0, v[182:183]
	v_lshl_add_u64 v[72:73], v[180:181], 0, s[36:37]
	s_mov_b32 m0, s9
	s_add_i32 s19, s9, 0x2000
	s_waitcnt vmcnt(2)
	s_barrier
	global_load_lds_dwordx4 v[72:73], off
	v_lshl_add_u64 v[158:159], v[178:179], 0, s[36:37]
	s_mov_b32 m0, s19
	s_add_i32 s18, s67, 0x8000
	global_load_lds_dwordx4 v[158:159], off
	v_lshl_add_u64 v[70:71], v[172:173], 0, s[36:37]
	s_mov_b32 m0, s18
	s_add_i32 s43, s67, 0xa000
	global_load_lds_dwordx4 v[70:71], off
	v_lshl_add_u64 v[160:161], v[170:171], 0, s[36:37]
	s_mov_b32 m0, s43
	s_add_i32 s44, s61, s72
	global_load_lds_dwordx4 v[160:161], off
	v_lshl_add_u64 v[162:163], s[24:25], 0, v[154:155]
	s_mov_b32 m0, s44
	s_add_i32 s45, s44, 0x2000
	global_load_lds_dwordx4 v[162:163], off
	v_lshl_add_u64 v[164:165], s[24:25], 0, v[182:183]
	s_mov_b32 m0, s45
	s_add_i32 s73, 0, 0x10000
	global_load_lds_dwordx4 v[164:165], off
	v_add_u32_e32 v195, s73, v2
	s_add_i32 s75, 0, 0x14000
	s_waitcnt vmcnt(6)
	s_barrier
	v_add_u32_e32 v194, s75, v2
	v_add_u32_e32 v191, 0, v4
	v_add_u32_e32 v193, s60, v2
	v_add_u32_e32 v192, s61, v2
	ds_read_b128 v[54:57], v195
	ds_read_b128 v[58:61], v195 offset:1024
	ds_read_b128 v[196:199], v195 offset:2048
	ds_read_b128 v[200:203], v195 offset:3072
	ds_read_b128 v[10:13], v194
	ds_read_b128 v[14:17], v194 offset:1024
	ds_read_b128 v[2:5], v194 offset:2048
	ds_read_b128 v[6:9], v194 offset:3072
	s_lshl_b32 s66, s7, 6
	v_lshl_add_u64 v[176:177], s[22:23], 0, v[154:155]
	v_lshl_add_u64 v[174:175], s[22:23], 0, v[182:183]
	s_add_u32 s70, s4, 0x10080
	s_addc_u32 s71, s5, 0
	s_add_i32 s74, s67, 0xc000
	v_lshl_add_u64 v[30:31], s[70:71], 0, v[154:155]
	s_mov_b32 m0, s74
	s_add_i32 s69, s67, 0xe000
	ds_read_b128 v[22:25], v191
	ds_read_b128 v[26:29], v191 offset:1024
	ds_read_b128 v[34:37], v191 offset:2048
	ds_read_b128 v[38:41], v191 offset:3072
	ds_read_b128 v[82:85], v191 offset:4096
	ds_read_b128 v[86:89], v191 offset:5120
	ds_read_b128 v[94:97], v191 offset:6144
	ds_read_b128 v[98:101], v191 offset:7168
	global_load_lds_dwordx4 v[30:31], off
	v_lshl_add_u64 v[30:31], s[70:71], 0, v[182:183]
	s_mov_b32 m0, s69
	s_nop 0
	global_load_lds_dwordx4 v[30:31], off
	s_waitcnt vmcnt(8) lgkmcnt(0)
	s_barrier
	s_setprio 1
	v_mov_b64_e32 v[32:33], v[20:21]
	v_mov_b64_e32 v[152:153], v[20:21]
	v_mov_b64_e32 v[92:93], v[20:21]
	v_mov_b64_e32 v[44:45], v[20:21]
	v_mov_b64_e32 v[116:117], v[20:21]
	v_mov_b64_e32 v[64:65], v[20:21]
	v_mov_b64_e32 v[80:81], v[20:21]
	v_mov_b64_e32 v[52:53], v[20:21]
	v_mov_b64_e32 v[30:31], v[18:19]
	v_mov_b64_e32 v[150:151], v[18:19]
	v_mov_b64_e32 v[90:91], v[18:19]
	v_mov_b64_e32 v[42:43], v[18:19]
	v_mov_b64_e32 v[114:115], v[18:19]
	v_mov_b64_e32 v[62:63], v[18:19]
	v_mov_b64_e32 v[78:79], v[18:19]
	v_mov_b64_e32 v[50:51], v[18:19]
	s_waitcnt lgkmcnt(0)
	v_mfma_f32_16x16x128_f8f6f4 v[30:33], v[54:61], v[22:29], v[30:33]
	v_mfma_f32_16x16x128_f8f6f4 v[150:153], v[196:203], v[22:29], v[150:153]
	v_mfma_f32_16x16x128_f8f6f4 v[42:45], v[196:203], v[34:41], v[42:45]
	v_mfma_f32_16x16x128_f8f6f4 v[90:93], v[54:61], v[34:41], v[90:93]
	v_mfma_f32_16x16x128_f8f6f4 v[114:117], v[54:61], v[82:89], v[114:117]
	v_mfma_f32_16x16x128_f8f6f4 v[62:65], v[196:203], v[82:89], v[62:65]
	v_mfma_f32_16x16x128_f8f6f4 v[50:53], v[196:203], v[94:101], v[50:53]
	v_mfma_f32_16x16x128_f8f6f4 v[78:81], v[54:61], v[94:101], v[78:81]
	v_mov_b64_e32 v[144:145], v[20:21]
	v_mov_b64_e32 v[148:149], v[20:21]
	v_mov_b64_e32 v[142:143], v[18:19]
	v_mov_b64_e32 v[146:147], v[18:19]
	v_mfma_f32_16x16x128_f8f6f4 v[142:145], v[10:17], v[22:29], v[142:145]
	v_mfma_f32_16x16x128_f8f6f4 v[146:149], v[2:9], v[22:29], v[146:149]
	v_mov_b64_e32 v[28:29], v[20:21]
	v_mov_b64_e32 v[140:141], v[20:21]
	v_mov_b64_e32 v[26:27], v[18:19]
	v_mov_b64_e32 v[138:139], v[18:19]
	v_mfma_f32_16x16x128_f8f6f4 v[26:29], v[10:17], v[34:41], v[26:29]
	v_mfma_f32_16x16x128_f8f6f4 v[138:141], v[2:9], v[34:41], v[138:141]
	v_mov_b64_e32 v[40:41], v[20:21]
	v_mov_b64_e32 v[128:129], v[20:21]
	v_mov_b64_e32 v[24:25], v[20:21]
	v_mov_b64_e32 v[76:77], v[20:21]
	v_mov_b64_e32 v[38:39], v[18:19]
	v_mov_b64_e32 v[126:127], v[18:19]
	v_mov_b64_e32 v[22:23], v[18:19]
	v_mov_b64_e32 v[74:75], v[18:19]
	v_mfma_f32_16x16x128_f8f6f4 v[38:41], v[10:17], v[82:89], v[38:41]
	v_mfma_f32_16x16x128_f8f6f4 v[126:129], v[2:9], v[82:89], v[126:129]
	v_mfma_f32_16x16x128_f8f6f4 v[22:25], v[10:17], v[94:101], v[22:25]
	v_mfma_f32_16x16x128_f8f6f4 v[74:77], v[2:9], v[94:101], v[74:77]
	s_setprio 0
	s_barrier
	s_add_i32 s70, s73, s72
	v_lshl_add_u64 v[34:35], v[180:181], 0, s[14:15]
	s_mov_b32 m0, s70
	s_add_i32 s71, s70, 0x2000
	ds_read_b128 v[204:207], v191 offset:16384
	ds_read_b128 v[208:211], v191 offset:17408
	ds_read_b128 v[212:215], v191 offset:18432
	ds_read_b128 v[216:219], v191 offset:19456
	ds_read_b128 v[220:223], v191 offset:20480
	ds_read_b128 v[224:227], v191 offset:21504
	ds_read_b128 v[228:231], v191 offset:22528
	ds_read_b128 v[232:235], v191 offset:23552
	global_load_lds_dwordx4 v[34:35], off
	v_lshl_add_u64 v[34:35], v[178:179], 0, s[14:15]
	s_mov_b32 m0, s71
	s_add_i32 s72, s75, s72
	global_load_lds_dwordx4 v[34:35], off
	v_lshl_add_u64 v[34:35], s[26:27], 0, v[154:155]
	s_mov_b32 m0, s72
	s_add_i32 s73, s72, 0x2000
	global_load_lds_dwordx4 v[34:35], off
	v_lshl_add_u64 v[34:35], s[26:27], 0, v[182:183]
	s_mov_b32 m0, s73
	s_nop 0
	global_load_lds_dwordx4 v[34:35], off
	v_lshl_add_u64 v[34:35], v[172:173], 0, s[14:15]
	s_mov_b32 m0, s67
	s_nop 0
	global_load_lds_dwordx4 v[34:35], off
	v_lshl_add_u64 v[34:35], v[170:171], 0, s[14:15]
	s_mov_b32 m0, s68
	s_nop 0
	global_load_lds_dwordx4 v[34:35], off
	s_waitcnt vmcnt(8) lgkmcnt(0)
	s_barrier
	s_setprio 1
	v_mov_b64_e32 v[136:137], v[20:21]
	v_mov_b64_e32 v[104:105], v[20:21]
	v_mov_b64_e32 v[124:125], v[20:21]
	v_mov_b64_e32 v[100:101], v[20:21]
	v_mov_b64_e32 v[112:113], v[20:21]
	v_mov_b64_e32 v[108:109], v[20:21]
	v_mov_b64_e32 v[88:89], v[20:21]
	v_mov_b64_e32 v[84:85], v[20:21]
	v_mov_b64_e32 v[134:135], v[18:19]
	v_mov_b64_e32 v[102:103], v[18:19]
	v_mov_b64_e32 v[122:123], v[18:19]
	v_mov_b64_e32 v[98:99], v[18:19]
	v_mov_b64_e32 v[110:111], v[18:19]
	v_mov_b64_e32 v[106:107], v[18:19]
	v_mov_b64_e32 v[86:87], v[18:19]
	v_mov_b64_e32 v[82:83], v[18:19]
	s_waitcnt lgkmcnt(0)
	v_mfma_f32_16x16x128_f8f6f4 v[134:137], v[54:61], v[204:211], v[134:137]
	v_mfma_f32_16x16x128_f8f6f4 v[102:105], v[196:203], v[204:211], v[102:105]
	v_mfma_f32_16x16x128_f8f6f4 v[98:101], v[196:203], v[212:219], v[98:101]
	v_mfma_f32_16x16x128_f8f6f4 v[122:125], v[54:61], v[212:219], v[122:125]
	v_mfma_f32_16x16x128_f8f6f4 v[110:113], v[54:61], v[220:227], v[110:113]
	v_mfma_f32_16x16x128_f8f6f4 v[106:109], v[196:203], v[220:227], v[106:109]
	v_mfma_f32_16x16x128_f8f6f4 v[82:85], v[196:203], v[228:235], v[82:85]
	v_mfma_f32_16x16x128_f8f6f4 v[86:89], v[54:61], v[228:235], v[86:89]
	v_mov_b64_e32 v[36:37], v[20:21]
	v_mov_b64_e32 v[132:133], v[20:21]
	v_mov_b64_e32 v[48:49], v[20:21]
	v_mov_b64_e32 v[120:121], v[20:21]
	v_mov_b64_e32 v[68:69], v[20:21]
	v_mov_b64_e32 v[96:97], v[20:21]
	v_mov_b64_e32 v[56:57], v[20:21]
	v_mov_b64_e32 v[60:61], v[20:21]
	v_mov_b64_e32 v[34:35], v[18:19]
	v_mov_b64_e32 v[130:131], v[18:19]
	v_mov_b64_e32 v[46:47], v[18:19]
	v_mov_b64_e32 v[118:119], v[18:19]
	v_mov_b64_e32 v[66:67], v[18:19]
	v_mov_b64_e32 v[94:95], v[18:19]
	v_mov_b64_e32 v[54:55], v[18:19]
	v_mov_b64_e32 v[58:59], v[18:19]
	v_mfma_f32_16x16x128_f8f6f4 v[54:57], v[10:17], v[228:235], v[54:57]
	v_mfma_f32_16x16x128_f8f6f4 v[58:61], v[2:9], v[228:235], v[58:61]
	v_mfma_f32_16x16x128_f8f6f4 v[130:133], v[2:9], v[204:211], v[130:133]
	v_mfma_f32_16x16x128_f8f6f4 v[34:37], v[10:17], v[204:211], v[34:37]
	v_mfma_f32_16x16x128_f8f6f4 v[46:49], v[10:17], v[212:219], v[46:49]
	v_mfma_f32_16x16x128_f8f6f4 v[118:121], v[2:9], v[212:219], v[118:121]
	v_mfma_f32_16x16x128_f8f6f4 v[94:97], v[2:9], v[220:227], v[94:97]
	v_mfma_f32_16x16x128_f8f6f4 v[66:69], v[10:17], v[220:227], v[66:69]
	s_setprio 0
	s_barrier
	ds_read_b128 v[2:5], v193
	ds_read_b128 v[6:9], v193 offset:1024
	ds_read_b128 v[10:13], v193 offset:2048
	ds_read_b128 v[14:17], v193 offset:3072
	ds_read_b128 v[196:199], v192
	ds_read_b128 v[200:203], v192 offset:1024
	ds_read_b128 v[204:207], v192 offset:2048
	ds_read_b128 v[208:211], v192 offset:3072
	s_add_u32 s76, s4, 0x10100
	s_addc_u32 s77, s5, 0
	s_mov_b32 m0, s48
	v_lshl_add_u64 v[244:245], s[76:77], 0, v[154:155]
	ds_read_b128 v[212:215], v191 offset:32768
	ds_read_b128 v[216:219], v191 offset:33792
	ds_read_b128 v[220:223], v191 offset:34816
	ds_read_b128 v[224:227], v191 offset:35840
	ds_read_b128 v[228:231], v191 offset:36864
	ds_read_b128 v[232:235], v191 offset:37888
	ds_read_b128 v[236:239], v191 offset:38912
	ds_read_b128 v[240:243], v191 offset:39936
	global_load_lds_dwordx4 v[244:245], off
	v_lshl_add_u64 v[244:245], s[76:77], 0, v[182:183]
	s_mov_b32 m0, s49
	s_nop 0
	global_load_lds_dwordx4 v[244:245], off
	s_waitcnt vmcnt(8) lgkmcnt(0)
	s_barrier
	s_setprio 1
	v_mfma_f32_16x16x128_f8f6f4 v[42:45], v[10:17], v[220:227], v[42:45]
	v_mfma_f32_16x16x128_f8f6f4 v[90:93], v[2:9], v[220:227], v[90:93]
	v_mfma_f32_16x16x128_f8f6f4 v[30:33], v[2:9], v[212:219], v[30:33]
	v_mfma_f32_16x16x128_f8f6f4 v[150:153], v[10:17], v[212:219], v[150:153]
	v_mfma_f32_16x16x128_f8f6f4 v[62:65], v[10:17], v[228:235], v[62:65]
	v_mfma_f32_16x16x128_f8f6f4 v[114:117], v[2:9], v[228:235], v[114:117]
	v_mfma_f32_16x16x128_f8f6f4 v[78:81], v[2:9], v[236:243], v[78:81]
	v_mfma_f32_16x16x128_f8f6f4 v[50:53], v[10:17], v[236:243], v[50:53]
	v_mfma_f32_16x16x128_f8f6f4 v[22:25], v[196:203], v[236:243], v[22:25]
	v_mfma_f32_16x16x128_f8f6f4 v[74:77], v[204:211], v[236:243], v[74:77]
	v_mfma_f32_16x16x128_f8f6f4 v[146:149], v[204:211], v[212:219], v[146:149]
	v_mfma_f32_16x16x128_f8f6f4 v[142:145], v[196:203], v[212:219], v[142:145]
	v_mfma_f32_16x16x128_f8f6f4 v[26:29], v[196:203], v[220:227], v[26:29]
	v_mfma_f32_16x16x128_f8f6f4 v[138:141], v[204:211], v[220:227], v[138:141]
	v_mfma_f32_16x16x128_f8f6f4 v[126:129], v[204:211], v[228:235], v[126:129]
	v_mfma_f32_16x16x128_f8f6f4 v[38:41], v[196:203], v[228:235], v[38:41]
	s_setprio 0
	s_barrier
	s_mov_b32 m0, s9
	v_lshl_add_u64 v[244:245], v[180:181], 0, s[38:39]
	ds_read_b128 v[212:215], v191 offset:49152
	ds_read_b128 v[216:219], v191 offset:50176
	ds_read_b128 v[220:223], v191 offset:51200
	ds_read_b128 v[224:227], v191 offset:52224
	ds_read_b128 v[228:231], v191 offset:53248
	ds_read_b128 v[232:235], v191 offset:54272
	ds_read_b128 v[236:239], v191 offset:55296
	ds_read_b128 v[240:243], v191 offset:56320
	global_load_lds_dwordx4 v[244:245], off
	v_lshl_add_u64 v[244:245], v[178:179], 0, s[38:39]
	s_mov_b32 m0, s19
	s_nop 0
	global_load_lds_dwordx4 v[244:245], off
	v_lshl_add_u64 v[244:245], s[28:29], 0, v[154:155]
	s_mov_b32 m0, s44
	s_nop 0
	global_load_lds_dwordx4 v[244:245], off
	v_lshl_add_u64 v[244:245], s[28:29], 0, v[182:183]
	s_mov_b32 m0, s45
	s_nop 0
	global_load_lds_dwordx4 v[244:245], off
	v_lshl_add_u64 v[244:245], v[172:173], 0, s[38:39]
	s_mov_b32 m0, s18
	s_nop 0
	global_load_lds_dwordx4 v[244:245], off
	v_lshl_add_u64 v[244:245], v[170:171], 0, s[38:39]
	s_mov_b32 m0, s43
	s_nop 0
	global_load_lds_dwordx4 v[244:245], off
	s_waitcnt vmcnt(8) lgkmcnt(0)
	s_barrier
	s_setprio 1
	v_mfma_f32_16x16x128_f8f6f4 v[110:113], v[2:9], v[228:235], v[110:113]
	v_mfma_f32_16x16x128_f8f6f4 v[106:109], v[10:17], v[228:235], v[106:109]
	v_mfma_f32_16x16x128_f8f6f4 v[102:105], v[10:17], v[212:219], v[102:105]
	v_mfma_f32_16x16x128_f8f6f4 v[134:137], v[2:9], v[212:219], v[134:137]
	v_mfma_f32_16x16x128_f8f6f4 v[122:125], v[2:9], v[220:227], v[122:125]
	v_mfma_f32_16x16x128_f8f6f4 v[98:101], v[10:17], v[220:227], v[98:101]
	v_mfma_f32_16x16x128_f8f6f4 v[82:85], v[10:17], v[236:243], v[82:85]
	v_mfma_f32_16x16x128_f8f6f4 v[86:89], v[2:9], v[236:243], v[86:89]
	v_mfma_f32_16x16x128_f8f6f4 v[54:57], v[196:203], v[236:243], v[54:57]
	v_mfma_f32_16x16x128_f8f6f4 v[58:61], v[204:211], v[236:243], v[58:61]
	v_mfma_f32_16x16x128_f8f6f4 v[130:133], v[204:211], v[212:219], v[130:133]
	v_mfma_f32_16x16x128_f8f6f4 v[34:37], v[196:203], v[212:219], v[34:37]
	v_mfma_f32_16x16x128_f8f6f4 v[46:49], v[196:203], v[220:227], v[46:49]
	v_mfma_f32_16x16x128_f8f6f4 v[118:121], v[204:211], v[220:227], v[118:121]
	v_mfma_f32_16x16x128_f8f6f4 v[94:97], v[204:211], v[228:235], v[94:97]
	v_mfma_f32_16x16x128_f8f6f4 v[66:69], v[196:203], v[228:235], v[66:69]
	s_setprio 0
	s_barrier
	ds_read_b128 v[2:5], v195
	ds_read_b128 v[6:9], v195 offset:1024
	ds_read_b128 v[10:13], v195 offset:2048
	ds_read_b128 v[14:17], v195 offset:3072
	ds_read_b128 v[196:199], v194
	ds_read_b128 v[200:203], v194 offset:1024
	ds_read_b128 v[204:207], v194 offset:2048
	ds_read_b128 v[208:211], v194 offset:3072
	s_add_u32 s4, s4, 0x10180
	s_addc_u32 s5, s5, 0
	s_mov_b32 m0, s74
	v_lshl_add_u64 v[194:195], s[4:5], 0, v[154:155]
	ds_read_b128 v[212:215], v191
	ds_read_b128 v[216:219], v191 offset:1024
	ds_read_b128 v[220:223], v191 offset:2048
	ds_read_b128 v[224:227], v191 offset:3072
	ds_read_b128 v[228:231], v191 offset:4096
	ds_read_b128 v[232:235], v191 offset:5120
	ds_read_b128 v[236:239], v191 offset:6144
	ds_read_b128 v[240:243], v191 offset:7168
	global_load_lds_dwordx4 v[194:195], off
	v_lshl_add_u64 v[182:183], s[4:5], 0, v[182:183]
	s_mov_b32 m0, s69
	s_nop 0
	global_load_lds_dwordx4 v[182:183], off
	s_waitcnt vmcnt(8) lgkmcnt(0)
	s_barrier
	s_setprio 1
	v_mfma_f32_16x16x128_f8f6f4 v[114:117], v[2:9], v[228:235], v[114:117]
	v_mfma_f32_16x16x128_f8f6f4 v[62:65], v[10:17], v[228:235], v[62:65]
	v_mfma_f32_16x16x128_f8f6f4 v[150:153], v[10:17], v[212:219], v[150:153]
	v_mfma_f32_16x16x128_f8f6f4 v[30:33], v[2:9], v[212:219], v[30:33]
	v_mfma_f32_16x16x128_f8f6f4 v[90:93], v[2:9], v[220:227], v[90:93]
	v_mfma_f32_16x16x128_f8f6f4 v[42:45], v[10:17], v[220:227], v[42:45]
	v_mfma_f32_16x16x128_f8f6f4 v[50:53], v[10:17], v[236:243], v[50:53]
	v_mfma_f32_16x16x128_f8f6f4 v[78:81], v[2:9], v[236:243], v[78:81]
	v_mfma_f32_16x16x128_f8f6f4 v[22:25], v[196:203], v[236:243], v[22:25]
	v_mfma_f32_16x16x128_f8f6f4 v[74:77], v[204:211], v[236:243], v[74:77]
	v_mfma_f32_16x16x128_f8f6f4 v[146:149], v[204:211], v[212:219], v[146:149]
	v_mfma_f32_16x16x128_f8f6f4 v[142:145], v[196:203], v[212:219], v[142:145]
	v_mfma_f32_16x16x128_f8f6f4 v[26:29], v[196:203], v[220:227], v[26:29]
	v_mfma_f32_16x16x128_f8f6f4 v[138:141], v[204:211], v[220:227], v[138:141]
	v_mfma_f32_16x16x128_f8f6f4 v[126:129], v[204:211], v[228:235], v[126:129]
	v_mfma_f32_16x16x128_f8f6f4 v[38:41], v[196:203], v[228:235], v[38:41]
	s_setprio 0
	s_barrier
	s_mov_b32 m0, s70
	ds_read_b128 v[212:215], v191 offset:16384
	ds_read_b128 v[216:219], v191 offset:17408
	ds_read_b128 v[220:223], v191 offset:18432
	ds_read_b128 v[224:227], v191 offset:19456
	ds_read_b128 v[228:231], v191 offset:20480
	ds_read_b128 v[232:235], v191 offset:21504
	ds_read_b128 v[236:239], v191 offset:22528
	ds_read_b128 v[240:243], v191 offset:23552
	global_load_lds_dwordx4 v[180:181], off
	s_mov_b32 m0, s71
	s_nop 0
	global_load_lds_dwordx4 v[178:179], off
	s_mov_b32 m0, s72
	s_nop 0
	global_load_lds_dwordx4 v[176:177], off
	s_mov_b32 m0, s73
	s_nop 0
	global_load_lds_dwordx4 v[174:175], off
	s_mov_b32 m0, s67
	s_nop 0
	global_load_lds_dwordx4 v[172:173], off
	s_mov_b32 m0, s68
	s_nop 0
	global_load_lds_dwordx4 v[170:171], off
	s_waitcnt vmcnt(8) lgkmcnt(0)
	s_barrier
	s_setprio 1
	v_mfma_f32_16x16x128_f8f6f4 v[110:113], v[2:9], v[228:235], v[110:113]
	v_mfma_f32_16x16x128_f8f6f4 v[106:109], v[10:17], v[228:235], v[106:109]
	v_mfma_f32_16x16x128_f8f6f4 v[102:105], v[10:17], v[212:219], v[102:105]
	v_mfma_f32_16x16x128_f8f6f4 v[134:137], v[2:9], v[212:219], v[134:137]
	v_mfma_f32_16x16x128_f8f6f4 v[122:125], v[2:9], v[220:227], v[122:125]
	v_mfma_f32_16x16x128_f8f6f4 v[98:101], v[10:17], v[220:227], v[98:101]
	v_mfma_f32_16x16x128_f8f6f4 v[82:85], v[10:17], v[236:243], v[82:85]
	v_mfma_f32_16x16x128_f8f6f4 v[86:89], v[2:9], v[236:243], v[86:89]
	v_mfma_f32_16x16x128_f8f6f4 v[54:57], v[196:203], v[236:243], v[54:57]
	v_mfma_f32_16x16x128_f8f6f4 v[58:61], v[204:211], v[236:243], v[58:61]
	v_mfma_f32_16x16x128_f8f6f4 v[130:133], v[204:211], v[212:219], v[130:133]
	v_mfma_f32_16x16x128_f8f6f4 v[34:37], v[196:203], v[212:219], v[34:37]
	v_mfma_f32_16x16x128_f8f6f4 v[46:49], v[196:203], v[220:227], v[46:49]
	v_mfma_f32_16x16x128_f8f6f4 v[118:121], v[204:211], v[220:227], v[118:121]
	v_mfma_f32_16x16x128_f8f6f4 v[94:97], v[204:211], v[228:235], v[94:97]
	v_mfma_f32_16x16x128_f8f6f4 v[66:69], v[196:203], v[228:235], v[66:69]
	s_setprio 0
	s_barrier
	ds_read_b128 v[2:5], v193
	ds_read_b128 v[6:9], v193 offset:1024
	ds_read_b128 v[10:13], v193 offset:2048
	ds_read_b128 v[14:17], v193 offset:3072
	ds_read_b128 v[170:173], v192
	ds_read_b128 v[174:177], v192 offset:1024
	ds_read_b128 v[194:197], v192 offset:2048
	ds_read_b128 v[198:201], v192 offset:3072
	s_mov_b32 m0, s48
	ds_read_b128 v[202:205], v191 offset:32768
	ds_read_b128 v[206:209], v191 offset:33792
	ds_read_b128 v[210:213], v191 offset:34816
	ds_read_b128 v[214:217], v191 offset:35840
	ds_read_b128 v[218:221], v191 offset:36864
	ds_read_b128 v[222:225], v191 offset:37888
	ds_read_b128 v[226:229], v191 offset:38912
	ds_read_b128 v[230:233], v191 offset:39936
	global_load_lds_dwordx4 v[166:167], off
	s_mov_b32 m0, s49
	s_nop 0
	global_load_lds_dwordx4 v[168:169], off
	s_waitcnt vmcnt(8) lgkmcnt(0)
	s_barrier
	s_setprio 1
	v_mfma_f32_16x16x128_f8f6f4 v[30:33], v[2:9], v[202:209], v[30:33]
	v_mfma_f32_16x16x128_f8f6f4 v[150:153], v[10:17], v[202:209], v[150:153]
	v_mfma_f32_16x16x128_f8f6f4 v[42:45], v[10:17], v[210:217], v[42:45]
	v_mfma_f32_16x16x128_f8f6f4 v[90:93], v[2:9], v[210:217], v[90:93]
	v_mfma_f32_16x16x128_f8f6f4 v[114:117], v[2:9], v[218:225], v[114:117]
	v_mfma_f32_16x16x128_f8f6f4 v[62:65], v[10:17], v[218:225], v[62:65]
	v_mfma_f32_16x16x128_f8f6f4 v[50:53], v[10:17], v[226:233], v[50:53]
	v_mfma_f32_16x16x128_f8f6f4 v[78:81], v[2:9], v[226:233], v[78:81]
	v_mfma_f32_16x16x128_f8f6f4 v[22:25], v[170:177], v[226:233], v[22:25]
	v_mfma_f32_16x16x128_f8f6f4 v[74:77], v[194:201], v[226:233], v[74:77]
	v_mfma_f32_16x16x128_f8f6f4 v[146:149], v[194:201], v[202:209], v[146:149]
	v_mfma_f32_16x16x128_f8f6f4 v[142:145], v[170:177], v[202:209], v[142:145]
	v_mfma_f32_16x16x128_f8f6f4 v[26:29], v[170:177], v[210:217], v[26:29]
	v_mfma_f32_16x16x128_f8f6f4 v[138:141], v[194:201], v[210:217], v[138:141]
	v_mfma_f32_16x16x128_f8f6f4 v[126:129], v[194:201], v[218:225], v[126:129]
	v_mfma_f32_16x16x128_f8f6f4 v[38:41], v[170:177], v[218:225], v[38:41]
	s_setprio 0
	s_barrier
	s_mov_b32 m0, s9
	ds_read_b128 v[202:205], v191 offset:49152
	ds_read_b128 v[206:209], v191 offset:50176
	ds_read_b128 v[210:213], v191 offset:51200
	ds_read_b128 v[214:217], v191 offset:52224
	ds_read_b128 v[218:221], v191 offset:53248
	ds_read_b128 v[222:225], v191 offset:54272
	ds_read_b128 v[226:229], v191 offset:55296
	ds_read_b128 v[230:233], v191 offset:56320
	global_load_lds_dwordx4 v[72:73], off
	s_mov_b32 m0, s19
	s_nop 0
	global_load_lds_dwordx4 v[158:159], off
	s_mov_b32 m0, s44
	s_nop 0
	global_load_lds_dwordx4 v[162:163], off
	s_mov_b32 m0, s45
	s_nop 0
	global_load_lds_dwordx4 v[164:165], off
	s_mov_b32 m0, s18
	s_nop 0
	global_load_lds_dwordx4 v[70:71], off
	s_mov_b32 m0, s43
	s_nop 0
	global_load_lds_dwordx4 v[160:161], off
	s_waitcnt vmcnt(8) lgkmcnt(0)
	s_barrier
	s_setprio 1
	v_mfma_f32_16x16x128_f8f6f4 v[110:113], v[2:9], v[218:225], v[110:113]
	v_mfma_f32_16x16x128_f8f6f4 v[106:109], v[10:17], v[218:225], v[106:109]
	v_mfma_f32_16x16x128_f8f6f4 v[102:105], v[10:17], v[202:209], v[102:105]
	v_mfma_f32_16x16x128_f8f6f4 v[134:137], v[2:9], v[202:209], v[134:137]
	v_mfma_f32_16x16x128_f8f6f4 v[122:125], v[2:9], v[210:217], v[122:125]
	v_mfma_f32_16x16x128_f8f6f4 v[98:101], v[10:17], v[210:217], v[98:101]
	v_mfma_f32_16x16x128_f8f6f4 v[82:85], v[10:17], v[226:233], v[82:85]
	v_mfma_f32_16x16x128_f8f6f4 v[86:89], v[2:9], v[226:233], v[86:89]
	v_mfma_f32_16x16x128_f8f6f4 v[54:57], v[170:177], v[226:233], v[54:57]
	v_mfma_f32_16x16x128_f8f6f4 v[58:61], v[194:201], v[226:233], v[58:61]
	v_mfma_f32_16x16x128_f8f6f4 v[130:133], v[194:201], v[202:209], v[130:133]
	v_mfma_f32_16x16x128_f8f6f4 v[34:37], v[170:177], v[202:209], v[34:37]
	v_mfma_f32_16x16x128_f8f6f4 v[46:49], v[170:177], v[210:217], v[46:49]
	v_mfma_f32_16x16x128_f8f6f4 v[118:121], v[194:201], v[210:217], v[118:121]
	v_mfma_f32_16x16x128_f8f6f4 v[94:97], v[194:201], v[218:225], v[94:97]
	v_mfma_f32_16x16x128_f8f6f4 v[66:69], v[170:177], v[218:225], v[66:69]
	s_setprio 0
	s_barrier
	s_waitcnt vmcnt(0)
	s_cmpk_gt_u32 s65, 0xff
	s_cbranch_scc1 .LBB0_1439
	s_barrier

.LBB0_1558:
	s_add_u32 s39, s30, s38
	s_addc_u32 s44, s31, 0
	s_add_u32 s42, s39, 0x100
	s_addc_u32 s43, s44, 0
	s_and_b64 s[40:41], s[36:37], exec
	s_cselect_b32 s41, s18, s43
	s_cselect_b32 s40, s19, s42
	s_add_u32 s38, s28, s38
	s_addc_u32 s42, s29, 0
	s_add_u32 s38, s38, 0x100
	s_addc_u32 s42, s42, 0
	s_and_b64 s[36:37], s[36:37], exec
	s_cselect_b32 s43, s17, s42
	s_cselect_b32 s42, s21, s38
	s_add_u32 s76, s39, 0x10080
	ds_read_b128 v[26:29], v181
	ds_read_b128 v[30:33], v181 offset:1024
	ds_read_b128 v[18:21], v181 offset:2048
	ds_read_b128 v[22:25], v181 offset:3072
	ds_read_b128 v[10:13], v182
	ds_read_b128 v[14:17], v182 offset:1024
	ds_read_b128 v[2:5], v182 offset:2048
	ds_read_b128 v[6:9], v182 offset:3072
	s_addc_u32 s77, s44, 0
	s_add_i32 s75, s63, s15
	s_add_i32 m0, s27, 0xc000
	s_add_i32 s78, s27, 0xe000
	s_add_i32 s72, s75, 0x2000
	s_add_u32 s44, s42, 0x10000
	s_addc_u32 s45, s43, 0
	s_add_i32 s74, s64, s15
	s_add_i32 s73, s74, 0x2000
	s_add_i32 s71, 0, 0x18000
	s_add_i32 s70, 0, 0x1c000
	s_add_u32 s38, s40, 0x10000
	s_addc_u32 s39, s41, 0
	s_add_i32 s69, s71, s15
	s_add_i32 s67, s69, 0x2000
	s_add_u32 s36, s42, 0x10080
	s_addc_u32 s37, s43, 0
	s_add_i32 s68, s70, s15
	s_add_i32 s66, s68, 0x2000
	v_lshl_add_u64 v[208:209], s[76:77], 0, v[164:165]
	ds_read_b128 v[170:173], v183
	ds_read_b128 v[174:177], v183 offset:1024
	ds_read_b128 v[184:187], v183 offset:2048
	ds_read_b128 v[188:191], v183 offset:3072
	ds_read_b128 v[192:195], v183 offset:4096
	ds_read_b128 v[196:199], v183 offset:5120
	ds_read_b128 v[200:203], v183 offset:6144
	ds_read_b128 v[204:207], v183 offset:7168
	global_load_lds_dwordx4 v[208:209], off
	v_lshl_add_u64 v[208:209], s[76:77], 0, v[162:163]
	s_mov_b32 m0, s78
	s_nop 0
	global_load_lds_dwordx4 v[208:209], off
	s_waitcnt vmcnt(8) lgkmcnt(0)
	s_barrier
	s_setprio 1
	v_mfma_f32_16x16x128_f8f6f4 v[158:161], v[26:33], v[170:177], v[158:161]
	v_mfma_f32_16x16x128_f8f6f4 v[154:157], v[18:25], v[170:177], v[154:157]
	v_mfma_f32_16x16x128_f8f6f4 v[138:141], v[18:25], v[184:191], v[138:141]
	v_mfma_f32_16x16x128_f8f6f4 v[142:145], v[26:33], v[184:191], v[142:145]
	v_mfma_f32_16x16x128_f8f6f4 v[126:129], v[26:33], v[192:199], v[126:129]
	v_mfma_f32_16x16x128_f8f6f4 v[122:125], v[18:25], v[192:199], v[122:125]
	v_mfma_f32_16x16x128_f8f6f4 v[106:109], v[18:25], v[200:207], v[106:109]
	v_mfma_f32_16x16x128_f8f6f4 v[110:113], v[26:33], v[200:207], v[110:113]
	v_mfma_f32_16x16x128_f8f6f4 v[102:105], v[10:17], v[200:207], v[102:105]
	v_mfma_f32_16x16x128_f8f6f4 v[98:101], v[2:9], v[200:207], v[98:101]
	v_mfma_f32_16x16x128_f8f6f4 v[146:149], v[2:9], v[170:177], v[146:149]
	v_mfma_f32_16x16x128_f8f6f4 v[150:153], v[10:17], v[170:177], v[150:153]
	v_mfma_f32_16x16x128_f8f6f4 v[134:137], v[10:17], v[184:191], v[134:137]
	v_mfma_f32_16x16x128_f8f6f4 v[130:133], v[2:9], v[184:191], v[130:133]
	v_mfma_f32_16x16x128_f8f6f4 v[114:117], v[2:9], v[192:199], v[114:117]
	v_mfma_f32_16x16x128_f8f6f4 v[118:121], v[10:17], v[192:199], v[118:121]
	s_setprio 0
	s_barrier
	s_mov_b32 m0, s75
	v_lshl_add_u64 v[170:171], s[42:43], 0, v[164:165]
	ds_read_b128 v[184:187], v183 offset:16384
	ds_read_b128 v[188:191], v183 offset:17408
	ds_read_b128 v[192:195], v183 offset:18432
	ds_read_b128 v[196:199], v183 offset:19456
	ds_read_b128 v[200:203], v183 offset:20480
	ds_read_b128 v[204:207], v183 offset:21504
	ds_read_b128 v[208:211], v183 offset:22528
	ds_read_b128 v[212:215], v183 offset:23552
	global_load_lds_dwordx4 v[170:171], off
	v_lshl_add_u64 v[172:173], s[42:43], 0, v[162:163]
	s_mov_b32 m0, s72
	v_lshl_add_u64 v[174:175], s[44:45], 0, v[164:165]
	global_load_lds_dwordx4 v[172:173], off
	s_mov_b32 m0, s74
	v_lshl_add_u64 v[176:177], s[40:41], 0, v[162:163]
	global_load_lds_dwordx4 v[174:175], off
	v_lshl_add_u64 v[174:175], s[44:45], 0, v[162:163]
	s_mov_b32 m0, s73
	s_nop 0
	global_load_lds_dwordx4 v[174:175], off
	v_lshl_add_u64 v[174:175], s[40:41], 0, v[164:165]
	s_mov_b32 m0, s27
	s_nop 0
	global_load_lds_dwordx4 v[174:175], off
	s_mov_b32 m0, s49
	s_nop 0
	global_load_lds_dwordx4 v[176:177], off
	s_waitcnt vmcnt(8) lgkmcnt(0)
	s_barrier
	s_setprio 1
	v_mfma_f32_16x16x128_f8f6f4 v[78:81], v[26:33], v[192:199], v[78:81]
	v_mfma_f32_16x16x128_f8f6f4 v[74:77], v[18:25], v[192:199], v[74:77]
	v_mfma_f32_16x16x128_f8f6f4 v[90:93], v[18:25], v[184:191], v[90:93]
	v_mfma_f32_16x16x128_f8f6f4 v[94:97], v[26:33], v[184:191], v[94:97]
	v_mfma_f32_16x16x128_f8f6f4 v[62:65], v[26:33], v[200:207], v[62:65]
	v_mfma_f32_16x16x128_f8f6f4 v[58:61], v[18:25], v[200:207], v[58:61]
	v_mfma_f32_16x16x128_f8f6f4 v[42:45], v[18:25], v[208:215], v[42:45]
	v_mfma_f32_16x16x128_f8f6f4 v[54:57], v[26:33], v[208:215], v[54:57]
	v_mfma_f32_16x16x128_f8f6f4 v[38:41], v[10:17], v[208:215], v[38:41]
	v_mfma_f32_16x16x128_f8f6f4 v[34:37], v[2:9], v[208:215], v[34:37]
	v_mfma_f32_16x16x128_f8f6f4 v[82:85], v[2:9], v[184:191], v[82:85]
	v_mfma_f32_16x16x128_f8f6f4 v[86:89], v[10:17], v[184:191], v[86:89]
	v_mfma_f32_16x16x128_f8f6f4 v[70:73], v[10:17], v[192:199], v[70:73]
	v_mfma_f32_16x16x128_f8f6f4 v[66:69], v[2:9], v[192:199], v[66:69]
	v_mfma_f32_16x16x128_f8f6f4 v[46:49], v[2:9], v[200:207], v[46:49]
	v_mfma_f32_16x16x128_f8f6f4 v[50:53], v[10:17], v[200:207], v[50:53]
	s_setprio 0
	s_barrier
	v_add_u32_e32 v14, s71, v179
	v_add_u32_e32 v30, s70, v179
	ds_read_b128 v[2:5], v14
	ds_read_b128 v[6:9], v14 offset:1024
	ds_read_b128 v[10:13], v14 offset:2048
	ds_read_b128 v[14:17], v14 offset:3072
	ds_read_b128 v[18:21], v30
	ds_read_b128 v[22:25], v30 offset:1024
	ds_read_b128 v[26:29], v30 offset:2048
	ds_read_b128 v[30:33], v30 offset:3072
	s_mov_b32 m0, s50
	v_lshl_add_u64 v[216:217], s[38:39], 0, v[164:165]
	ds_read_b128 v[184:187], v183 offset:32768
	ds_read_b128 v[188:191], v183 offset:33792
	ds_read_b128 v[192:195], v183 offset:34816
	ds_read_b128 v[196:199], v183 offset:35840
	ds_read_b128 v[200:203], v183 offset:36864
	ds_read_b128 v[204:207], v183 offset:37888
	ds_read_b128 v[208:211], v183 offset:38912
	ds_read_b128 v[212:215], v183 offset:39936
	global_load_lds_dwordx4 v[216:217], off
	v_lshl_add_u64 v[216:217], s[38:39], 0, v[162:163]
	s_mov_b32 m0, s51
	s_nop 0
	global_load_lds_dwordx4 v[216:217], off
	s_waitcnt vmcnt(8) lgkmcnt(0)
	s_barrier
	s_setprio 1
	v_mfma_f32_16x16x128_f8f6f4 v[122:125], v[10:17], v[200:207], v[122:125]
	v_mfma_f32_16x16x128_f8f6f4 v[126:129], v[2:9], v[200:207], v[126:129]
	v_mfma_f32_16x16x128_f8f6f4 v[158:161], v[2:9], v[184:191], v[158:161]
	v_mfma_f32_16x16x128_f8f6f4 v[154:157], v[10:17], v[184:191], v[154:157]
	v_mfma_f32_16x16x128_f8f6f4 v[138:141], v[10:17], v[192:199], v[138:141]
	v_mfma_f32_16x16x128_f8f6f4 v[142:145], v[2:9], v[192:199], v[142:145]
	v_mfma_f32_16x16x128_f8f6f4 v[110:113], v[2:9], v[208:215], v[110:113]
	v_mfma_f32_16x16x128_f8f6f4 v[106:109], v[10:17], v[208:215], v[106:109]
	v_mfma_f32_16x16x128_f8f6f4 v[102:105], v[18:25], v[208:215], v[102:105]
	v_mfma_f32_16x16x128_f8f6f4 v[98:101], v[26:33], v[208:215], v[98:101]
	v_mfma_f32_16x16x128_f8f6f4 v[146:149], v[26:33], v[184:191], v[146:149]
	v_mfma_f32_16x16x128_f8f6f4 v[150:153], v[18:25], v[184:191], v[150:153]
	v_mfma_f32_16x16x128_f8f6f4 v[134:137], v[18:25], v[192:199], v[134:137]
	v_mfma_f32_16x16x128_f8f6f4 v[130:133], v[26:33], v[192:199], v[130:133]
	v_mfma_f32_16x16x128_f8f6f4 v[114:117], v[26:33], v[200:207], v[114:117]
	v_mfma_f32_16x16x128_f8f6f4 v[118:121], v[18:25], v[200:207], v[118:121]
	s_setprio 0
	s_barrier
	s_mov_b32 m0, s69
	v_lshl_add_u64 v[170:171], v[170:171], 0, s[8:9]
	ds_read_b128 v[184:187], v183 offset:49152
	ds_read_b128 v[188:191], v183 offset:50176
	ds_read_b128 v[192:195], v183 offset:51200
	ds_read_b128 v[196:199], v183 offset:52224
	ds_read_b128 v[200:203], v183 offset:53248
	ds_read_b128 v[204:207], v183 offset:54272
	ds_read_b128 v[208:211], v183 offset:55296
	ds_read_b128 v[212:215], v183 offset:56320
	global_load_lds_dwordx4 v[170:171], off
	v_lshl_add_u64 v[170:171], v[172:173], 0, s[8:9]
	s_mov_b32 m0, s67
	s_nop 0
	global_load_lds_dwordx4 v[170:171], off
	v_lshl_add_u64 v[170:171], s[36:37], 0, v[164:165]
	s_mov_b32 m0, s68
	s_nop 0
	global_load_lds_dwordx4 v[170:171], off
	v_lshl_add_u64 v[170:171], s[36:37], 0, v[162:163]
	s_mov_b32 m0, s66
	s_nop 0
	global_load_lds_dwordx4 v[170:171], off
	v_lshl_add_u64 v[170:171], v[174:175], 0, s[8:9]
	s_mov_b32 m0, s61
	s_nop 0
	global_load_lds_dwordx4 v[170:171], off
	v_lshl_add_u64 v[170:171], v[176:177], 0, s[8:9]
	s_mov_b32 m0, s62
	s_nop 0
	global_load_lds_dwordx4 v[170:171], off
	s_waitcnt vmcnt(8) lgkmcnt(0)
	s_barrier
	s_setprio 1
	v_mfma_f32_16x16x128_f8f6f4 v[62:65], v[2:9], v[200:207], v[62:65]
	v_mfma_f32_16x16x128_f8f6f4 v[58:61], v[10:17], v[200:207], v[58:61]
	v_mfma_f32_16x16x128_f8f6f4 v[90:93], v[10:17], v[184:191], v[90:93]
	v_mfma_f32_16x16x128_f8f6f4 v[94:97], v[2:9], v[184:191], v[94:97]
	v_mfma_f32_16x16x128_f8f6f4 v[78:81], v[2:9], v[192:199], v[78:81]
	v_mfma_f32_16x16x128_f8f6f4 v[74:77], v[10:17], v[192:199], v[74:77]
	v_mfma_f32_16x16x128_f8f6f4 v[42:45], v[10:17], v[208:215], v[42:45]
	v_mfma_f32_16x16x128_f8f6f4 v[54:57], v[2:9], v[208:215], v[54:57]
	v_mfma_f32_16x16x128_f8f6f4 v[38:41], v[18:25], v[208:215], v[38:41]
	v_mfma_f32_16x16x128_f8f6f4 v[34:37], v[26:33], v[208:215], v[34:37]
	v_mfma_f32_16x16x128_f8f6f4 v[82:85], v[26:33], v[184:191], v[82:85]
	v_mfma_f32_16x16x128_f8f6f4 v[86:89], v[18:25], v[184:191], v[86:89]
	v_mfma_f32_16x16x128_f8f6f4 v[70:73], v[18:25], v[192:199], v[70:73]
	v_mfma_f32_16x16x128_f8f6f4 v[66:69], v[26:33], v[192:199], v[66:69]
	v_mfma_f32_16x16x128_f8f6f4 v[46:49], v[26:33], v[200:207], v[46:49]
	v_mfma_f32_16x16x128_f8f6f4 v[50:53], v[18:25], v[200:207], v[50:53]
	s_setprio 0
	s_barrier
	s_movk_i32 s38, 0x100
	s_andn2_b64 vcc, exec, s[34:35]
	s_mov_b64 s[36:37], -1
	s_mov_b64 s[34:35], 0
	s_cbranch_vccz .LBB0_1558
	s_and_b64 vcc, exec, s[12:13]
	s_cbranch_vccz .LBB0_1561
	s_barrier

.LBB0_1681:
	ds_read_b128 v[26:29], v189
	ds_read_b128 v[30:33], v189 offset:1024
	ds_read_b128 v[18:21], v189 offset:2048
	ds_read_b128 v[22:25], v189 offset:3072
	ds_read_b128 v[10:13], v190
	ds_read_b128 v[14:17], v190 offset:1024
	ds_read_b128 v[2:5], v190 offset:2048
	ds_read_b128 v[6:9], v190 offset:3072
	s_add_u32 s34, s30, 0xfff80080
	s_addc_u32 s35, s31, -1
	s_cmp_eq_u32 s60, 28
	s_cselect_b32 s37, s18, s35
	s_cselect_b32 s36, s19, s34
	s_cselect_b32 s35, s21, s59
	s_cselect_b32 s34, s23, s58
	s_mov_b32 m0, s43
	s_nop 0
	global_load_lds_dwordx4 v168, s[100:101]
	s_mov_b32 m0, s44
	s_nop 0
	global_load_lds_dwordx4 v164, s[100:101]
	s_add_i32 m0, s29, 0xc000
	ds_read_b128 v[178:181], v191
	ds_read_b128 v[182:185], v191 offset:1024
	ds_read_b128 v[194:197], v191 offset:2048
	ds_read_b128 v[198:201], v191 offset:3072
	ds_read_b128 v[202:205], v191 offset:4096
	ds_read_b128 v[206:209], v191 offset:5120
	ds_read_b128 v[210:213], v191 offset:6144
	ds_read_b128 v[214:217], v191 offset:7168
	global_load_lds_dwordx4 v170, s[30:31]
	s_add_i32 m0, s29, 0xe000
	s_nop 0
	global_load_lds_dwordx4 v172, s[30:31]
	s_waitcnt vmcnt(8) lgkmcnt(0)
	s_barrier
	s_setprio 1
	v_mfma_f32_16x16x128_f8f6f4 v[158:161], v[26:33], v[178:185], v[158:161]
	v_mfma_f32_16x16x128_f8f6f4 v[154:157], v[18:25], v[178:185], v[154:157]
	v_mfma_f32_16x16x128_f8f6f4 v[138:141], v[18:25], v[194:201], v[138:141]
	v_mfma_f32_16x16x128_f8f6f4 v[142:145], v[26:33], v[194:201], v[142:145]
	v_mfma_f32_16x16x128_f8f6f4 v[126:129], v[26:33], v[202:209], v[126:129]
	v_mfma_f32_16x16x128_f8f6f4 v[122:125], v[18:25], v[202:209], v[122:125]
	v_mfma_f32_16x16x128_f8f6f4 v[106:109], v[18:25], v[210:217], v[106:109]
	v_mfma_f32_16x16x128_f8f6f4 v[110:113], v[26:33], v[210:217], v[110:113]
	v_mfma_f32_16x16x128_f8f6f4 v[102:105], v[10:17], v[210:217], v[102:105]
	v_mfma_f32_16x16x128_f8f6f4 v[98:101], v[2:9], v[210:217], v[98:101]
	v_mfma_f32_16x16x128_f8f6f4 v[146:149], v[2:9], v[178:185], v[146:149]
	v_mfma_f32_16x16x128_f8f6f4 v[150:153], v[10:17], v[178:185], v[150:153]
	v_mfma_f32_16x16x128_f8f6f4 v[134:137], v[10:17], v[194:201], v[134:137]
	v_mfma_f32_16x16x128_f8f6f4 v[130:133], v[2:9], v[194:201], v[130:133]
	v_mfma_f32_16x16x128_f8f6f4 v[114:117], v[2:9], v[202:209], v[114:117]
	v_mfma_f32_16x16x128_f8f6f4 v[118:121], v[10:17], v[202:209], v[118:121]
	s_setprio 0
	s_barrier
	s_add_i32 s61, s45, s3
	s_mov_b32 m0, s61
	ds_read_b128 v[194:197], v191 offset:16384
	ds_read_b128 v[198:201], v191 offset:17408
	ds_read_b128 v[202:205], v191 offset:18432
	ds_read_b128 v[206:209], v191 offset:19456
	ds_read_b128 v[210:213], v191 offset:20480
	ds_read_b128 v[214:217], v191 offset:21504
	ds_read_b128 v[218:221], v191 offset:22528
	ds_read_b128 v[222:225], v191 offset:23552
	global_load_lds_dwordx4 v166, s[34:35]
	s_add_i32 m0, s61, 0x2000
	s_add_u32 s62, s34, 0x80000
	s_addc_u32 s63, s35, 0
	s_add_i32 s61, s48, s3
	global_load_lds_dwordx4 v162, s[34:35]
	s_mov_b32 m0, s61
	s_nop 0
	global_load_lds_dwordx4 v166, s[62:63]
	s_add_i32 m0, s61, 0x2000
	s_nop 0
	global_load_lds_dwordx4 v162, s[62:63]
	s_waitcnt vmcnt(6) lgkmcnt(0)
	s_barrier
	s_setprio 1
	v_mfma_f32_16x16x128_f8f6f4 v[78:81], v[26:33], v[202:209], v[78:81]
	v_mfma_f32_16x16x128_f8f6f4 v[74:77], v[18:25], v[202:209], v[74:77]
	v_mfma_f32_16x16x128_f8f6f4 v[90:93], v[18:25], v[194:201], v[90:93]
	v_mfma_f32_16x16x128_f8f6f4 v[94:97], v[26:33], v[194:201], v[94:97]
	v_mfma_f32_16x16x128_f8f6f4 v[62:65], v[26:33], v[210:217], v[62:65]
	v_mfma_f32_16x16x128_f8f6f4 v[58:61], v[18:25], v[210:217], v[58:61]
	v_mfma_f32_16x16x128_f8f6f4 v[42:45], v[18:25], v[218:225], v[42:45]
	v_mfma_f32_16x16x128_f8f6f4 v[46:49], v[26:33], v[218:225], v[46:49]
	v_mfma_f32_16x16x128_f8f6f4 v[38:41], v[10:17], v[218:225], v[38:41]
	v_mfma_f32_16x16x128_f8f6f4 v[34:37], v[2:9], v[218:225], v[34:37]
	v_mfma_f32_16x16x128_f8f6f4 v[82:85], v[2:9], v[194:201], v[82:85]
	v_mfma_f32_16x16x128_f8f6f4 v[86:89], v[10:17], v[194:201], v[86:89]
	v_mfma_f32_16x16x128_f8f6f4 v[70:73], v[10:17], v[202:209], v[70:73]
	v_mfma_f32_16x16x128_f8f6f4 v[66:69], v[2:9], v[202:209], v[66:69]
	v_mfma_f32_16x16x128_f8f6f4 v[50:53], v[2:9], v[210:217], v[50:53]
	v_mfma_f32_16x16x128_f8f6f4 v[54:57], v[10:17], v[210:217], v[54:57]
	s_setprio 0
	s_barrier
	s_add_i32 s61, 0, 0x18000
	s_add_i32 s62, 0, 0x1c000
	v_add_u32_e32 v14, s61, v187
	v_add_u32_e32 v30, s62, v187
	ds_read_b128 v[2:5], v14
	ds_read_b128 v[6:9], v14 offset:1024
	ds_read_b128 v[10:13], v14 offset:2048
	ds_read_b128 v[14:17], v14 offset:3072
	ds_read_b128 v[18:21], v30
	ds_read_b128 v[22:25], v30 offset:1024
	ds_read_b128 v[26:29], v30 offset:2048
	ds_read_b128 v[30:33], v30 offset:3072
	s_mov_b32 m0, s29
	s_nop 0
	global_load_lds_dwordx4 v168, s[36:37]
	s_mov_b32 m0, s38
	s_nop 0
	global_load_lds_dwordx4 v164, s[36:37]
	s_add_u32 s36, s36, 0x80000
	s_addc_u32 s37, s37, 0
	s_add_u32 s100, s36, 0xfff80080
	s_addc_u32 s101, s37, -1
	s_mov_b32 m0, s39
	ds_read_b128 v[194:197], v191 offset:32768
	ds_read_b128 v[198:201], v191 offset:33792
	ds_read_b128 v[202:205], v191 offset:34816
	ds_read_b128 v[206:209], v191 offset:35840
	ds_read_b128 v[210:213], v191 offset:36864
	ds_read_b128 v[214:217], v191 offset:37888
	ds_read_b128 v[218:221], v191 offset:38912
	ds_read_b128 v[222:225], v191 offset:39936
	global_load_lds_dwordx4 v168, s[36:37]
	s_mov_b32 m0, s40
	s_nop 0
	global_load_lds_dwordx4 v164, s[36:37]
	s_waitcnt vmcnt(8) lgkmcnt(0)
	s_barrier
	s_setprio 1
	v_mfma_f32_16x16x128_f8f6f4 v[122:125], v[10:17], v[210:217], v[122:125]
	v_mfma_f32_16x16x128_f8f6f4 v[126:129], v[2:9], v[210:217], v[126:129]
	v_mfma_f32_16x16x128_f8f6f4 v[158:161], v[2:9], v[194:201], v[158:161]
	v_mfma_f32_16x16x128_f8f6f4 v[154:157], v[10:17], v[194:201], v[154:157]
	v_mfma_f32_16x16x128_f8f6f4 v[138:141], v[10:17], v[202:209], v[138:141]
	v_mfma_f32_16x16x128_f8f6f4 v[142:145], v[2:9], v[202:209], v[142:145]
	v_mfma_f32_16x16x128_f8f6f4 v[110:113], v[2:9], v[218:225], v[110:113]
	v_mfma_f32_16x16x128_f8f6f4 v[106:109], v[10:17], v[218:225], v[106:109]
	v_mfma_f32_16x16x128_f8f6f4 v[102:105], v[18:25], v[218:225], v[102:105]
	v_mfma_f32_16x16x128_f8f6f4 v[98:101], v[26:33], v[218:225], v[98:101]
	v_mfma_f32_16x16x128_f8f6f4 v[146:149], v[26:33], v[194:201], v[146:149]
	v_mfma_f32_16x16x128_f8f6f4 v[150:153], v[18:25], v[194:201], v[150:153]
	v_mfma_f32_16x16x128_f8f6f4 v[134:137], v[18:25], v[202:209], v[134:137]
	v_mfma_f32_16x16x128_f8f6f4 v[130:133], v[26:33], v[202:209], v[130:133]
	v_mfma_f32_16x16x128_f8f6f4 v[114:117], v[26:33], v[210:217], v[114:117]
	v_mfma_f32_16x16x128_f8f6f4 v[118:121], v[18:25], v[210:217], v[118:121]
	s_setprio 0
	s_barrier
	s_add_i32 s36, s61, s3
	s_mov_b32 m0, s36
	s_add_u32 s98, s34, 0x80
	s_addc_u32 s99, s35, 0
	ds_read_b128 v[194:197], v191 offset:49152
	ds_read_b128 v[198:201], v191 offset:50176
	ds_read_b128 v[202:205], v191 offset:51200
	ds_read_b128 v[206:209], v191 offset:52224
	ds_read_b128 v[210:213], v191 offset:53248
	ds_read_b128 v[214:217], v191 offset:54272
	ds_read_b128 v[218:221], v191 offset:55296
	ds_read_b128 v[222:225], v191 offset:56320
	global_load_lds_dwordx4 v166, s[98:99]
	s_add_i32 m0, s36, 0x2000
	s_add_u32 s34, s34, 0x80080
	s_addc_u32 s35, s35, 0
	s_add_i32 s36, s62, s3
	global_load_lds_dwordx4 v162, s[98:99]
	s_mov_b32 m0, s36
	s_nop 0
	global_load_lds_dwordx4 v166, s[34:35]
	s_add_i32 m0, s36, 0x2000
	s_nop 0
	global_load_lds_dwordx4 v162, s[34:35]
	s_waitcnt vmcnt(6) lgkmcnt(0)
	s_barrier
	s_setprio 1
	v_mfma_f32_16x16x128_f8f6f4 v[62:65], v[2:9], v[210:217], v[62:65]
	v_mfma_f32_16x16x128_f8f6f4 v[58:61], v[10:17], v[210:217], v[58:61]
	v_mfma_f32_16x16x128_f8f6f4 v[90:93], v[10:17], v[194:201], v[90:93]
	v_mfma_f32_16x16x128_f8f6f4 v[94:97], v[2:9], v[194:201], v[94:97]
	v_mfma_f32_16x16x128_f8f6f4 v[78:81], v[2:9], v[202:209], v[78:81]
	v_mfma_f32_16x16x128_f8f6f4 v[74:77], v[10:17], v[202:209], v[74:77]
	v_mfma_f32_16x16x128_f8f6f4 v[42:45], v[10:17], v[218:225], v[42:45]
	v_mfma_f32_16x16x128_f8f6f4 v[46:49], v[2:9], v[218:225], v[46:49]
	v_mfma_f32_16x16x128_f8f6f4 v[38:41], v[18:25], v[218:225], v[38:41]
	v_mfma_f32_16x16x128_f8f6f4 v[34:37], v[26:33], v[218:225], v[34:37]
	v_mfma_f32_16x16x128_f8f6f4 v[82:85], v[26:33], v[194:201], v[82:85]
	v_mfma_f32_16x16x128_f8f6f4 v[86:89], v[18:25], v[194:201], v[86:89]
	v_mfma_f32_16x16x128_f8f6f4 v[70:73], v[18:25], v[202:209], v[70:73]
	v_mfma_f32_16x16x128_f8f6f4 v[66:69], v[26:33], v[202:209], v[66:69]
	v_mfma_f32_16x16x128_f8f6f4 v[50:53], v[26:33], v[210:217], v[50:53]
	v_mfma_f32_16x16x128_f8f6f4 v[54:57], v[18:25], v[210:217], v[54:57]
	s_setprio 0
	s_barrier
	s_add_i32 s60, s60, 2
	s_add_u32 s30, s30, 0x100
	s_addc_u32 s31, s31, 0
	s_add_u32 s58, s58, 0x100
	s_addc_u32 s59, s59, 0
	s_cmp_gt_u32 s60, 29
	s_cbranch_scc0 .LBB0_1681
	s_and_b64 vcc, exec, s[12:13]
	s_cbranch_vccz .LBB0_1684
	s_barrier

.LBB0_1745:
	s_add_u32 s8, s49, s6
	s_addc_u32 s9, s50, s7
	s_add_u32 s8, s8, 0x32800100
	s_addc_u32 s9, s9, 0
	s_add_u32 s73, s51, s6
	s_addc_u32 s74, s54, s7
	s_add_i32 s72, 0, 0x10000
	s_cmpk_eq_i32 s6, 0x2a00
	s_cselect_b32 s37, s5, s9
	s_cselect_b32 s36, s4, s8
	s_cselect_b32 s9, s13, s74
	s_cselect_b32 s8, s12, s73
	s_add_i32 s73, 0, 0x14000
	v_add_u32_e32 v2, s72, v188
	v_add_u32_e32 v6, s73, v188
	ds_read_b128 v[26:29], v2
	ds_read_b128 v[30:33], v2 offset:1024
	ds_read_b128 v[18:21], v2 offset:2048
	ds_read_b128 v[22:25], v2 offset:3072
	ds_read_b128 v[10:13], v6
	ds_read_b128 v[14:17], v6 offset:1024
	ds_read_b128 v[2:5], v6 offset:2048
	ds_read_b128 v[6:9], v6 offset:3072
	v_lshl_add_u64 v[214:215], v[168:169], 0, s[6:7]
	s_add_i32 m0, s64, 0xc000
	ds_read_b128 v[172:175], v189
	ds_read_b128 v[176:179], v189 offset:1024
	ds_read_b128 v[190:193], v189 offset:2048
	ds_read_b128 v[194:197], v189 offset:3072
	ds_read_b128 v[198:201], v189 offset:4096
	ds_read_b128 v[202:205], v189 offset:5120
	ds_read_b128 v[206:209], v189 offset:6144
	ds_read_b128 v[210:213], v189 offset:7168
	global_load_lds_dwordx4 v[214:215], off
	v_lshl_add_u64 v[214:215], v[170:171], 0, s[6:7]
	s_add_i32 m0, s64, 0xe000
	s_nop 0
	global_load_lds_dwordx4 v[214:215], off
	s_waitcnt vmcnt(8) lgkmcnt(0)
	s_barrier
	s_setprio 1
	v_mfma_f32_16x16x128_f8f6f4 v[158:161], v[26:33], v[172:179], v[158:161]
	v_mfma_f32_16x16x128_f8f6f4 v[154:157], v[18:25], v[172:179], v[154:157]
	v_mfma_f32_16x16x128_f8f6f4 v[118:121], v[18:25], v[190:197], v[118:121]
	v_mfma_f32_16x16x128_f8f6f4 v[122:125], v[26:33], v[190:197], v[122:125]
	v_mfma_f32_16x16x128_f8f6f4 v[126:129], v[26:33], v[198:205], v[126:129]
	v_mfma_f32_16x16x128_f8f6f4 v[114:117], v[18:25], v[198:205], v[114:117]
	v_mfma_f32_16x16x128_f8f6f4 v[106:109], v[18:25], v[206:213], v[106:109]
	v_mfma_f32_16x16x128_f8f6f4 v[110:113], v[26:33], v[206:213], v[110:113]
	v_mfma_f32_16x16x128_f8f6f4 v[102:105], v[10:17], v[206:213], v[102:105]
	v_mfma_f32_16x16x128_f8f6f4 v[98:101], v[2:9], v[206:213], v[98:101]
	v_mfma_f32_16x16x128_f8f6f4 v[146:149], v[2:9], v[172:179], v[146:149]
	v_mfma_f32_16x16x128_f8f6f4 v[150:153], v[10:17], v[172:179], v[150:153]
	v_mfma_f32_16x16x128_f8f6f4 v[142:145], v[10:17], v[190:197], v[142:145]
	v_mfma_f32_16x16x128_f8f6f4 v[138:141], v[2:9], v[190:197], v[138:141]
	v_mfma_f32_16x16x128_f8f6f4 v[130:133], v[2:9], v[198:205], v[130:133]
	v_mfma_f32_16x16x128_f8f6f4 v[134:137], v[10:17], v[198:205], v[134:137]
	s_setprio 0
	s_barrier
	s_add_i32 s72, s72, s43
	v_lshl_add_u64 v[172:173], s[8:9], 0, v[162:163]
	s_mov_b32 m0, s72
	ds_read_b128 v[190:193], v189 offset:16384
	ds_read_b128 v[194:197], v189 offset:17408
	ds_read_b128 v[198:201], v189 offset:18432
	ds_read_b128 v[202:205], v189 offset:19456
	ds_read_b128 v[206:209], v189 offset:20480
	ds_read_b128 v[210:213], v189 offset:21504
	ds_read_b128 v[214:217], v189 offset:22528
	ds_read_b128 v[218:221], v189 offset:23552
	global_load_lds_dwordx4 v[172:173], off
	s_add_i32 m0, s72, 0x2000
	s_add_u32 s74, s8, 0x158000
	v_lshl_add_u64 v[174:175], s[8:9], 0, v[166:167]
	s_addc_u32 s75, s9, 0
	s_add_i32 s72, s73, s43
	global_load_lds_dwordx4 v[174:175], off
	v_lshl_add_u64 v[176:177], s[74:75], 0, v[162:163]
	s_mov_b32 m0, s72
	v_lshl_add_u64 v[178:179], s[36:37], 0, v[166:167]
	global_load_lds_dwordx4 v[176:177], off
	v_lshl_add_u64 v[176:177], s[74:75], 0, v[166:167]
	s_add_i32 m0, s72, 0x2000
	s_nop 0
	global_load_lds_dwordx4 v[176:177], off
	v_lshl_add_u64 v[176:177], s[36:37], 0, v[162:163]
	s_mov_b32 m0, s64
	s_nop 0
	global_load_lds_dwordx4 v[176:177], off
	s_mov_b32 m0, s65
	s_nop 0
	global_load_lds_dwordx4 v[178:179], off
	s_waitcnt vmcnt(8) lgkmcnt(0)
	s_barrier
	s_setprio 1
	v_mfma_f32_16x16x128_f8f6f4 v[78:81], v[26:33], v[198:205], v[78:81]
	v_mfma_f32_16x16x128_f8f6f4 v[74:77], v[18:25], v[198:205], v[74:77]
	v_mfma_f32_16x16x128_f8f6f4 v[90:93], v[18:25], v[190:197], v[90:93]
	v_mfma_f32_16x16x128_f8f6f4 v[94:97], v[26:33], v[190:197], v[94:97]
	v_mfma_f32_16x16x128_f8f6f4 v[62:65], v[26:33], v[206:213], v[62:65]
	v_mfma_f32_16x16x128_f8f6f4 v[58:61], v[18:25], v[206:213], v[58:61]
	v_mfma_f32_16x16x128_f8f6f4 v[42:45], v[18:25], v[214:221], v[42:45]
	v_mfma_f32_16x16x128_f8f6f4 v[46:49], v[26:33], v[214:221], v[46:49]
	v_mfma_f32_16x16x128_f8f6f4 v[38:41], v[10:17], v[214:221], v[38:41]
	v_mfma_f32_16x16x128_f8f6f4 v[34:37], v[2:9], v[214:221], v[34:37]
	v_mfma_f32_16x16x128_f8f6f4 v[82:85], v[2:9], v[190:197], v[82:85]
	v_mfma_f32_16x16x128_f8f6f4 v[86:89], v[10:17], v[190:197], v[86:89]
	v_mfma_f32_16x16x128_f8f6f4 v[70:73], v[10:17], v[198:205], v[70:73]
	v_mfma_f32_16x16x128_f8f6f4 v[66:69], v[2:9], v[198:205], v[66:69]
	v_mfma_f32_16x16x128_f8f6f4 v[50:53], v[2:9], v[206:213], v[50:53]
	v_mfma_f32_16x16x128_f8f6f4 v[54:57], v[10:17], v[206:213], v[54:57]
	s_setprio 0
	s_barrier
	s_add_i32 s72, 0, 0x18000
	s_add_i32 s73, 0, 0x1c000
	v_add_u32_e32 v14, s72, v188
	v_add_u32_e32 v30, s73, v188
	ds_read_b128 v[2:5], v14
	ds_read_b128 v[6:9], v14 offset:1024
	ds_read_b128 v[10:13], v14 offset:2048
	ds_read_b128 v[14:17], v14 offset:3072
	ds_read_b128 v[18:21], v30
	ds_read_b128 v[22:25], v30 offset:1024
	ds_read_b128 v[26:29], v30 offset:2048
	ds_read_b128 v[30:33], v30 offset:3072
	s_add_u32 s36, s36, 0x158000
	s_addc_u32 s37, s37, 0
	s_mov_b32 m0, s66
	v_lshl_add_u64 v[222:223], s[36:37], 0, v[162:163]
	ds_read_b128 v[190:193], v189 offset:32768
	ds_read_b128 v[194:197], v189 offset:33792
	ds_read_b128 v[198:201], v189 offset:34816
	ds_read_b128 v[202:205], v189 offset:35840
	ds_read_b128 v[206:209], v189 offset:36864
	ds_read_b128 v[210:213], v189 offset:37888
	ds_read_b128 v[214:217], v189 offset:38912
	ds_read_b128 v[218:221], v189 offset:39936
	global_load_lds_dwordx4 v[222:223], off
	v_lshl_add_u64 v[222:223], s[36:37], 0, v[166:167]
	s_mov_b32 m0, s67
	s_nop 0
	global_load_lds_dwordx4 v[222:223], off
	s_waitcnt vmcnt(8) lgkmcnt(0)
	s_barrier
	s_setprio 1
	v_mfma_f32_16x16x128_f8f6f4 v[114:117], v[10:17], v[206:213], v[114:117]
	v_mfma_f32_16x16x128_f8f6f4 v[126:129], v[2:9], v[206:213], v[126:129]
	v_mfma_f32_16x16x128_f8f6f4 v[158:161], v[2:9], v[190:197], v[158:161]
	v_mfma_f32_16x16x128_f8f6f4 v[154:157], v[10:17], v[190:197], v[154:157]
	v_mfma_f32_16x16x128_f8f6f4 v[118:121], v[10:17], v[198:205], v[118:121]
	v_mfma_f32_16x16x128_f8f6f4 v[122:125], v[2:9], v[198:205], v[122:125]
	v_mfma_f32_16x16x128_f8f6f4 v[110:113], v[2:9], v[214:221], v[110:113]
	v_mfma_f32_16x16x128_f8f6f4 v[106:109], v[10:17], v[214:221], v[106:109]
	v_mfma_f32_16x16x128_f8f6f4 v[102:105], v[18:25], v[214:221], v[102:105]
	v_mfma_f32_16x16x128_f8f6f4 v[98:101], v[26:33], v[214:221], v[98:101]
	v_mfma_f32_16x16x128_f8f6f4 v[146:149], v[26:33], v[190:197], v[146:149]
	v_mfma_f32_16x16x128_f8f6f4 v[150:153], v[18:25], v[190:197], v[150:153]
	v_mfma_f32_16x16x128_f8f6f4 v[142:145], v[18:25], v[198:205], v[142:145]
	v_mfma_f32_16x16x128_f8f6f4 v[138:141], v[26:33], v[198:205], v[138:141]
	v_mfma_f32_16x16x128_f8f6f4 v[130:133], v[26:33], v[206:213], v[130:133]
	v_mfma_f32_16x16x128_f8f6f4 v[134:137], v[18:25], v[206:213], v[134:137]
	s_setprio 0
	s_barrier
	s_add_i32 s36, s72, s43
	v_lshl_add_u64 v[172:173], v[172:173], 0, s[22:23]
	s_mov_b32 m0, s36
	ds_read_b128 v[190:193], v189 offset:49152
	ds_read_b128 v[194:197], v189 offset:50176
	ds_read_b128 v[198:201], v189 offset:51200
	ds_read_b128 v[202:205], v189 offset:52224
	ds_read_b128 v[206:209], v189 offset:53248
	ds_read_b128 v[210:213], v189 offset:54272
	ds_read_b128 v[214:217], v189 offset:55296
	ds_read_b128 v[218:221], v189 offset:56320
	global_load_lds_dwordx4 v[172:173], off
	s_add_i32 m0, s36, 0x2000
	s_add_u32 s8, s8, 0x158080
	v_lshl_add_u64 v[172:173], v[174:175], 0, s[22:23]
	s_addc_u32 s9, s9, 0
	s_add_i32 s36, s73, s43
	global_load_lds_dwordx4 v[172:173], off
	v_lshl_add_u64 v[172:173], s[8:9], 0, v[162:163]
	s_mov_b32 m0, s36
	s_nop 0
	global_load_lds_dwordx4 v[172:173], off
	v_lshl_add_u64 v[172:173], s[8:9], 0, v[166:167]
	s_add_i32 m0, s36, 0x2000
	s_nop 0
	global_load_lds_dwordx4 v[172:173], off
	v_lshl_add_u64 v[172:173], v[176:177], 0, s[22:23]
	s_mov_b32 m0, s69
	s_nop 0
	global_load_lds_dwordx4 v[172:173], off
	v_lshl_add_u64 v[172:173], v[178:179], 0, s[22:23]
	s_mov_b32 m0, s70
	s_nop 0
	global_load_lds_dwordx4 v[172:173], off
	s_waitcnt vmcnt(8) lgkmcnt(0)
	s_barrier
	s_setprio 1
	v_mfma_f32_16x16x128_f8f6f4 v[62:65], v[2:9], v[206:213], v[62:65]
	v_mfma_f32_16x16x128_f8f6f4 v[58:61], v[10:17], v[206:213], v[58:61]
	v_mfma_f32_16x16x128_f8f6f4 v[90:93], v[10:17], v[190:197], v[90:93]
	v_mfma_f32_16x16x128_f8f6f4 v[94:97], v[2:9], v[190:197], v[94:97]
	v_mfma_f32_16x16x128_f8f6f4 v[78:81], v[2:9], v[198:205], v[78:81]
	v_mfma_f32_16x16x128_f8f6f4 v[74:77], v[10:17], v[198:205], v[74:77]
	v_mfma_f32_16x16x128_f8f6f4 v[42:45], v[10:17], v[214:221], v[42:45]
	v_mfma_f32_16x16x128_f8f6f4 v[46:49], v[2:9], v[214:221], v[46:49]
	v_mfma_f32_16x16x128_f8f6f4 v[38:41], v[18:25], v[214:221], v[38:41]
	v_mfma_f32_16x16x128_f8f6f4 v[34:37], v[26:33], v[214:221], v[34:37]
	v_mfma_f32_16x16x128_f8f6f4 v[82:85], v[26:33], v[190:197], v[82:85]
	v_mfma_f32_16x16x128_f8f6f4 v[86:89], v[18:25], v[190:197], v[86:89]
	v_mfma_f32_16x16x128_f8f6f4 v[70:73], v[18:25], v[198:205], v[70:73]
	v_mfma_f32_16x16x128_f8f6f4 v[66:69], v[26:33], v[198:205], v[66:69]
	v_mfma_f32_16x16x128_f8f6f4 v[50:53], v[26:33], v[206:213], v[50:53]
	v_mfma_f32_16x16x128_f8f6f4 v[54:57], v[18:25], v[206:213], v[54:57]
	s_setprio 0
	s_barrier
	s_add_i32 s71, s71, 2
	s_add_u32 s6, s6, 0x100
	s_addc_u32 s7, s7, 0
	s_cmpk_lt_u32 s71, 0x54
	s_cbranch_scc1 .LBB0_1745
	s_waitcnt vmcnt(0)
	s_cmpk_gt_u32 s40, 0xff
	s_cbranch_scc1 .LBB0_1748
	s_barrier

.LBB0_1807:
	ds_read_b128 v[26:29], v185
	ds_read_b128 v[30:33], v185 offset:1024
	ds_read_b128 v[18:21], v185 offset:2048
	ds_read_b128 v[22:25], v185 offset:3072
	ds_read_b128 v[10:13], v186
	ds_read_b128 v[14:17], v186 offset:1024
	ds_read_b128 v[2:5], v186 offset:2048
	ds_read_b128 v[6:9], v186 offset:3072
	s_add_u32 s28, s26, 0xffea8080
	s_addc_u32 s29, s27, -1
	s_cmpk_eq_i32 s58, 0x52
	s_cselect_b32 s31, s5, s29
	s_cselect_b32 s30, s4, s28
	s_cselect_b32 s29, s25, s57
	s_cselect_b32 s28, s24, s56
	v_lshl_add_u64 v[212:213], s[26:27], 0, v[166:167]
	s_add_i32 m0, s34, 0xc000
	ds_read_b128 v[174:177], v187
	ds_read_b128 v[178:181], v187 offset:1024
	ds_read_b128 v[188:191], v187 offset:2048
	ds_read_b128 v[192:195], v187 offset:3072
	ds_read_b128 v[196:199], v187 offset:4096
	ds_read_b128 v[200:203], v187 offset:5120
	ds_read_b128 v[204:207], v187 offset:6144
	ds_read_b128 v[208:211], v187 offset:7168
	global_load_lds_dwordx4 v[212:213], off
	v_lshl_add_u64 v[212:213], s[26:27], 0, v[168:169]
	s_add_i32 m0, s34, 0xe000
	s_nop 0
	global_load_lds_dwordx4 v[212:213], off
	s_waitcnt vmcnt(8) lgkmcnt(0)
	s_barrier
	s_setprio 1
	v_mfma_f32_16x16x128_f8f6f4 v[158:161], v[26:33], v[174:181], v[158:161]
	v_mfma_f32_16x16x128_f8f6f4 v[154:157], v[18:25], v[174:181], v[154:157]
	v_mfma_f32_16x16x128_f8f6f4 v[138:141], v[18:25], v[188:195], v[138:141]
	v_mfma_f32_16x16x128_f8f6f4 v[142:145], v[26:33], v[188:195], v[142:145]
	v_mfma_f32_16x16x128_f8f6f4 v[126:129], v[26:33], v[196:203], v[126:129]
	v_mfma_f32_16x16x128_f8f6f4 v[122:125], v[18:25], v[196:203], v[122:125]
	v_mfma_f32_16x16x128_f8f6f4 v[106:109], v[18:25], v[204:211], v[106:109]
	v_mfma_f32_16x16x128_f8f6f4 v[110:113], v[26:33], v[204:211], v[110:113]
	v_mfma_f32_16x16x128_f8f6f4 v[102:105], v[10:17], v[204:211], v[102:105]
	v_mfma_f32_16x16x128_f8f6f4 v[98:101], v[2:9], v[204:211], v[98:101]
	v_mfma_f32_16x16x128_f8f6f4 v[146:149], v[2:9], v[174:181], v[146:149]
	v_mfma_f32_16x16x128_f8f6f4 v[150:153], v[10:17], v[174:181], v[150:153]
	v_mfma_f32_16x16x128_f8f6f4 v[134:137], v[10:17], v[188:195], v[134:137]
	v_mfma_f32_16x16x128_f8f6f4 v[130:133], v[2:9], v[188:195], v[130:133]
	v_mfma_f32_16x16x128_f8f6f4 v[114:117], v[2:9], v[196:203], v[114:117]
	v_mfma_f32_16x16x128_f8f6f4 v[118:121], v[10:17], v[196:203], v[118:121]
	s_setprio 0
	s_barrier
	s_add_i32 s59, s42, s3
	v_lshl_add_u64 v[174:175], s[28:29], 0, v[164:165]
	s_mov_b32 m0, s59
	ds_read_b128 v[188:191], v187 offset:16384
	ds_read_b128 v[192:195], v187 offset:17408
	ds_read_b128 v[196:199], v187 offset:18432
	ds_read_b128 v[200:203], v187 offset:19456
	ds_read_b128 v[204:207], v187 offset:20480
	ds_read_b128 v[208:211], v187 offset:21504
	ds_read_b128 v[212:215], v187 offset:22528
	ds_read_b128 v[216:219], v187 offset:23552
	global_load_lds_dwordx4 v[174:175], off
	s_add_i32 m0, s59, 0x2000
	s_add_u32 s60, s28, 0x158000
	v_lshl_add_u64 v[176:177], s[28:29], 0, v[162:163]
	s_addc_u32 s61, s29, 0
	s_add_i32 s59, s43, s3
	global_load_lds_dwordx4 v[176:177], off
	v_lshl_add_u64 v[178:179], s[60:61], 0, v[164:165]
	s_mov_b32 m0, s59
	v_lshl_add_u64 v[180:181], s[30:31], 0, v[162:163]
	global_load_lds_dwordx4 v[178:179], off
	v_lshl_add_u64 v[178:179], s[60:61], 0, v[162:163]
	s_add_i32 m0, s59, 0x2000
	s_nop 0
	global_load_lds_dwordx4 v[178:179], off
	v_lshl_add_u64 v[178:179], s[30:31], 0, v[164:165]
	s_mov_b32 m0, s34
	s_nop 0
	global_load_lds_dwordx4 v[178:179], off
	s_mov_b32 m0, s35
	s_nop 0
	global_load_lds_dwordx4 v[180:181], off
	s_waitcnt vmcnt(8) lgkmcnt(0)
	s_barrier
	s_setprio 1
	v_mfma_f32_16x16x128_f8f6f4 v[78:81], v[26:33], v[196:203], v[78:81]
	v_mfma_f32_16x16x128_f8f6f4 v[74:77], v[18:25], v[196:203], v[74:77]
	v_mfma_f32_16x16x128_f8f6f4 v[90:93], v[18:25], v[188:195], v[90:93]
	v_mfma_f32_16x16x128_f8f6f4 v[94:97], v[26:33], v[188:195], v[94:97]
	v_mfma_f32_16x16x128_f8f6f4 v[62:65], v[26:33], v[204:211], v[62:65]
	v_mfma_f32_16x16x128_f8f6f4 v[58:61], v[18:25], v[204:211], v[58:61]
	v_mfma_f32_16x16x128_f8f6f4 v[42:45], v[18:25], v[212:219], v[42:45]
	v_mfma_f32_16x16x128_f8f6f4 v[54:57], v[26:33], v[212:219], v[54:57]
	v_mfma_f32_16x16x128_f8f6f4 v[38:41], v[10:17], v[212:219], v[38:41]
	v_mfma_f32_16x16x128_f8f6f4 v[34:37], v[2:9], v[212:219], v[34:37]
	v_mfma_f32_16x16x128_f8f6f4 v[82:85], v[2:9], v[188:195], v[82:85]
	v_mfma_f32_16x16x128_f8f6f4 v[86:89], v[10:17], v[188:195], v[86:89]
	v_mfma_f32_16x16x128_f8f6f4 v[70:73], v[10:17], v[196:203], v[70:73]
	v_mfma_f32_16x16x128_f8f6f4 v[66:69], v[2:9], v[196:203], v[66:69]
	v_mfma_f32_16x16x128_f8f6f4 v[46:49], v[2:9], v[204:211], v[46:49]
	v_mfma_f32_16x16x128_f8f6f4 v[50:53], v[10:17], v[204:211], v[50:53]
	s_setprio 0
	s_barrier
	s_add_i32 s59, 0, 0x18000
	s_add_i32 s60, 0, 0x1c000
	v_add_u32_e32 v14, s59, v183
	v_add_u32_e32 v30, s60, v183
	ds_read_b128 v[2:5], v14
	ds_read_b128 v[6:9], v14 offset:1024
	ds_read_b128 v[10:13], v14 offset:2048
	ds_read_b128 v[14:17], v14 offset:3072
	ds_read_b128 v[18:21], v30
	ds_read_b128 v[22:25], v30 offset:1024
	ds_read_b128 v[26:29], v30 offset:2048
	ds_read_b128 v[30:33], v30 offset:3072
	s_add_u32 s30, s30, 0x158000
	s_addc_u32 s31, s31, 0
	s_mov_b32 m0, s36
	v_lshl_add_u64 v[220:221], s[30:31], 0, v[164:165]
	ds_read_b128 v[188:191], v187 offset:32768
	ds_read_b128 v[192:195], v187 offset:33792
	ds_read_b128 v[196:199], v187 offset:34816
	ds_read_b128 v[200:203], v187 offset:35840
	ds_read_b128 v[204:207], v187 offset:36864
	ds_read_b128 v[208:211], v187 offset:37888
	ds_read_b128 v[212:215], v187 offset:38912
	ds_read_b128 v[216:219], v187 offset:39936
	global_load_lds_dwordx4 v[220:221], off
	v_lshl_add_u64 v[220:221], s[30:31], 0, v[162:163]
	s_mov_b32 m0, s37
	s_nop 0
	global_load_lds_dwordx4 v[220:221], off
	s_waitcnt vmcnt(8) lgkmcnt(0)
	s_barrier
	s_setprio 1
	v_mfma_f32_16x16x128_f8f6f4 v[122:125], v[10:17], v[204:211], v[122:125]
	v_mfma_f32_16x16x128_f8f6f4 v[126:129], v[2:9], v[204:211], v[126:129]
	v_mfma_f32_16x16x128_f8f6f4 v[158:161], v[2:9], v[188:195], v[158:161]
	v_mfma_f32_16x16x128_f8f6f4 v[154:157], v[10:17], v[188:195], v[154:157]
	v_mfma_f32_16x16x128_f8f6f4 v[138:141], v[10:17], v[196:203], v[138:141]
	v_mfma_f32_16x16x128_f8f6f4 v[142:145], v[2:9], v[196:203], v[142:145]
	v_mfma_f32_16x16x128_f8f6f4 v[110:113], v[2:9], v[212:219], v[110:113]
	v_mfma_f32_16x16x128_f8f6f4 v[106:109], v[10:17], v[212:219], v[106:109]
	v_mfma_f32_16x16x128_f8f6f4 v[102:105], v[18:25], v[212:219], v[102:105]
	v_mfma_f32_16x16x128_f8f6f4 v[98:101], v[26:33], v[212:219], v[98:101]
	v_mfma_f32_16x16x128_f8f6f4 v[146:149], v[26:33], v[188:195], v[146:149]
	v_mfma_f32_16x16x128_f8f6f4 v[150:153], v[18:25], v[188:195], v[150:153]
	v_mfma_f32_16x16x128_f8f6f4 v[134:137], v[18:25], v[196:203], v[134:137]
	v_mfma_f32_16x16x128_f8f6f4 v[130:133], v[26:33], v[196:203], v[130:133]
	v_mfma_f32_16x16x128_f8f6f4 v[114:117], v[26:33], v[204:211], v[114:117]
	v_mfma_f32_16x16x128_f8f6f4 v[118:121], v[18:25], v[204:211], v[118:121]
	s_setprio 0
	s_barrier
	s_add_i32 s30, s59, s3
	v_lshl_add_u64 v[174:175], v[174:175], 0, s[10:11]
	s_mov_b32 m0, s30
	ds_read_b128 v[188:191], v187 offset:49152
	ds_read_b128 v[192:195], v187 offset:50176
	ds_read_b128 v[196:199], v187 offset:51200
	ds_read_b128 v[200:203], v187 offset:52224
	ds_read_b128 v[204:207], v187 offset:53248
	ds_read_b128 v[208:211], v187 offset:54272
	ds_read_b128 v[212:215], v187 offset:55296
	ds_read_b128 v[216:219], v187 offset:56320
	global_load_lds_dwordx4 v[174:175], off
	s_add_i32 m0, s30, 0x2000
	s_add_u32 s28, s28, 0x158080
	v_lshl_add_u64 v[174:175], v[176:177], 0, s[10:11]
	s_addc_u32 s29, s29, 0
	s_add_i32 s30, s60, s3
	global_load_lds_dwordx4 v[174:175], off
	v_lshl_add_u64 v[174:175], s[28:29], 0, v[164:165]
	s_mov_b32 m0, s30
	s_nop 0
	global_load_lds_dwordx4 v[174:175], off
	v_lshl_add_u64 v[174:175], s[28:29], 0, v[162:163]
	s_add_i32 m0, s30, 0x2000
	s_nop 0
	global_load_lds_dwordx4 v[174:175], off
	v_lshl_add_u64 v[174:175], v[178:179], 0, s[10:11]
	s_mov_b32 m0, s40
	s_nop 0
	global_load_lds_dwordx4 v[174:175], off
	v_lshl_add_u64 v[174:175], v[180:181], 0, s[10:11]
	s_mov_b32 m0, s41
	s_nop 0
	global_load_lds_dwordx4 v[174:175], off
	s_waitcnt vmcnt(8) lgkmcnt(0)
	s_barrier
	s_setprio 1
	v_mfma_f32_16x16x128_f8f6f4 v[62:65], v[2:9], v[204:211], v[62:65]
	v_mfma_f32_16x16x128_f8f6f4 v[58:61], v[10:17], v[204:211], v[58:61]
	v_mfma_f32_16x16x128_f8f6f4 v[90:93], v[10:17], v[188:195], v[90:93]
	v_mfma_f32_16x16x128_f8f6f4 v[94:97], v[2:9], v[188:195], v[94:97]
	v_mfma_f32_16x16x128_f8f6f4 v[78:81], v[2:9], v[196:203], v[78:81]
	v_mfma_f32_16x16x128_f8f6f4 v[74:77], v[10:17], v[196:203], v[74:77]
	v_mfma_f32_16x16x128_f8f6f4 v[42:45], v[10:17], v[212:219], v[42:45]
	v_mfma_f32_16x16x128_f8f6f4 v[54:57], v[2:9], v[212:219], v[54:57]
	v_mfma_f32_16x16x128_f8f6f4 v[38:41], v[18:25], v[212:219], v[38:41]
	v_mfma_f32_16x16x128_f8f6f4 v[34:37], v[26:33], v[212:219], v[34:37]
	v_mfma_f32_16x16x128_f8f6f4 v[82:85], v[26:33], v[188:195], v[82:85]
	v_mfma_f32_16x16x128_f8f6f4 v[86:89], v[18:25], v[188:195], v[86:89]
	v_mfma_f32_16x16x128_f8f6f4 v[70:73], v[18:25], v[196:203], v[70:73]
	v_mfma_f32_16x16x128_f8f6f4 v[66:69], v[26:33], v[196:203], v[66:69]
	v_mfma_f32_16x16x128_f8f6f4 v[46:49], v[26:33], v[204:211], v[46:49]
	v_mfma_f32_16x16x128_f8f6f4 v[50:53], v[18:25], v[204:211], v[50:53]
	s_setprio 0
	s_barrier
	s_add_i32 s58, s58, 2
	s_add_u32 s26, s26, 0x100
	s_addc_u32 s27, s27, 0
	s_add_u32 s56, s56, 0x100
	s_addc_u32 s57, s57, 0
	s_cmpk_gt_u32 s58, 0x53
	s_cbranch_scc0 .LBB0_1807
	s_and_b64 vcc, exec, s[12:13]
	s_cbranch_vccz .LBB0_1810
	s_barrier
